# GQA K/V prefetch distance 2; router-logit GEMM loads pipelined 14 deep; NA window-bias LDS reads batched (one wait per tile); zprep loads batched
# speedup vs baseline: 1.0210x; 1.0210x over previous
; __device__ __forceinline__ void phase_na_attention(const Params& P, float* sm, int bid, int nb) {
;     ...
;             if (win) {
;                 const float* rp = sm + (head * 15 + (rs + ti - rr + 7)) * 31 - c + 15;
; #pragma unroll
;                 for (int kt = 0; kt < 2; ++kt)
; #pragma unroll
;                     for (int q = 0; q < 16; ++q) {
;                         const int kc = kt * 32 + (q & 3) + 8 * (q >> 2) + 4 * h;
;                         const bool in = (kc >= cs) && (kc < cs + 16);
;                         const float bias = rp[in ? kc : c];
;                         s[kt][q] = in ? s[kt][q] * SC + bias : -1e30f;
;                     }
.LBB0_502:
	s_andn2_saveexec_b64 s[0:1], s[0:1]
	s_cbranch_execz .LBB0_491
	v_mov_b32_e32 v35, 0xf149f2ca
	v_mov_b32_e32 v34, 0xf149f2ca
	v_mov_b32_e32 v37, 0xf149f2ca
	v_mov_b32_e32 v36, 0xf149f2ca
	v_mov_b32_e32 v39, 0xf149f2ca
	v_mov_b32_e32 v38, 0xf149f2ca
	v_mov_b32_e32 v41, 0xf149f2ca
	v_mov_b32_e32 v40, 0xf149f2ca
	v_mov_b32_e32 v43, 0xf149f2ca
	v_mov_b32_e32 v42, 0xf149f2ca
	v_mov_b32_e32 v45, 0xf149f2ca
	v_mov_b32_e32 v44, 0xf149f2ca
	v_mov_b32_e32 v47, 0xf149f2ca
	v_mov_b32_e32 v46, 0xf149f2ca
	v_mov_b32_e32 v49, 0xf149f2ca
	v_mov_b32_e32 v48, 0xf149f2ca
	v_mov_b32_e32 v51, 0xf149f2ca
	v_mov_b32_e32 v50, 0xf149f2ca
	v_mov_b32_e32 v53, 0xf149f2ca
	v_mov_b32_e32 v52, 0xf149f2ca
	v_mov_b32_e32 v55, 0xf149f2ca
	v_mov_b32_e32 v54, 0xf149f2ca
	v_mov_b32_e32 v57, 0xf149f2ca
	v_mov_b32_e32 v56, 0xf149f2ca
	v_mov_b32_e32 v59, 0xf149f2ca
	v_mov_b32_e32 v58, 0xf149f2ca
	v_mov_b32_e32 v61, 0xf149f2ca
	v_mov_b32_e32 v60, 0xf149f2ca
	v_mov_b32_e32 v63, 0xf149f2ca
	v_mov_b32_e32 v62, 0xf149f2ca
	v_mov_b32_e32 v65, 0xf149f2ca
	v_mov_b32_e32 v64, 0xf149f2ca
	s_mov_b64 s[98:99], exec
	s_and_b64 exec, s[98:99], s[36:37]
	ds_read_b32 v34, v249
	s_and_b64 exec, s[98:99], s[34:35]
	ds_read_b32 v35, v249 offset:4
	s_and_b64 exec, s[98:99], s[30:31]
	ds_read_b32 v36, v249 offset:8
	s_and_b64 exec, s[98:99], s[28:29]
	ds_read_b32 v37, v249 offset:12
	s_and_b64 exec, s[98:99], s[26:27]
	ds_read_b32 v38, v249 offset:32
	s_and_b64 exec, s[98:99], s[24:25]
	ds_read_b32 v39, v249 offset:36
	s_and_b64 exec, s[98:99], s[22:23]
	ds_read_b32 v40, v249 offset:40
	s_and_b64 exec, s[98:99], s[20:21]
	ds_read_b32 v41, v249 offset:44
	s_and_b64 exec, s[98:99], s[46:47]
	ds_read_b32 v42, v249 offset:64
	s_and_b64 exec, s[98:99], s[2:3]
	ds_read_b32 v43, v249 offset:68
	s_and_b64 exec, s[98:99], s[96:97]
	ds_read_b32 v44, v249 offset:72
	s_and_b64 exec, s[98:99], s[50:51]
	ds_read_b32 v45, v249 offset:76
	s_and_b64 exec, s[98:99], s[90:91]
	ds_read_b32 v46, v249 offset:96
	s_and_b64 exec, s[98:99], s[88:89]
	ds_read_b32 v47, v249 offset:100
	s_and_b64 exec, s[98:99], s[86:87]
	ds_read_b32 v48, v249 offset:104
	s_and_b64 exec, s[98:99], s[84:85]
	ds_read_b32 v49, v249 offset:108
	s_and_b64 exec, s[98:99], s[40:41]
	ds_read_b32 v50, v249 offset:128
	s_and_b64 exec, s[98:99], s[4:5]
	ds_read_b32 v51, v249 offset:132
	s_and_b64 exec, s[98:99], s[76:77]
	ds_read_b32 v52, v249 offset:136
	s_and_b64 exec, s[98:99], s[72:73]
	ds_read_b32 v53, v249 offset:140
	s_and_b64 exec, s[98:99], s[68:69]
	ds_read_b32 v54, v249 offset:160
	s_and_b64 exec, s[98:99], s[66:67]
	ds_read_b32 v55, v249 offset:164
	s_and_b64 exec, s[98:99], s[64:65]
	ds_read_b32 v56, v249 offset:168
	s_and_b64 exec, s[98:99], s[62:63]
	ds_read_b32 v57, v249 offset:172
	s_and_b64 exec, s[98:99], s[18:19]
	ds_read_b32 v58, v249 offset:192
	s_and_b64 exec, s[98:99], s[16:17]
	ds_read_b32 v59, v249 offset:196
	s_and_b64 exec, s[98:99], s[14:15]
	ds_read_b32 v60, v249 offset:200
	s_and_b64 exec, s[98:99], s[12:13]
	ds_read_b32 v61, v249 offset:204
	s_and_b64 exec, s[98:99], s[10:11]
	ds_read_b32 v62, v249 offset:224
	s_and_b64 exec, s[98:99], s[8:9]
	ds_read_b32 v63, v249 offset:228
	s_and_b64 exec, s[98:99], s[6:7]
	ds_read_b32 v64, v249 offset:232
	s_and_b64 exec, s[98:99], vcc
	ds_read_b32 v65, v249 offset:236
	s_mov_b64 exec, s[98:99]
	s_waitcnt lgkmcnt(0)
	v_fmac_f32_e32 v34, 0x3e38aa3b, v82
	v_fmac_f32_e32 v35, 0x3e38aa3b, v83
	v_fmac_f32_e32 v36, 0x3e38aa3b, v84
	v_fmac_f32_e32 v37, 0x3e38aa3b, v85
	v_fmac_f32_e32 v38, 0x3e38aa3b, v86
	v_fmac_f32_e32 v39, 0x3e38aa3b, v87
	v_fmac_f32_e32 v40, 0x3e38aa3b, v88
	v_fmac_f32_e32 v41, 0x3e38aa3b, v89
	v_fmac_f32_e32 v42, 0x3e38aa3b, v90
	v_fmac_f32_e32 v43, 0x3e38aa3b, v91
	v_fmac_f32_e32 v44, 0x3e38aa3b, v92
	v_fmac_f32_e32 v45, 0x3e38aa3b, v93
	v_fmac_f32_e32 v46, 0x3e38aa3b, v94
	v_fmac_f32_e32 v47, 0x3e38aa3b, v95
	v_fmac_f32_e32 v48, 0x3e38aa3b, v96
	v_fmac_f32_e32 v49, 0x3e38aa3b, v97
	v_fmac_f32_e32 v50, 0x3e38aa3b, v66
	v_fmac_f32_e32 v51, 0x3e38aa3b, v67
	v_fmac_f32_e32 v52, 0x3e38aa3b, v68
	v_fmac_f32_e32 v53, 0x3e38aa3b, v69
	v_fmac_f32_e32 v54, 0x3e38aa3b, v70
	v_fmac_f32_e32 v55, 0x3e38aa3b, v71
	v_fmac_f32_e32 v56, 0x3e38aa3b, v72
	v_fmac_f32_e32 v57, 0x3e38aa3b, v73
	v_fmac_f32_e32 v58, 0x3e38aa3b, v74
	v_fmac_f32_e32 v59, 0x3e38aa3b, v75
	v_fmac_f32_e32 v60, 0x3e38aa3b, v76
	v_fmac_f32_e32 v61, 0x3e38aa3b, v77
	v_fmac_f32_e32 v62, 0x3e38aa3b, v78
	v_fmac_f32_e32 v63, 0x3e38aa3b, v79
	v_fmac_f32_e32 v64, 0x3e38aa3b, v80
	v_fmac_f32_e32 v65, 0x3e38aa3b, v81
	s_mov_b64 s[74:75], exec
	s_branch .LBB0_490

; __device__ __forceinline__ void phase_na_attention(const Params& P, float* sm, int bid, int nb) {
;     ...
;             if (win) {
;                 const float* rp = sm + (head * 15 + (rs + ti - rr + 7)) * 31 - c + 15;
; #pragma unroll
;                 for (int kt = 0; kt < 2; ++kt)
; #pragma unroll
;                     for (int q = 0; q < 16; ++q) {
;                         const int kc = kt * 32 + (q & 3) + 8 * (q >> 2) + 4 * h;
;                         const bool in = (kc >= cs) && (kc < cs + 16);
;                         const float bias = rp[in ? kc : c];
;                         s[kt][q] = in ? s[kt][q] * SC + bias : -1e30f;
;                     }
.LBB0_573:
	s_andn2_saveexec_b64 s[0:1], s[0:1]
	s_cbranch_execz .LBB0_488
	v_sub_u32_e32 v34, v245, v242
	v_add3_u32 v34, v34, v244, v208
	v_lshlrev_b32_e32 v35, 2, v243
	s_movk_i32 s33, 0x7c
	v_sub_u32_e32 v35, 0, v35
	v_mul_lo_u32 v34, v34, s33
	s_movk_i32 s33, 0x554
	v_add3_u32 v34, v34, v35, s33
	v_mov_b32_e32 v35, 0xf149f2ca
	v_lshl_add_u32 v98, v186, 2, v34
	v_mov_b32_e32 v34, 0xf149f2ca
	v_mov_b32_e32 v37, 0xf149f2ca
	v_mov_b32_e32 v36, 0xf149f2ca
	v_mov_b32_e32 v39, 0xf149f2ca
	v_mov_b32_e32 v38, 0xf149f2ca
	v_mov_b32_e32 v41, 0xf149f2ca
	v_mov_b32_e32 v40, 0xf149f2ca
	v_mov_b32_e32 v43, 0xf149f2ca
	v_mov_b32_e32 v42, 0xf149f2ca
	v_mov_b32_e32 v45, 0xf149f2ca
	v_mov_b32_e32 v44, 0xf149f2ca
	v_mov_b32_e32 v47, 0xf149f2ca
	v_mov_b32_e32 v46, 0xf149f2ca
	v_mov_b32_e32 v49, 0xf149f2ca
	v_mov_b32_e32 v48, 0xf149f2ca
	v_mov_b32_e32 v51, 0xf149f2ca
	v_mov_b32_e32 v50, 0xf149f2ca
	v_mov_b32_e32 v53, 0xf149f2ca
	v_mov_b32_e32 v52, 0xf149f2ca
	v_mov_b32_e32 v55, 0xf149f2ca
	v_mov_b32_e32 v54, 0xf149f2ca
	v_mov_b32_e32 v57, 0xf149f2ca
	v_mov_b32_e32 v56, 0xf149f2ca
	v_mov_b32_e32 v59, 0xf149f2ca
	v_mov_b32_e32 v58, 0xf149f2ca
	v_mov_b32_e32 v61, 0xf149f2ca
	v_mov_b32_e32 v60, 0xf149f2ca
	v_mov_b32_e32 v63, 0xf149f2ca
	v_mov_b32_e32 v62, 0xf149f2ca
	v_mov_b32_e32 v65, 0xf149f2ca
	v_mov_b32_e32 v64, 0xf149f2ca
	s_mov_b64 s[98:99], exec
	s_and_b64 exec, s[98:99], s[36:37]
	ds_read_b32 v34, v98 offset:76
	s_and_b64 exec, s[98:99], s[34:35]
	ds_read_b32 v35, v98 offset:80
	s_and_b64 exec, s[98:99], s[30:31]
	ds_read_b32 v36, v98 offset:84
	s_and_b64 exec, s[98:99], s[28:29]
	ds_read_b32 v37, v98 offset:88
	s_and_b64 exec, s[98:99], s[26:27]
	ds_read_b32 v38, v98 offset:108
	s_and_b64 exec, s[98:99], s[24:25]
	ds_read_b32 v39, v98 offset:112
	s_and_b64 exec, s[98:99], s[22:23]
	ds_read_b32 v40, v98 offset:116
	s_and_b64 exec, s[98:99], s[20:21]
	ds_read_b32 v41, v98 offset:120
	s_and_b64 exec, s[98:99], s[46:47]
	ds_read_b32 v42, v98 offset:140
	s_and_b64 exec, s[98:99], s[2:3]
	ds_read_b32 v43, v98 offset:144
	s_and_b64 exec, s[98:99], s[96:97]
	ds_read_b32 v44, v98 offset:148
	s_and_b64 exec, s[98:99], s[50:51]
	ds_read_b32 v45, v98 offset:152
	s_and_b64 exec, s[98:99], s[90:91]
	ds_read_b32 v46, v98 offset:172
	s_and_b64 exec, s[98:99], s[88:89]
	ds_read_b32 v47, v98 offset:176
	s_and_b64 exec, s[98:99], s[86:87]
	ds_read_b32 v48, v98 offset:180
	s_and_b64 exec, s[98:99], s[84:85]
	ds_read_b32 v49, v98 offset:184
	s_and_b64 exec, s[98:99], s[40:41]
	ds_read_b32 v50, v98 offset:204
	s_and_b64 exec, s[98:99], s[4:5]
	ds_read_b32 v51, v98 offset:208
	s_and_b64 exec, s[98:99], s[76:77]
	ds_read_b32 v52, v98 offset:212
	s_and_b64 exec, s[98:99], s[72:73]
	ds_read_b32 v53, v98 offset:216
	s_and_b64 exec, s[98:99], s[68:69]
	ds_read_b32 v54, v98 offset:236
	s_and_b64 exec, s[98:99], s[66:67]
	ds_read_b32 v55, v98 offset:240
	s_and_b64 exec, s[98:99], s[64:65]
	ds_read_b32 v56, v98 offset:244
	s_and_b64 exec, s[98:99], s[62:63]
	ds_read_b32 v57, v98 offset:248
	s_and_b64 exec, s[98:99], s[18:19]
	ds_read_b32 v58, v98 offset:268
	s_and_b64 exec, s[98:99], s[16:17]
	ds_read_b32 v59, v98 offset:272
	s_and_b64 exec, s[98:99], s[14:15]
	ds_read_b32 v60, v98 offset:276
	s_and_b64 exec, s[98:99], s[12:13]
	ds_read_b32 v61, v98 offset:280
	s_and_b64 exec, s[98:99], s[10:11]
	ds_read_b32 v62, v98 offset:300
	s_and_b64 exec, s[98:99], s[8:9]
	ds_read_b32 v63, v98 offset:304
	s_and_b64 exec, s[98:99], s[6:7]
	ds_read_b32 v64, v98 offset:308
	s_and_b64 exec, s[98:99], vcc
	ds_read_b32 v65, v98 offset:312
	s_mov_b64 exec, s[98:99]
	s_waitcnt lgkmcnt(0)
	v_fmac_f32_e32 v34, 0x3e38aa3b, v82
	v_fmac_f32_e32 v35, 0x3e38aa3b, v83
	v_fmac_f32_e32 v36, 0x3e38aa3b, v84
	v_fmac_f32_e32 v37, 0x3e38aa3b, v85
	v_fmac_f32_e32 v38, 0x3e38aa3b, v86
	v_fmac_f32_e32 v39, 0x3e38aa3b, v87
	v_fmac_f32_e32 v40, 0x3e38aa3b, v88
	v_fmac_f32_e32 v41, 0x3e38aa3b, v89
	v_fmac_f32_e32 v42, 0x3e38aa3b, v90
	v_fmac_f32_e32 v43, 0x3e38aa3b, v91
	v_fmac_f32_e32 v44, 0x3e38aa3b, v92
	v_fmac_f32_e32 v45, 0x3e38aa3b, v93
	v_fmac_f32_e32 v46, 0x3e38aa3b, v94
	v_fmac_f32_e32 v47, 0x3e38aa3b, v95
	v_fmac_f32_e32 v48, 0x3e38aa3b, v96
	v_fmac_f32_e32 v49, 0x3e38aa3b, v97
	v_fmac_f32_e32 v50, 0x3e38aa3b, v66
	v_fmac_f32_e32 v51, 0x3e38aa3b, v67
	v_fmac_f32_e32 v52, 0x3e38aa3b, v68
	v_fmac_f32_e32 v53, 0x3e38aa3b, v69
	v_fmac_f32_e32 v54, 0x3e38aa3b, v70
	v_fmac_f32_e32 v55, 0x3e38aa3b, v71
	v_fmac_f32_e32 v56, 0x3e38aa3b, v72
	v_fmac_f32_e32 v57, 0x3e38aa3b, v73
	v_fmac_f32_e32 v58, 0x3e38aa3b, v74
	v_fmac_f32_e32 v59, 0x3e38aa3b, v75
	v_fmac_f32_e32 v60, 0x3e38aa3b, v76
	v_fmac_f32_e32 v61, 0x3e38aa3b, v77
	v_fmac_f32_e32 v62, 0x3e38aa3b, v78
	v_fmac_f32_e32 v63, 0x3e38aa3b, v79
	v_fmac_f32_e32 v64, 0x3e38aa3b, v80
	v_fmac_f32_e32 v65, 0x3e38aa3b, v81
	s_mov_b64 s[2:3], exec
	s_branch .LBB0_487

; __device__ __forceinline__ float bf2f(bfr h) { return __uint_as_float(((unsigned)h) << 16); }
; __device__ __forceinline__ void phase_zprep(const Params& P, float* sm, int bid, int nb) {
;     ...
;     for (int u = bid; u < NT / 32; u += nb) {
;         const int r0 = u * 32;
;         const int seg0 = r0 < NCTX ? 0 : NCTX, seg1 = r0 < NCTX ? NCTX : NT;
;         const bfr* up = QK + (size_t)r0 * 3072 + 1536 + tid;
;         float pv[3], cv[3];
; #pragma unroll
;         for (int g = 0; g < 3; ++g) { pv[g] = (r0 - 1 >= seg0) ? bf2f(up[g * 512 - 3072]) : 0.f; cv[g] = bf2f(up[g * 512]); }
;         __syncthreads();
; #pragma unroll 8
;         for (int tt = 0; tt < 32; ++tt) {
;             float nv[3], y[3];
; #pragma unroll
;             for (int g = 0; g < 3; ++g) {
;                 nv[g] = (r0 + tt + 1 < seg1) ? bf2f(up[(size_t)(tt + 1) * 3072 + g * 512]) : 0.f;
;                 y[g] = bs[g] + pv[g] * w0[g] + cv[g] * w1[g] + nv[g] * w2[g];
.LBB0_641:
	s_lshl_b32 s24, s23, 5
	s_cmp_lt_i32 s23, 8
	s_cselect_b32 s7, 0, 0x100
	s_cselect_b32 s26, s21, s20
	s_ashr_i32 s25, s24, 31
	s_mul_i32 s0, s23, 0x30000
	s_mul_hi_i32 s1, s24, 0x1800
	s_add_u32 s0, s42, s0
	s_addc_u32 s1, s43, s1
	s_add_u32 s0, s0, 0x7077400
	s_addc_u32 s1, s1, 0
	s_cmp_gt_i32 s24, s7
	s_cbranch_scc0 .Lzp_noprev
	global_load_ushort v80, v10, s[0:1]
	global_load_ushort v81, v10, s[0:1] offset:1024
	global_load_ushort v82, v10, s[0:1] offset:2048
	s_branch .Lzp_rows
.Lzp_noprev:
	v_mov_b32_e32 v80, 0
	v_mov_b32_e32 v81, 0
	v_mov_b32_e32 v82, 0
.Lzp_rows:
	s_add_u32 s0, s0, 0x1800
	s_addc_u32 s1, s1, 0
	global_load_ushort v83, v10, s[0:1]
	global_load_ushort v84, v10, s[0:1] offset:1024
	global_load_ushort v85, v10, s[0:1] offset:2048
	s_add_u32 s0, s0, 0x1800
	s_addc_u32 s1, s1, 0
	global_load_ushort v86, v10, s[0:1]
	global_load_ushort v87, v10, s[0:1] offset:1024
	global_load_ushort v88, v10, s[0:1] offset:2048
	s_add_u32 s0, s0, 0x1800
	s_addc_u32 s1, s1, 0
	global_load_ushort v89, v10, s[0:1]
	global_load_ushort v90, v10, s[0:1] offset:1024
	global_load_ushort v91, v10, s[0:1] offset:2048
	s_add_u32 s0, s0, 0x1800
	s_addc_u32 s1, s1, 0
	global_load_ushort v92, v10, s[0:1]
	global_load_ushort v93, v10, s[0:1] offset:1024
	global_load_ushort v94, v10, s[0:1] offset:2048
	s_add_u32 s0, s0, 0x1800
	s_addc_u32 s1, s1, 0
	global_load_ushort v95, v10, s[0:1]
	global_load_ushort v96, v10, s[0:1] offset:1024
	global_load_ushort v97, v10, s[0:1] offset:2048
	s_add_u32 s0, s0, 0x1800
	s_addc_u32 s1, s1, 0
	global_load_ushort v98, v10, s[0:1]
	global_load_ushort v99, v10, s[0:1] offset:1024
	global_load_ushort v100, v10, s[0:1] offset:2048
	s_add_u32 s0, s0, 0x1800
	s_addc_u32 s1, s1, 0
	global_load_ushort v101, v10, s[0:1]
	global_load_ushort v102, v10, s[0:1] offset:1024
	global_load_ushort v103, v10, s[0:1] offset:2048
	s_add_u32 s0, s0, 0x1800
	s_addc_u32 s1, s1, 0
	global_load_ushort v104, v10, s[0:1]
	global_load_ushort v105, v10, s[0:1] offset:1024
	global_load_ushort v106, v10, s[0:1] offset:2048
	s_add_u32 s0, s0, 0x1800
	s_addc_u32 s1, s1, 0
	global_load_ushort v107, v10, s[0:1]
	global_load_ushort v108, v10, s[0:1] offset:1024
	global_load_ushort v109, v10, s[0:1] offset:2048
	s_add_u32 s0, s0, 0x1800
	s_addc_u32 s1, s1, 0
	global_load_ushort v110, v10, s[0:1]
	global_load_ushort v111, v10, s[0:1] offset:1024
	global_load_ushort v112, v10, s[0:1] offset:2048
	s_add_u32 s0, s0, 0x1800
	s_addc_u32 s1, s1, 0
	global_load_ushort v113, v10, s[0:1]
	global_load_ushort v114, v10, s[0:1] offset:1024
	global_load_ushort v115, v10, s[0:1] offset:2048
	s_add_u32 s0, s0, 0x1800
	s_addc_u32 s1, s1, 0
	global_load_ushort v116, v10, s[0:1]
	global_load_ushort v117, v10, s[0:1] offset:1024
	global_load_ushort v118, v10, s[0:1] offset:2048
	s_add_u32 s0, s0, 0x1800
	s_addc_u32 s1, s1, 0
	global_load_ushort v119, v10, s[0:1]
	global_load_ushort v120, v10, s[0:1] offset:1024
	global_load_ushort v121, v10, s[0:1] offset:2048
	s_add_u32 s0, s0, 0x1800
	s_addc_u32 s1, s1, 0
	global_load_ushort v122, v10, s[0:1]
	global_load_ushort v123, v10, s[0:1] offset:1024
	global_load_ushort v124, v10, s[0:1] offset:2048
	s_add_u32 s0, s0, 0x1800
	s_addc_u32 s1, s1, 0
	global_load_ushort v125, v10, s[0:1]
	global_load_ushort v126, v10, s[0:1] offset:1024
	global_load_ushort v127, v10, s[0:1] offset:2048
	s_add_u32 s0, s0, 0x1800
	s_addc_u32 s1, s1, 0
	global_load_ushort v128, v10, s[0:1]
	global_load_ushort v129, v10, s[0:1] offset:1024
	global_load_ushort v130, v10, s[0:1] offset:2048
	s_add_u32 s0, s0, 0x1800
	s_addc_u32 s1, s1, 0
	global_load_ushort v131, v10, s[0:1]
	global_load_ushort v132, v10, s[0:1] offset:1024
	global_load_ushort v133, v10, s[0:1] offset:2048
	s_add_u32 s0, s0, 0x1800
	s_addc_u32 s1, s1, 0
	global_load_ushort v134, v10, s[0:1]
	global_load_ushort v135, v10, s[0:1] offset:1024
	global_load_ushort v136, v10, s[0:1] offset:2048
	s_add_u32 s0, s0, 0x1800
	s_addc_u32 s1, s1, 0
	global_load_ushort v137, v10, s[0:1]
	global_load_ushort v138, v10, s[0:1] offset:1024
	global_load_ushort v139, v10, s[0:1] offset:2048
	s_add_u32 s0, s0, 0x1800
	s_addc_u32 s1, s1, 0
	global_load_ushort v140, v10, s[0:1]
	global_load_ushort v141, v10, s[0:1] offset:1024
	global_load_ushort v142, v10, s[0:1] offset:2048
	s_add_u32 s0, s0, 0x1800
	s_addc_u32 s1, s1, 0
	global_load_ushort v143, v10, s[0:1]
	global_load_ushort v144, v10, s[0:1] offset:1024
	global_load_ushort v145, v10, s[0:1] offset:2048
	s_add_u32 s0, s0, 0x1800
	s_addc_u32 s1, s1, 0
	global_load_ushort v146, v10, s[0:1]
	global_load_ushort v147, v10, s[0:1] offset:1024
	global_load_ushort v148, v10, s[0:1] offset:2048
	s_add_u32 s0, s0, 0x1800
	s_addc_u32 s1, s1, 0
	global_load_ushort v149, v10, s[0:1]
	global_load_ushort v150, v10, s[0:1] offset:1024
	global_load_ushort v151, v10, s[0:1] offset:2048
	s_add_u32 s0, s0, 0x1800
	s_addc_u32 s1, s1, 0
	global_load_ushort v152, v10, s[0:1]
	global_load_ushort v153, v10, s[0:1] offset:1024
	global_load_ushort v154, v10, s[0:1] offset:2048
	s_add_u32 s0, s0, 0x1800
	s_addc_u32 s1, s1, 0
	global_load_ushort v155, v10, s[0:1]
	global_load_ushort v156, v10, s[0:1] offset:1024
	global_load_ushort v157, v10, s[0:1] offset:2048
	s_add_u32 s0, s0, 0x1800
	s_addc_u32 s1, s1, 0
	global_load_ushort v158, v10, s[0:1]
	global_load_ushort v159, v10, s[0:1] offset:1024
	global_load_ushort v160, v10, s[0:1] offset:2048
	s_add_u32 s0, s0, 0x1800
	s_addc_u32 s1, s1, 0
	global_load_ushort v161, v10, s[0:1]
	global_load_ushort v162, v10, s[0:1] offset:1024
	global_load_ushort v163, v10, s[0:1] offset:2048
	s_add_u32 s0, s0, 0x1800
	s_addc_u32 s1, s1, 0
	global_load_ushort v164, v10, s[0:1]
	global_load_ushort v165, v10, s[0:1] offset:1024
	global_load_ushort v166, v10, s[0:1] offset:2048
	s_add_u32 s0, s0, 0x1800
	s_addc_u32 s1, s1, 0
	global_load_ushort v167, v10, s[0:1]
	global_load_ushort v168, v10, s[0:1] offset:1024
	global_load_ushort v169, v10, s[0:1] offset:2048
	s_add_u32 s0, s0, 0x1800
	s_addc_u32 s1, s1, 0
	global_load_ushort v170, v10, s[0:1]
	global_load_ushort v171, v10, s[0:1] offset:1024
	global_load_ushort v172, v10, s[0:1] offset:2048
	s_add_u32 s0, s0, 0x1800
	s_addc_u32 s1, s1, 0
	global_load_ushort v173, v10, s[0:1]
	global_load_ushort v174, v10, s[0:1] offset:1024
	global_load_ushort v175, v10, s[0:1] offset:2048
	s_add_u32 s0, s0, 0x1800
	s_addc_u32 s1, s1, 0
	global_load_ushort v176, v10, s[0:1]
	global_load_ushort v177, v10, s[0:1] offset:1024
	global_load_ushort v184, v10, s[0:1] offset:2048
	s_add_i32 s27, s24, 32
	s_cmp_lt_i32 s27, s26
	s_cbranch_scc0 .Lzp_nonext
	s_add_u32 s0, s0, 0x1800
	s_addc_u32 s1, s1, 0
	global_load_ushort v185, v10, s[0:1]
	global_load_ushort v186, v10, s[0:1] offset:1024
	global_load_ushort v187, v10, s[0:1] offset:2048
	s_branch .Lzp_loaded
; __device__ __forceinline__ float bf2f(bfr h) { return __uint_as_float(((unsigned)h) << 16); }
; __device__ __forceinline__ void phase_zprep(const Params& P, float* sm, int bid, int nb) {
;     ...
;         for (int tt = 0; tt < 32; ++tt) {
;             float nv[3], y[3];
; #pragma unroll
;             for (int g = 0; g < 3; ++g) {
;                 nv[g] = (r0 + tt + 1 < seg1) ? bf2f(up[(size_t)(tt + 1) * 3072 + g * 512]) : 0.f;
;                 y[g] = bs[g] + pv[g] * w0[g] + cv[g] * w1[g] + nv[g] * w2[g];
;                 pv[g] = cv[g]; cv[g] = nv[g];
;             }
;             sz[tid * 33 + tt] = y[1] * y[2];
;             sx[tid * 33 + tt] = y[0];
;         }
.Lzp_nonext:
	v_mov_b32_e32 v185, 0
	v_mov_b32_e32 v186, 0
	v_mov_b32_e32 v187, 0
.Lzp_loaded:
	s_ashr_i32 s7, s6, 31
	v_add_u32_e32 v9, 0xfffef800, v32
	s_barrier
	s_waitcnt vmcnt(0)
	v_lshlrev_b32_e32 v80, 16, v80
	v_lshlrev_b32_e32 v81, 16, v81
	v_lshlrev_b32_e32 v82, 16, v82
	v_lshlrev_b32_e32 v83, 16, v83
	v_lshlrev_b32_e32 v84, 16, v84
	v_lshlrev_b32_e32 v85, 16, v85
	v_lshlrev_b32_e32 v86, 16, v86
	v_lshlrev_b32_e32 v87, 16, v87
	v_lshlrev_b32_e32 v88, 16, v88
	v_lshlrev_b32_e32 v89, 16, v89
	v_lshlrev_b32_e32 v90, 16, v90
	v_lshlrev_b32_e32 v91, 16, v91
	v_lshlrev_b32_e32 v92, 16, v92
	v_lshlrev_b32_e32 v93, 16, v93
	v_lshlrev_b32_e32 v94, 16, v94
	v_lshlrev_b32_e32 v95, 16, v95
	v_lshlrev_b32_e32 v96, 16, v96
	v_lshlrev_b32_e32 v97, 16, v97
	v_lshlrev_b32_e32 v98, 16, v98
	v_lshlrev_b32_e32 v99, 16, v99
	v_lshlrev_b32_e32 v100, 16, v100
	v_lshlrev_b32_e32 v101, 16, v101
	v_lshlrev_b32_e32 v102, 16, v102
	v_lshlrev_b32_e32 v103, 16, v103
	v_lshlrev_b32_e32 v104, 16, v104
	v_lshlrev_b32_e32 v105, 16, v105
	v_lshlrev_b32_e32 v106, 16, v106
	v_lshlrev_b32_e32 v107, 16, v107
	v_lshlrev_b32_e32 v108, 16, v108
	v_lshlrev_b32_e32 v109, 16, v109
	v_lshlrev_b32_e32 v110, 16, v110
	v_lshlrev_b32_e32 v111, 16, v111
	v_lshlrev_b32_e32 v112, 16, v112
	v_lshlrev_b32_e32 v113, 16, v113
	v_lshlrev_b32_e32 v114, 16, v114
	v_lshlrev_b32_e32 v115, 16, v115
	v_lshlrev_b32_e32 v116, 16, v116
	v_lshlrev_b32_e32 v117, 16, v117
	v_lshlrev_b32_e32 v118, 16, v118
	v_lshlrev_b32_e32 v119, 16, v119
	v_lshlrev_b32_e32 v120, 16, v120
	v_lshlrev_b32_e32 v121, 16, v121
	v_lshlrev_b32_e32 v122, 16, v122
	v_lshlrev_b32_e32 v123, 16, v123
	v_lshlrev_b32_e32 v124, 16, v124
	v_lshlrev_b32_e32 v125, 16, v125
	v_lshlrev_b32_e32 v126, 16, v126
	v_lshlrev_b32_e32 v127, 16, v127
	v_lshlrev_b32_e32 v128, 16, v128
	v_lshlrev_b32_e32 v129, 16, v129
	v_lshlrev_b32_e32 v130, 16, v130
	v_lshlrev_b32_e32 v131, 16, v131
	v_lshlrev_b32_e32 v132, 16, v132
	v_lshlrev_b32_e32 v133, 16, v133
	v_lshlrev_b32_e32 v134, 16, v134
	v_lshlrev_b32_e32 v135, 16, v135
	v_lshlrev_b32_e32 v136, 16, v136
	v_lshlrev_b32_e32 v137, 16, v137
	v_lshlrev_b32_e32 v138, 16, v138
	v_lshlrev_b32_e32 v139, 16, v139
	v_lshlrev_b32_e32 v140, 16, v140
	v_lshlrev_b32_e32 v141, 16, v141
	v_lshlrev_b32_e32 v142, 16, v142
	v_lshlrev_b32_e32 v143, 16, v143
	v_lshlrev_b32_e32 v144, 16, v144
	v_lshlrev_b32_e32 v145, 16, v145
	v_lshlrev_b32_e32 v146, 16, v146
	v_lshlrev_b32_e32 v147, 16, v147
	v_lshlrev_b32_e32 v148, 16, v148
	v_lshlrev_b32_e32 v149, 16, v149
	v_lshlrev_b32_e32 v150, 16, v150
	v_lshlrev_b32_e32 v151, 16, v151
	v_lshlrev_b32_e32 v152, 16, v152
	v_lshlrev_b32_e32 v153, 16, v153
	v_lshlrev_b32_e32 v154, 16, v154
	v_lshlrev_b32_e32 v155, 16, v155
	v_lshlrev_b32_e32 v156, 16, v156
	v_lshlrev_b32_e32 v157, 16, v157
	v_lshlrev_b32_e32 v158, 16, v158
	v_lshlrev_b32_e32 v159, 16, v159
	v_lshlrev_b32_e32 v160, 16, v160
	v_lshlrev_b32_e32 v161, 16, v161
	v_lshlrev_b32_e32 v162, 16, v162
	v_lshlrev_b32_e32 v163, 16, v163
	v_lshlrev_b32_e32 v164, 16, v164
	v_lshlrev_b32_e32 v165, 16, v165
	v_lshlrev_b32_e32 v166, 16, v166
	v_lshlrev_b32_e32 v167, 16, v167
	v_lshlrev_b32_e32 v168, 16, v168
	v_lshlrev_b32_e32 v169, 16, v169
	v_lshlrev_b32_e32 v170, 16, v170
	v_lshlrev_b32_e32 v171, 16, v171
	v_lshlrev_b32_e32 v172, 16, v172
	v_lshlrev_b32_e32 v173, 16, v173
	v_lshlrev_b32_e32 v174, 16, v174
	v_lshlrev_b32_e32 v175, 16, v175
	v_lshlrev_b32_e32 v176, 16, v176
	v_lshlrev_b32_e32 v177, 16, v177
	v_lshlrev_b32_e32 v184, 16, v184
	v_lshlrev_b32_e32 v185, 16, v185
	v_lshlrev_b32_e32 v186, 16, v186
	v_lshlrev_b32_e32 v187, 16, v187
	v_fma_f32 v188, v28, v80, v29
	v_fma_f32 v189, v30, v81, v31
	v_fma_f32 v190, v23, v82, v25
	v_fmac_f32_e32 v188, v20, v83
	v_fmac_f32_e32 v189, v22, v84
	v_fmac_f32_e32 v190, v24, v85
	v_fmac_f32_e32 v188, v21, v86
	v_fmac_f32_e32 v189, v27, v87
	v_fmac_f32_e32 v190, v26, v88
	v_mul_f32_e32 v189, v189, v190
	ds_write_b32 v9, v189
	ds_write_b32 v32, v188
	v_fma_f32 v191, v28, v83, v29
	v_fma_f32 v192, v30, v84, v31
	v_fma_f32 v193, v23, v85, v25
	v_fmac_f32_e32 v191, v20, v86
	v_fmac_f32_e32 v192, v22, v87
	v_fmac_f32_e32 v193, v24, v88
	v_fmac_f32_e32 v191, v21, v89
	v_fmac_f32_e32 v192, v27, v90
	v_fmac_f32_e32 v193, v26, v91
	v_mul_f32_e32 v192, v192, v193
	ds_write_b32 v9, v192 offset:4
	ds_write_b32 v32, v191 offset:4
	v_fma_f32 v194, v28, v86, v29
	v_fma_f32 v195, v30, v87, v31
	v_fma_f32 v196, v23, v88, v25
	v_fmac_f32_e32 v194, v20, v89
	v_fmac_f32_e32 v195, v22, v90
	v_fmac_f32_e32 v196, v24, v91
	v_fmac_f32_e32 v194, v21, v92
	v_fmac_f32_e32 v195, v27, v93
	v_fmac_f32_e32 v196, v26, v94
	v_mul_f32_e32 v195, v195, v196
	ds_write_b32 v9, v195 offset:8
	ds_write_b32 v32, v194 offset:8
	v_fma_f32 v197, v28, v89, v29
	v_fma_f32 v198, v30, v90, v31
	v_fma_f32 v199, v23, v91, v25
	v_fmac_f32_e32 v197, v20, v92
	v_fmac_f32_e32 v198, v22, v93
	v_fmac_f32_e32 v199, v24, v94
	v_fmac_f32_e32 v197, v21, v95
	v_fmac_f32_e32 v198, v27, v96
	v_fmac_f32_e32 v199, v26, v97
	v_mul_f32_e32 v198, v198, v199
	ds_write_b32 v9, v198 offset:12
	ds_write_b32 v32, v197 offset:12
	v_fma_f32 v188, v28, v92, v29
	v_fma_f32 v189, v30, v93, v31
	v_fma_f32 v190, v23, v94, v25
	v_fmac_f32_e32 v188, v20, v95
	v_fmac_f32_e32 v189, v22, v96
	v_fmac_f32_e32 v190, v24, v97
	v_fmac_f32_e32 v188, v21, v98
	v_fmac_f32_e32 v189, v27, v99
	v_fmac_f32_e32 v190, v26, v100
	v_mul_f32_e32 v189, v189, v190
	ds_write_b32 v9, v189 offset:16
	ds_write_b32 v32, v188 offset:16
	v_fma_f32 v191, v28, v95, v29
	v_fma_f32 v192, v30, v96, v31
	v_fma_f32 v193, v23, v97, v25
	v_fmac_f32_e32 v191, v20, v98
	v_fmac_f32_e32 v192, v22, v99
; __device__ __forceinline__ float bf2f(bfr h) { return __uint_as_float(((unsigned)h) << 16); }
; __device__ __forceinline__ void phase_zprep(const Params& P, float* sm, int bid, int nb) {
;     ...
;         for (int tt = 0; tt < 32; ++tt) {
;             float nv[3], y[3];
; #pragma unroll
;             for (int g = 0; g < 3; ++g) {
;                 nv[g] = (r0 + tt + 1 < seg1) ? bf2f(up[(size_t)(tt + 1) * 3072 + g * 512]) : 0.f;
;                 y[g] = bs[g] + pv[g] * w0[g] + cv[g] * w1[g] + nv[g] * w2[g];
;                 pv[g] = cv[g]; cv[g] = nv[g];
;             }
;             sz[tid * 33 + tt] = y[1] * y[2];
;             sx[tid * 33 + tt] = y[0];
;         }
	v_fmac_f32_e32 v193, v24, v100
	v_fmac_f32_e32 v191, v21, v101
	v_fmac_f32_e32 v192, v27, v102
	v_fmac_f32_e32 v193, v26, v103
	v_mul_f32_e32 v192, v192, v193
	ds_write_b32 v9, v192 offset:20
	ds_write_b32 v32, v191 offset:20
	v_fma_f32 v194, v28, v98, v29
	v_fma_f32 v195, v30, v99, v31
	v_fma_f32 v196, v23, v100, v25
	v_fmac_f32_e32 v194, v20, v101
	v_fmac_f32_e32 v195, v22, v102
	v_fmac_f32_e32 v196, v24, v103
	v_fmac_f32_e32 v194, v21, v104
	v_fmac_f32_e32 v195, v27, v105
	v_fmac_f32_e32 v196, v26, v106
	v_mul_f32_e32 v195, v195, v196
	ds_write_b32 v9, v195 offset:24
	ds_write_b32 v32, v194 offset:24
	v_fma_f32 v197, v28, v101, v29
	v_fma_f32 v198, v30, v102, v31
	v_fma_f32 v199, v23, v103, v25
	v_fmac_f32_e32 v197, v20, v104
	v_fmac_f32_e32 v198, v22, v105
	v_fmac_f32_e32 v199, v24, v106
	v_fmac_f32_e32 v197, v21, v107
	v_fmac_f32_e32 v198, v27, v108
	v_fmac_f32_e32 v199, v26, v109
	v_mul_f32_e32 v198, v198, v199
	ds_write_b32 v9, v198 offset:28
	ds_write_b32 v32, v197 offset:28
	v_fma_f32 v188, v28, v104, v29
	v_fma_f32 v189, v30, v105, v31
	v_fma_f32 v190, v23, v106, v25
	v_fmac_f32_e32 v188, v20, v107
	v_fmac_f32_e32 v189, v22, v108
	v_fmac_f32_e32 v190, v24, v109
	v_fmac_f32_e32 v188, v21, v110
	v_fmac_f32_e32 v189, v27, v111
	v_fmac_f32_e32 v190, v26, v112
	v_mul_f32_e32 v189, v189, v190
	ds_write_b32 v9, v189 offset:32
	ds_write_b32 v32, v188 offset:32
	v_fma_f32 v191, v28, v107, v29
	v_fma_f32 v192, v30, v108, v31
	v_fma_f32 v193, v23, v109, v25
	v_fmac_f32_e32 v191, v20, v110
	v_fmac_f32_e32 v192, v22, v111
	v_fmac_f32_e32 v193, v24, v112
	v_fmac_f32_e32 v191, v21, v113
	v_fmac_f32_e32 v192, v27, v114
	v_fmac_f32_e32 v193, v26, v115
	v_mul_f32_e32 v192, v192, v193
	ds_write_b32 v9, v192 offset:36
	ds_write_b32 v32, v191 offset:36
	v_fma_f32 v194, v28, v110, v29
	v_fma_f32 v195, v30, v111, v31
	v_fma_f32 v196, v23, v112, v25
	v_fmac_f32_e32 v194, v20, v113
	v_fmac_f32_e32 v195, v22, v114
	v_fmac_f32_e32 v196, v24, v115
	v_fmac_f32_e32 v194, v21, v116
	v_fmac_f32_e32 v195, v27, v117
	v_fmac_f32_e32 v196, v26, v118
	v_mul_f32_e32 v195, v195, v196
	ds_write_b32 v9, v195 offset:40
	ds_write_b32 v32, v194 offset:40
	v_fma_f32 v197, v28, v113, v29
	v_fma_f32 v198, v30, v114, v31
	v_fma_f32 v199, v23, v115, v25
	v_fmac_f32_e32 v197, v20, v116
	v_fmac_f32_e32 v198, v22, v117
	v_fmac_f32_e32 v199, v24, v118
	v_fmac_f32_e32 v197, v21, v119
	v_fmac_f32_e32 v198, v27, v120
	v_fmac_f32_e32 v199, v26, v121
	v_mul_f32_e32 v198, v198, v199
	ds_write_b32 v9, v198 offset:44
	ds_write_b32 v32, v197 offset:44
	v_fma_f32 v188, v28, v116, v29
	v_fma_f32 v189, v30, v117, v31
	v_fma_f32 v190, v23, v118, v25
	v_fmac_f32_e32 v188, v20, v119
	v_fmac_f32_e32 v189, v22, v120
	v_fmac_f32_e32 v190, v24, v121
	v_fmac_f32_e32 v188, v21, v122
	v_fmac_f32_e32 v189, v27, v123
	v_fmac_f32_e32 v190, v26, v124
	v_mul_f32_e32 v189, v189, v190
	ds_write_b32 v9, v189 offset:48
	ds_write_b32 v32, v188 offset:48
	v_fma_f32 v191, v28, v119, v29
	v_fma_f32 v192, v30, v120, v31
	v_fma_f32 v193, v23, v121, v25
	v_fmac_f32_e32 v191, v20, v122
	v_fmac_f32_e32 v192, v22, v123
	v_fmac_f32_e32 v193, v24, v124
	v_fmac_f32_e32 v191, v21, v125
	v_fmac_f32_e32 v192, v27, v126
	v_fmac_f32_e32 v193, v26, v127
	v_mul_f32_e32 v192, v192, v193
	ds_write_b32 v9, v192 offset:52
	ds_write_b32 v32, v191 offset:52
	v_fma_f32 v194, v28, v122, v29
	v_fma_f32 v195, v30, v123, v31
	v_fma_f32 v196, v23, v124, v25
	v_fmac_f32_e32 v194, v20, v125
	v_fmac_f32_e32 v195, v22, v126
	v_fmac_f32_e32 v196, v24, v127
	v_fmac_f32_e32 v194, v21, v128
	v_fmac_f32_e32 v195, v27, v129
	v_fmac_f32_e32 v196, v26, v130
	v_mul_f32_e32 v195, v195, v196
	ds_write_b32 v9, v195 offset:56
	ds_write_b32 v32, v194 offset:56
	v_fma_f32 v197, v28, v125, v29
	v_fma_f32 v198, v30, v126, v31
	v_fma_f32 v199, v23, v127, v25
	v_fmac_f32_e32 v197, v20, v128
	v_fmac_f32_e32 v198, v22, v129
	v_fmac_f32_e32 v199, v24, v130
	v_fmac_f32_e32 v197, v21, v131
	v_fmac_f32_e32 v198, v27, v132
	v_fmac_f32_e32 v199, v26, v133
	v_mul_f32_e32 v198, v198, v199
	ds_write_b32 v9, v198 offset:60
	ds_write_b32 v32, v197 offset:60
	v_fma_f32 v188, v28, v128, v29
	v_fma_f32 v189, v30, v129, v31
	v_fma_f32 v190, v23, v130, v25
	v_fmac_f32_e32 v188, v20, v131
	v_fmac_f32_e32 v189, v22, v132
	v_fmac_f32_e32 v190, v24, v133
	v_fmac_f32_e32 v188, v21, v134
	v_fmac_f32_e32 v189, v27, v135
	v_fmac_f32_e32 v190, v26, v136
	v_mul_f32_e32 v189, v189, v190
	ds_write_b32 v9, v189 offset:64
	ds_write_b32 v32, v188 offset:64
	v_fma_f32 v191, v28, v131, v29
	v_fma_f32 v192, v30, v132, v31
	v_fma_f32 v193, v23, v133, v25
	v_fmac_f32_e32 v191, v20, v134
	v_fmac_f32_e32 v192, v22, v135
	v_fmac_f32_e32 v193, v24, v136
	v_fmac_f32_e32 v191, v21, v137
	v_fmac_f32_e32 v192, v27, v138
	v_fmac_f32_e32 v193, v26, v139
	v_mul_f32_e32 v192, v192, v193
	ds_write_b32 v9, v192 offset:68
	ds_write_b32 v32, v191 offset:68
	v_fma_f32 v194, v28, v134, v29
	v_fma_f32 v195, v30, v135, v31
	v_fma_f32 v196, v23, v136, v25
	v_fmac_f32_e32 v194, v20, v137
	v_fmac_f32_e32 v195, v22, v138
	v_fmac_f32_e32 v196, v24, v139
	v_fmac_f32_e32 v194, v21, v140
	v_fmac_f32_e32 v195, v27, v141
	v_fmac_f32_e32 v196, v26, v142
; __device__ __forceinline__ float bf2f(bfr h) { return __uint_as_float(((unsigned)h) << 16); }
; __device__ __forceinline__ void phase_zprep(const Params& P, float* sm, int bid, int nb) {
;     ...
;         for (int tt = 0; tt < 32; ++tt) {
;             float nv[3], y[3];
; #pragma unroll
;             for (int g = 0; g < 3; ++g) {
;                 nv[g] = (r0 + tt + 1 < seg1) ? bf2f(up[(size_t)(tt + 1) * 3072 + g * 512]) : 0.f;
;                 y[g] = bs[g] + pv[g] * w0[g] + cv[g] * w1[g] + nv[g] * w2[g];
;                 pv[g] = cv[g]; cv[g] = nv[g];
;             }
;             sz[tid * 33 + tt] = y[1] * y[2];
;             sx[tid * 33 + tt] = y[0];
;         }
	v_mul_f32_e32 v195, v195, v196
	ds_write_b32 v9, v195 offset:72
	ds_write_b32 v32, v194 offset:72
	v_fma_f32 v197, v28, v137, v29
	v_fma_f32 v198, v30, v138, v31
	v_fma_f32 v199, v23, v139, v25
	v_fmac_f32_e32 v197, v20, v140
	v_fmac_f32_e32 v198, v22, v141
	v_fmac_f32_e32 v199, v24, v142
	v_fmac_f32_e32 v197, v21, v143
	v_fmac_f32_e32 v198, v27, v144
	v_fmac_f32_e32 v199, v26, v145
	v_mul_f32_e32 v198, v198, v199
	ds_write_b32 v9, v198 offset:76
	ds_write_b32 v32, v197 offset:76
	v_fma_f32 v188, v28, v140, v29
	v_fma_f32 v189, v30, v141, v31
	v_fma_f32 v190, v23, v142, v25
	v_fmac_f32_e32 v188, v20, v143
	v_fmac_f32_e32 v189, v22, v144
	v_fmac_f32_e32 v190, v24, v145
	v_fmac_f32_e32 v188, v21, v146
	v_fmac_f32_e32 v189, v27, v147
	v_fmac_f32_e32 v190, v26, v148
	v_mul_f32_e32 v189, v189, v190
	ds_write_b32 v9, v189 offset:80
	ds_write_b32 v32, v188 offset:80
	v_fma_f32 v191, v28, v143, v29
	v_fma_f32 v192, v30, v144, v31
	v_fma_f32 v193, v23, v145, v25
	v_fmac_f32_e32 v191, v20, v146
	v_fmac_f32_e32 v192, v22, v147
	v_fmac_f32_e32 v193, v24, v148
	v_fmac_f32_e32 v191, v21, v149
	v_fmac_f32_e32 v192, v27, v150
	v_fmac_f32_e32 v193, v26, v151
	v_mul_f32_e32 v192, v192, v193
	ds_write_b32 v9, v192 offset:84
	ds_write_b32 v32, v191 offset:84
	v_fma_f32 v194, v28, v146, v29
	v_fma_f32 v195, v30, v147, v31
	v_fma_f32 v196, v23, v148, v25
	v_fmac_f32_e32 v194, v20, v149
	v_fmac_f32_e32 v195, v22, v150
	v_fmac_f32_e32 v196, v24, v151
	v_fmac_f32_e32 v194, v21, v152
	v_fmac_f32_e32 v195, v27, v153
	v_fmac_f32_e32 v196, v26, v154
	v_mul_f32_e32 v195, v195, v196
	ds_write_b32 v9, v195 offset:88
	ds_write_b32 v32, v194 offset:88
	v_fma_f32 v197, v28, v149, v29
	v_fma_f32 v198, v30, v150, v31
	v_fma_f32 v199, v23, v151, v25
	v_fmac_f32_e32 v197, v20, v152
	v_fmac_f32_e32 v198, v22, v153
	v_fmac_f32_e32 v199, v24, v154
	v_fmac_f32_e32 v197, v21, v155
	v_fmac_f32_e32 v198, v27, v156
	v_fmac_f32_e32 v199, v26, v157
	v_mul_f32_e32 v198, v198, v199
	ds_write_b32 v9, v198 offset:92
	ds_write_b32 v32, v197 offset:92
	v_fma_f32 v188, v28, v152, v29
	v_fma_f32 v189, v30, v153, v31
	v_fma_f32 v190, v23, v154, v25
	v_fmac_f32_e32 v188, v20, v155
	v_fmac_f32_e32 v189, v22, v156
	v_fmac_f32_e32 v190, v24, v157
	v_fmac_f32_e32 v188, v21, v158
	v_fmac_f32_e32 v189, v27, v159
	v_fmac_f32_e32 v190, v26, v160
	v_mul_f32_e32 v189, v189, v190
	ds_write_b32 v9, v189 offset:96
	ds_write_b32 v32, v188 offset:96
	v_fma_f32 v191, v28, v155, v29
	v_fma_f32 v192, v30, v156, v31
	v_fma_f32 v193, v23, v157, v25
	v_fmac_f32_e32 v191, v20, v158
	v_fmac_f32_e32 v192, v22, v159
	v_fmac_f32_e32 v193, v24, v160
	v_fmac_f32_e32 v191, v21, v161
	v_fmac_f32_e32 v192, v27, v162
	v_fmac_f32_e32 v193, v26, v163
	v_mul_f32_e32 v192, v192, v193
	ds_write_b32 v9, v192 offset:100
	ds_write_b32 v32, v191 offset:100
	v_fma_f32 v194, v28, v158, v29
	v_fma_f32 v195, v30, v159, v31
	v_fma_f32 v196, v23, v160, v25
	v_fmac_f32_e32 v194, v20, v161
	v_fmac_f32_e32 v195, v22, v162
	v_fmac_f32_e32 v196, v24, v163
	v_fmac_f32_e32 v194, v21, v164
	v_fmac_f32_e32 v195, v27, v165
	v_fmac_f32_e32 v196, v26, v166
	v_mul_f32_e32 v195, v195, v196
	ds_write_b32 v9, v195 offset:104
	ds_write_b32 v32, v194 offset:104
	v_fma_f32 v197, v28, v161, v29
	v_fma_f32 v198, v30, v162, v31
	v_fma_f32 v199, v23, v163, v25
	v_fmac_f32_e32 v197, v20, v164
	v_fmac_f32_e32 v198, v22, v165
	v_fmac_f32_e32 v199, v24, v166
	v_fmac_f32_e32 v197, v21, v167
	v_fmac_f32_e32 v198, v27, v168
	v_fmac_f32_e32 v199, v26, v169
	v_mul_f32_e32 v198, v198, v199
	ds_write_b32 v9, v198 offset:108
	ds_write_b32 v32, v197 offset:108
	v_fma_f32 v188, v28, v164, v29
	v_fma_f32 v189, v30, v165, v31
	v_fma_f32 v190, v23, v166, v25
	v_fmac_f32_e32 v188, v20, v167
	v_fmac_f32_e32 v189, v22, v168
	v_fmac_f32_e32 v190, v24, v169
	v_fmac_f32_e32 v188, v21, v170
	v_fmac_f32_e32 v189, v27, v171
	v_fmac_f32_e32 v190, v26, v172
	v_mul_f32_e32 v189, v189, v190
	ds_write_b32 v9, v189 offset:112
	ds_write_b32 v32, v188 offset:112
	v_fma_f32 v191, v28, v167, v29
	v_fma_f32 v192, v30, v168, v31
	v_fma_f32 v193, v23, v169, v25
	v_fmac_f32_e32 v191, v20, v170
	v_fmac_f32_e32 v192, v22, v171
	v_fmac_f32_e32 v193, v24, v172
	v_fmac_f32_e32 v191, v21, v173
	v_fmac_f32_e32 v192, v27, v174
	v_fmac_f32_e32 v193, v26, v175
	v_mul_f32_e32 v192, v192, v193
	ds_write_b32 v9, v192 offset:116
	ds_write_b32 v32, v191 offset:116
	v_fma_f32 v194, v28, v170, v29
	v_fma_f32 v195, v30, v171, v31
	v_fma_f32 v196, v23, v172, v25
	v_fmac_f32_e32 v194, v20, v173
	v_fmac_f32_e32 v195, v22, v174
	v_fmac_f32_e32 v196, v24, v175
	v_fmac_f32_e32 v194, v21, v176
	v_fmac_f32_e32 v195, v27, v177
	v_fmac_f32_e32 v196, v26, v184
	v_mul_f32_e32 v195, v195, v196
	ds_write_b32 v9, v195 offset:120
	ds_write_b32 v32, v194 offset:120
	v_fma_f32 v197, v28, v173, v29
	v_fma_f32 v198, v30, v174, v31
	v_fma_f32 v199, v23, v175, v25
	v_fmac_f32_e32 v197, v20, v176
	v_fmac_f32_e32 v198, v22, v177
	v_fmac_f32_e32 v199, v24, v184
	v_fmac_f32_e32 v197, v21, v185
	v_fmac_f32_e32 v198, v27, v186
	v_fmac_f32_e32 v199, v26, v187
	v_mul_f32_e32 v198, v198, v199
	ds_write_b32 v9, v198 offset:124
	ds_write_b32 v32, v197 offset:124

;     ...
;     for (int u = bid; u < ntok / 32; u += nb) {
;         const int r0 = tok0 + u * 32;
;         __syncthreads();
;         const int whu = r0 >= NCTX;
;         float ga[16], be[16], a2[16], b2[16];
; #pragma unroll
;         for (int i = 0; i < 2; ++i) {
;             const int c0 = i * 512 + lane * 8;
;             float sc[8], sh[8];
;             ld8(lg_ + c0, ga + i * 8); ld8(lb_ + c0, be + i * 8); ld8(mod + (size_t)whu * 6144 + 4096 + c0, sc); ld8(mod + (size_t)whu * 6144 + 3072 + c0, sh);
; #pragma unroll
;             for (int j = 0; j < 8; ++j) { a2[i * 8 + j] = ga[i * 8 + j] * (1.f + sc[j]); b2[i * 8 + j] = be[i * 8 + j] * (1.f + sc[j]) + sh[j]; }
;         }
;         uint4 raw[4][2];
; #pragma unroll
;         for (int q = 0; q < 4; ++q) {
;             const bfr* src = PRE + (size_t)(r0 + wave * 4 + q) * 1024 + lane * 8;
;             raw[q][0] = *(const uint4*)src; raw[q][1] = *(const uint4*)(src + 512);
;         }
; #pragma unroll
;         for (int q = 0; q < 4; ++q) {
;             const int rl = wave * 4 + q, row = r0 + rl;
;             float v[16];
;             up8(raw[q][0], v); up8(raw[q][1], v + 8);
;             float s = 0.f;
; #pragma unroll
;             for (int i = 0; i < 16; ++i) s += v[i];
;             const float mu = wave_sum(s) * (1.f / 1024.f);
;             float s2 = 0.f;
; #pragma unroll
;             for (int i = 0; i < 16; ++i) { const float d = v[i] - mu; s2 += d * d; }
;             const float rstd = rsqrtf(wave_sum(s2) * (1.f / 1024.f) + 1e-5f);
.LBB0_1045:
	s_lshl_b32 s2, s58, 5
	v_or_b32_e32 v98, s2, v138
	v_ashrrev_i32_e32 v99, 31, v98
	v_lshlrev_b64 v[34:35], 11, v[98:99]
	v_lshl_add_u64 v[2:3], v[80:81], 0, v[34:35]
	s_barrier
	global_load_dwordx4 v[58:61], v[2:3], off
	global_load_dwordx4 v[50:53], v[2:3], off offset:1024
	s_cmp_gt_i32 s58, 7
	s_cselect_b32 s0, 0x6000, 0
	s_add_u32 s3, s50, s0
	s_addc_u32 s40, s51, 0
	s_add_u32 s0, s3, 0x4000
	s_addc_u32 s1, s40, 0
	s_add_u32 s60, s3, 0x3000
	s_addc_u32 s61, s40, 0
	global_load_dwordx4 v[106:109], v78, s[0:1] offset:16
	global_load_dwordx4 v[110:113], v78, s[0:1]
	global_load_dwordx4 v[114:117], v149, s[0:1] offset:16
	global_load_dwordx4 v[10:13], v[86:87], off offset:16
	global_load_dwordx4 v[18:21], v[86:87], off
	global_load_dwordx4 v[2:5], v[86:87], off offset:2064
	global_load_dwordx4 v[158:161], v78, s[60:61] offset:16
	global_load_dwordx4 v[14:17], v[88:89], off offset:16
	global_load_dwordx4 v[22:25], v[88:89], off
	global_load_dwordx4 v[162:165], v78, s[60:61]
	global_load_dwordx4 v[6:9], v[88:89], off offset:2064
	global_load_dwordx4 v[74:77], v149, s[60:61] offset:16
	global_load_dwordx4 v[26:29], v[86:87], off offset:2048
	global_load_dwordx4 v[66:69], v149, s[0:1]
	global_load_dwordx4 v[30:33], v[88:89], off offset:2048
	global_load_dwordx4 v[70:73], v149, s[60:61]
	v_or_b32_e32 v104, 1, v98
	v_or_b32_e32 v102, 2, v98
	v_or_b32_e32 v100, 3, v98
	v_ashrrev_i32_e32 v105, 31, v104
	v_ashrrev_i32_e32 v103, 31, v102
	v_ashrrev_i32_e32 v101, 31, v100
	v_lshlrev_b64 v[36:37], 11, v[104:105]
	v_lshlrev_b64 v[38:39], 11, v[102:103]
	v_lshlrev_b64 v[40:41], 11, v[100:101]
	v_lshl_add_u64 v[120:121], v[92:93], 0, v[34:35]
	v_lshl_add_u64 v[118:119], v[94:95], 0, v[34:35]
	v_lshl_add_u64 v[34:35], v[80:81], 0, v[36:37]
	v_lshl_add_u64 v[36:37], v[80:81], 0, v[38:39]
	v_lshl_add_u64 v[122:123], v[80:81], 0, v[40:41]
	global_load_dwordx4 v[62:65], v[34:35], off
	global_load_dwordx4 v[54:57], v[34:35], off offset:1024
	global_load_dwordx4 v[46:49], v[36:37], off
	global_load_dwordx4 v[42:45], v[36:37], off offset:1024
	global_load_dwordx4 v[38:41], v[122:123], off
	s_nop 0
	global_load_dwordx4 v[34:37], v[122:123], off offset:1024
	v_mov_b32_e32 v99, 0
	s_waitcnt vmcnt(23)
	v_lshlrev_b32_e32 v130, 16, v58
	v_and_b32_e32 v131, 0xffff0000, v58
	v_add_f32_e32 v1, 0, v130
	v_lshlrev_b32_e32 v132, 16, v59
	v_add_f32_e32 v1, v1, v131
	v_and_b32_e32 v133, 0xffff0000, v59
	v_add_f32_e32 v1, v1, v132
	v_lshlrev_b32_e32 v134, 16, v60
	v_add_f32_e32 v1, v1, v133
	v_and_b32_e32 v135, 0xffff0000, v60
	v_add_f32_e32 v1, v1, v134
	v_lshlrev_b32_e32 v136, 16, v61
	v_add_f32_e32 v1, v1, v135
	v_and_b32_e32 v137, 0xffff0000, v61
	v_add_f32_e32 v1, v1, v136
	s_waitcnt vmcnt(22)
	v_lshlrev_b32_e32 v122, 16, v50
	v_add_f32_e32 v1, v1, v137
	v_and_b32_e32 v123, 0xffff0000, v50
	v_add_f32_e32 v1, v1, v122
	v_lshlrev_b32_e32 v124, 16, v51
	v_add_f32_e32 v1, v1, v123
	v_and_b32_e32 v125, 0xffff0000, v51
	v_add_f32_e32 v1, v1, v124
	v_lshlrev_b32_e32 v126, 16, v52
	v_add_f32_e32 v1, v1, v125
	v_and_b32_e32 v127, 0xffff0000, v52
	v_add_f32_e32 v1, v1, v126
	v_lshlrev_b32_e32 v128, 16, v53
	v_add_f32_e32 v1, v1, v127
	v_and_b32_e32 v129, 0xffff0000, v53
	v_add_f32_e32 v1, v1, v128
	v_add_f32_e32 v1, v1, v129
	s_waitcnt vmcnt(21)
	v_pk_add_f32 v[166:167], v[106:107], 1.0 op_sel_hi:[1,0]
	s_waitcnt vmcnt(20)
	v_pk_add_f32 v[170:171], v[110:111], 1.0 op_sel_hi:[1,0]
	v_add_f32_dpp v1, v1, v1 row_shr:1 row_mask:0xf bank_mask:0xf bound_ctrl:1
	s_waitcnt vmcnt(14)
	v_pk_fma_f32 v[110:111], v[14:15], v[166:167], v[158:159]
	s_waitcnt vmcnt(8)
	v_pk_add_f32 v[158:159], v[68:69], 1.0 op_sel_hi:[1,0]
	v_add_f32_dpp v1, v1, v1 row_shr:2 row_mask:0xf bank_mask:0xf bound_ctrl:1
	v_pk_mul_f32 v[68:69], v[28:29], v[158:159]
	s_waitcnt vmcnt(6)
	v_pk_fma_f32 v[72:73], v[32:33], v[158:159], v[72:73]
	v_add_f32_dpp v1, v1, v1 row_shr:4 row_mask:0xf bank_mask:0xf bound_ctrl:1
	v_pk_add_f32 v[52:53], v[108:109], 1.0 op_sel_hi:[1,0]
	v_pk_add_f32 v[172:173], v[116:117], 1.0 op_sel_hi:[1,0]
	v_add_f32_dpp v1, v1, v1 row_shr:8 row_mask:0xf bank_mask:0xf bound_ctrl:1
	v_pk_fma_f32 v[106:107], v[16:17], v[52:53], v[160:161]
	v_pk_fma_f32 v[116:117], v[22:23], v[170:171], v[162:163]
	v_mov_b32_dpp v99, v1 row_bcast:15 row_mask:0xa bank_mask:0xf bound_ctrl:1
	v_add_f32_e32 v1, v1, v99
	v_mov_b32_e32 v99, 0
	v_pk_add_f32 v[168:169], v[112:113], 1.0 op_sel_hi:[1,0]
	v_pk_add_f32 v[174:175], v[114:115], 1.0 op_sel_hi:[1,0]
	v_mov_b32_dpp v99, v1 row_bcast:31 row_mask:0xc bank_mask:0xf bound_ctrl:1
	v_add_f32_e32 v1, v1, v99
	v_pk_fma_f32 v[114:115], v[24:25], v[168:169], v[164:165]
	v_readlane_b32 s0, v1, 63
	v_pk_mul_f32 v[60:61], v[10:11], v[166:167]
	v_pk_mul_f32 v[108:109], v[20:21], v[168:169]
	v_mul_f32_e32 v158, s0, v150
	v_pk_add_f32 v[130:131], v[130:131], v[158:159] op_sel_hi:[1,0] neg_lo:[0,1] neg_hi:[0,1]
	v_pk_add_f32 v[132:133], v[132:133], v[158:159] op_sel_hi:[1,0] neg_lo:[0,1] neg_hi:[0,1]
	v_pk_mul_f32 v[160:161], v[130:131], v[130:131]
	v_pk_mul_f32 v[162:163], v[132:133], v[132:133]
	v_add_f32_e32 v1, v160, v161
	v_pk_add_f32 v[134:135], v[134:135], v[158:159] op_sel_hi:[1,0] neg_lo:[0,1] neg_hi:[0,1]
	v_add_f32_e32 v1, v162, v1
	v_pk_mul_f32 v[164:165], v[134:135], v[134:135]
	v_add_f32_e32 v1, v163, v1
	v_pk_add_f32 v[136:137], v[136:137], v[158:159] op_sel_hi:[1,0] neg_lo:[0,1] neg_hi:[0,1]
	v_add_f32_e32 v1, v164, v1
	v_pk_mul_f32 v[166:167], v[136:137], v[136:137]
	v_add_f32_e32 v1, v165, v1
	v_pk_add_f32 v[168:169], v[122:123], v[158:159] op_sel_hi:[1,0] neg_lo:[0,1] neg_hi:[0,1]
	v_add_f32_e32 v1, v166, v1
	v_pk_mul_f32 v[122:123], v[168:169], v[168:169]
; __device__ __forceinline__ uint4 pack8(const float* v) { uint4 r; r.x = pack2(v[0], v[1]); r.y = pack2(v[2], v[3]); r.z = pack2(v[4], v[5]); r.w = pack2(v[6], v[7]); return r; }
;     ...
;             const float mu = wave_sum(s) * (1.f / 1024.f);
;             float s2 = 0.f;
; #pragma unroll
;             for (int i = 0; i < 16; ++i) { const float d = v[i] - mu; s2 += d * d; }
;             const float rstd = rsqrtf(wave_sum(s2) * (1.f / 1024.f) + 1e-5f);
; #pragma unroll
;             for (int i = 0; i < 2; ++i) {
;                 const int c0 = i * 512 + lane * 8;
;                 float x[8], hf[8];
; #pragma unroll
;                 for (int j = 0; j < 8; ++j) { const float n_ = (v[i * 8 + j] - mu) * rstd; x[j] = n_ * ga[i * 8 + j] + be[i * 8 + j]; hf[j] = n_ * a2[i * 8 + j] + b2[i * 8 + j]; }
;                 *(uint4*)(X1 + (size_t)row * 1024 + c0) = pack8(x);
;                 const uint4 pk = pack8(hf);
;                 *(uint4*)(HFF + (size_t)row * 1024 + c0) = pk;
;                 *(uint4*)(hfs + rl * 1032 + c0) = pk;
;             }
;         }
	v_add_f32_e32 v1, v167, v1
	v_pk_mul_f32 v[112:113], v[18:19], v[170:171]
	v_pk_add_f32 v[170:171], v[124:125], v[158:159] op_sel_hi:[1,0] neg_lo:[0,1] neg_hi:[0,1]
	v_add_f32_e32 v1, v122, v1
	v_pk_mul_f32 v[124:125], v[170:171], v[170:171]
	v_add_f32_e32 v1, v123, v1
	v_pk_add_f32 v[126:127], v[126:127], v[158:159] op_sel_hi:[1,0] neg_lo:[0,1] neg_hi:[0,1]
	v_add_f32_e32 v1, v124, v1
	v_pk_mul_f32 v[58:59], v[12:13], v[52:53]
	v_pk_mul_f32 v[50:51], v[4:5], v[172:173]
	v_pk_fma_f32 v[52:53], v[8:9], v[172:173], v[76:77]
	v_pk_mul_f32 v[172:173], v[126:127], v[126:127]
	v_add_f32_e32 v1, v125, v1
	v_pk_add_f32 v[128:129], v[128:129], v[158:159] op_sel_hi:[1,0] neg_lo:[0,1] neg_hi:[0,1]
	v_add_f32_e32 v1, v172, v1
	v_pk_mul_f32 v[158:159], v[128:129], v[128:129]
	v_add_f32_e32 v1, v173, v1
	v_add_f32_e32 v1, v158, v1
	v_add_f32_e32 v1, v159, v1
	v_mov_b32_e32 v99, 0
	v_pk_add_f32 v[122:123], v[66:67], 1.0 op_sel_hi:[1,0]
	v_add_f32_dpp v1, v1, v1 row_shr:1 row_mask:0xf bank_mask:0xf bound_ctrl:1
	v_pk_mul_f32 v[66:67], v[26:27], v[122:123]
	v_pk_fma_f32 v[70:71], v[30:31], v[122:123], v[70:71]
	v_add_f32_dpp v1, v1, v1 row_shr:2 row_mask:0xf bank_mask:0xf bound_ctrl:1
	v_pk_mul_f32 v[76:77], v[2:3], v[174:175]
	v_pk_fma_f32 v[74:75], v[6:7], v[174:175], v[74:75]
	v_add_f32_dpp v1, v1, v1 row_shr:4 row_mask:0xf bank_mask:0xf bound_ctrl:1
	s_nop 1
	v_add_f32_dpp v1, v1, v1 row_shr:8 row_mask:0xf bank_mask:0xf bound_ctrl:1
	s_nop 1
	v_mov_b32_dpp v99, v1 row_bcast:15 row_mask:0xa bank_mask:0xf bound_ctrl:1
	v_add_f32_e32 v1, v1, v99
	v_mov_b32_e32 v99, 0
	s_nop 1
	v_mov_b32_dpp v99, v1 row_bcast:31 row_mask:0xc bank_mask:0xf bound_ctrl:1
	v_add_f32_e32 v1, v1, v99
	s_nop 0
	v_readlane_b32 s0, v1, 63
	s_nop 1
	v_fma_f32 v1, s0, v150, v151
	v_mul_f32_e32 v99, 0x4b800000, v1
	v_cmp_gt_f32_e32 vcc, s56, v1
	s_nop 1
	v_cndmask_b32_e32 v1, v1, v99, vcc
	v_rsq_f32_e32 v1, v1
	s_nop 0
	v_mul_f32_e32 v99, 0x45800000, v1
	v_cndmask_b32_e32 v158, v1, v99, vcc
	v_pk_mul_f32 v[122:123], v[130:131], v[158:159] op_sel_hi:[1,0]
	v_pk_mul_f32 v[124:125], v[132:133], v[158:159] op_sel_hi:[1,0]
	v_pk_mul_f32 v[134:135], v[134:135], v[158:159] op_sel_hi:[1,0]
	v_pk_mul_f32 v[136:137], v[136:137], v[158:159] op_sel_hi:[1,0]
	v_pk_fma_f32 v[130:131], v[112:113], v[122:123], v[116:117]
	v_pk_fma_f32 v[122:123], v[18:19], v[122:123], v[22:23]
	v_pk_fma_f32 v[132:133], v[108:109], v[124:125], v[114:115]
	v_pk_fma_f32 v[124:125], v[20:21], v[124:125], v[24:25]
	v_pk_fma_f32 v[160:161], v[60:61], v[134:135], v[110:111]
	v_pk_fma_f32 v[134:135], v[10:11], v[134:135], v[14:15]
	v_pk_fma_f32 v[162:163], v[58:59], v[136:137], v[106:107]
	v_pk_fma_f32 v[136:137], v[12:13], v[136:137], v[16:17]
	v_cvt_pk_bf16_f32 v122, v122, v123
	v_cvt_pk_bf16_f32 v123, v124, v125
	v_cvt_pk_bf16_f32 v124, v134, v135
	v_cvt_pk_bf16_f32 v125, v136, v137
	global_store_dwordx4 v[120:121], v[122:125], off
	v_pk_mul_f32 v[126:127], v[126:127], v[158:159] op_sel_hi:[1,0]
	v_pk_mul_f32 v[128:129], v[128:129], v[158:159] op_sel_hi:[1,0]
	v_cvt_pk_bf16_f32 v122, v130, v131
	v_cvt_pk_bf16_f32 v123, v132, v133
	v_cvt_pk_bf16_f32 v124, v160, v161
	v_cvt_pk_bf16_f32 v125, v162, v163
	global_store_dwordx4 v[118:119], v[122:125], off
	ds_write_b128 v83, v[122:125] offset:16
	v_pk_fma_f32 v[134:135], v[76:77], v[126:127], v[74:75]
	v_pk_mul_f32 v[122:123], v[168:169], v[158:159] op_sel_hi:[1,0]
	v_pk_mul_f32 v[124:125], v[170:171], v[158:159] op_sel_hi:[1,0]
	v_pk_fma_f32 v[130:131], v[66:67], v[122:123], v[70:71]
	v_pk_fma_f32 v[122:123], v[26:27], v[122:123], v[30:31]
	v_pk_fma_f32 v[132:133], v[68:69], v[124:125], v[72:73]
	v_pk_fma_f32 v[124:125], v[28:29], v[124:125], v[32:33]
	v_pk_fma_f32 v[126:127], v[2:3], v[126:127], v[6:7]
	v_pk_fma_f32 v[136:137], v[50:51], v[128:129], v[52:53]
	v_pk_fma_f32 v[128:129], v[4:5], v[128:129], v[8:9]
	v_cvt_pk_bf16_f32 v122, v122, v123
	v_cvt_pk_bf16_f32 v123, v124, v125
	v_cvt_pk_bf16_f32 v124, v126, v127
	v_cvt_pk_bf16_f32 v125, v128, v129
	global_store_dwordx4 v[120:121], v[122:125], off offset:1024
	v_cvt_pk_bf16_f32 v120, v130, v131
	v_cvt_pk_bf16_f32 v121, v132, v133
	v_cvt_pk_bf16_f32 v122, v134, v135
	v_cvt_pk_bf16_f32 v123, v136, v137
	global_store_dwordx4 v[118:119], v[120:123], off offset:1024
	s_waitcnt vmcnt(9)
	v_lshlrev_b32_e32 v118, 16, v62
	v_and_b32_e32 v119, 0xffff0000, v62
	v_add_f32_e32 v1, 0, v118
	v_lshlrev_b32_e32 v62, 16, v63
	v_add_f32_e32 v1, v1, v119
	v_and_b32_e32 v63, 0xffff0000, v63
	v_add_f32_e32 v1, v1, v62
	ds_write_b128 v83, v[120:123] offset:1040
	v_lshlrev_b32_e32 v120, 16, v64
	v_add_f32_e32 v1, v1, v63
	v_and_b32_e32 v121, 0xffff0000, v64
	v_add_f32_e32 v1, v1, v120
	v_lshlrev_b32_e32 v64, 16, v65
	v_add_f32_e32 v1, v1, v121
	v_and_b32_e32 v65, 0xffff0000, v65
	v_add_f32_e32 v1, v1, v64
	s_waitcnt vmcnt(8)
; __device__ __forceinline__ uint4 pack8(const float* v) { uint4 r; r.x = pack2(v[0], v[1]); r.y = pack2(v[2], v[3]); r.z = pack2(v[4], v[5]); r.w = pack2(v[6], v[7]); return r; }
;     ...
;         for (int q = 0; q < 4; ++q) {
;             const int rl = wave * 4 + q, row = r0 + rl;
;             float v[16];
;             up8(raw[q][0], v); up8(raw[q][1], v + 8);
;             float s = 0.f;
; #pragma unroll
;             for (int i = 0; i < 16; ++i) s += v[i];
;             const float mu = wave_sum(s) * (1.f / 1024.f);
;             float s2 = 0.f;
; #pragma unroll
;             for (int i = 0; i < 16; ++i) { const float d = v[i] - mu; s2 += d * d; }
;             const float rstd = rsqrtf(wave_sum(s2) * (1.f / 1024.f) + 1e-5f);
; #pragma unroll
;             for (int i = 0; i < 2; ++i) {
;                 const int c0 = i * 512 + lane * 8;
;                 float x[8], hf[8];
; #pragma unroll
;                 for (int j = 0; j < 8; ++j) { const float n_ = (v[i * 8 + j] - mu) * rstd; x[j] = n_ * ga[i * 8 + j] + be[i * 8 + j]; hf[j] = n_ * a2[i * 8 + j] + b2[i * 8 + j]; }
;                 *(uint4*)(X1 + (size_t)row * 1024 + c0) = pack8(x);
;                 const uint4 pk = pack8(hf);
;                 *(uint4*)(HFF + (size_t)row * 1024 + c0) = pk;
;                 *(uint4*)(hfs + rl * 1032 + c0) = pk;
;             }
;         }
	v_lshlrev_b32_e32 v122, 16, v54
	v_add_f32_e32 v1, v1, v65
	v_and_b32_e32 v123, 0xffff0000, v54
	v_add_f32_e32 v1, v1, v122
	v_lshlrev_b32_e32 v54, 16, v55
	v_add_f32_e32 v1, v1, v123
	v_and_b32_e32 v55, 0xffff0000, v55
	v_add_f32_e32 v1, v1, v54
	v_lshlrev_b32_e32 v124, 16, v56
	v_add_f32_e32 v1, v1, v55
	v_and_b32_e32 v125, 0xffff0000, v56
	v_add_f32_e32 v1, v1, v124
	v_lshlrev_b32_e32 v56, 16, v57
	v_add_f32_e32 v1, v1, v125
	v_and_b32_e32 v57, 0xffff0000, v57
	v_add_f32_e32 v1, v1, v56
	v_add_f32_e32 v1, v1, v57
	v_mov_b32_e32 v99, 0
	v_or_b32_e32 v126, s2, v140
	v_add_f32_dpp v1, v1, v1 row_shr:1 row_mask:0xf bank_mask:0xf bound_ctrl:1
	v_ashrrev_i32_e32 v127, 31, v126
	s_nop 0
	v_add_f32_dpp v1, v1, v1 row_shr:2 row_mask:0xf bank_mask:0xf bound_ctrl:1
	s_nop 1
	v_add_f32_dpp v1, v1, v1 row_shr:4 row_mask:0xf bank_mask:0xf bound_ctrl:1
	s_nop 1
	v_add_f32_dpp v1, v1, v1 row_shr:8 row_mask:0xf bank_mask:0xf bound_ctrl:1
	s_nop 1
	v_mov_b32_dpp v99, v1 row_bcast:15 row_mask:0xa bank_mask:0xf bound_ctrl:1
	v_add_f32_e32 v1, v1, v99
	v_mov_b32_e32 v99, 0
	s_nop 1
	v_mov_b32_dpp v99, v1 row_bcast:31 row_mask:0xc bank_mask:0xf bound_ctrl:1
	v_add_f32_e32 v1, v1, v99
	v_mov_b32_e32 v99, 0
	v_readlane_b32 s0, v1, 63
	s_nop 1
	v_mul_f32_e32 v128, s0, v150
	v_pk_add_f32 v[118:119], v[118:119], v[128:129] op_sel_hi:[1,0] neg_lo:[0,1] neg_hi:[0,1]
	v_pk_add_f32 v[62:63], v[62:63], v[128:129] op_sel_hi:[1,0] neg_lo:[0,1] neg_hi:[0,1]
	v_pk_mul_f32 v[130:131], v[118:119], v[118:119]
	v_pk_mul_f32 v[132:133], v[62:63], v[62:63]
	v_add_f32_e32 v1, v130, v131
	v_pk_add_f32 v[120:121], v[120:121], v[128:129] op_sel_hi:[1,0] neg_lo:[0,1] neg_hi:[0,1]
	v_add_f32_e32 v1, v132, v1
	v_pk_mul_f32 v[134:135], v[120:121], v[120:121]
	v_add_f32_e32 v1, v133, v1
	v_pk_add_f32 v[64:65], v[64:65], v[128:129] op_sel_hi:[1,0] neg_lo:[0,1] neg_hi:[0,1]
	v_add_f32_e32 v1, v134, v1
	v_pk_mul_f32 v[136:137], v[64:65], v[64:65]
	v_add_f32_e32 v1, v135, v1
	v_pk_add_f32 v[122:123], v[122:123], v[128:129] op_sel_hi:[1,0] neg_lo:[0,1] neg_hi:[0,1]
	v_add_f32_e32 v1, v136, v1
	v_pk_mul_f32 v[158:159], v[122:123], v[122:123]
	v_add_f32_e32 v1, v137, v1
	v_pk_add_f32 v[160:161], v[54:55], v[128:129] op_sel_hi:[1,0] neg_lo:[0,1] neg_hi:[0,1]
	v_add_f32_e32 v1, v158, v1
	v_pk_mul_f32 v[54:55], v[160:161], v[160:161]
	v_add_f32_e32 v1, v159, v1
	v_pk_add_f32 v[124:125], v[124:125], v[128:129] op_sel_hi:[1,0] neg_lo:[0,1] neg_hi:[0,1]
	v_add_f32_e32 v1, v54, v1
	v_pk_mul_f32 v[162:163], v[124:125], v[124:125]
	v_add_f32_e32 v1, v55, v1
	v_pk_add_f32 v[128:129], v[56:57], v[128:129] op_sel_hi:[1,0] neg_lo:[0,1] neg_hi:[0,1]
	v_add_f32_e32 v1, v162, v1
	v_pk_mul_f32 v[56:57], v[128:129], v[128:129]
	v_add_f32_e32 v1, v163, v1
	v_add_f32_e32 v1, v56, v1
	v_add_f32_e32 v1, v57, v1
	v_mov_b32_e32 v54, 0
	s_nop 0
	v_add_f32_dpp v1, v1, v1 row_shr:1 row_mask:0xf bank_mask:0xf bound_ctrl:1
	s_nop 1
	v_add_f32_dpp v1, v1, v1 row_shr:2 row_mask:0xf bank_mask:0xf bound_ctrl:1
	s_nop 1
	v_add_f32_dpp v1, v1, v1 row_shr:4 row_mask:0xf bank_mask:0xf bound_ctrl:1
	s_nop 1
	v_add_f32_dpp v1, v1, v1 row_shr:8 row_mask:0xf bank_mask:0xf bound_ctrl:1
	s_nop 1
	v_mov_b32_dpp v54, v1 row_bcast:15 row_mask:0xa bank_mask:0xf bound_ctrl:1
	v_add_f32_e32 v1, v1, v54
	v_mov_b32_e32 v54, 0
	s_nop 1
	v_mov_b32_dpp v54, v1 row_bcast:31 row_mask:0xc bank_mask:0xf bound_ctrl:1
	v_add_f32_e32 v1, v1, v54
	s_nop 0
	v_readlane_b32 s0, v1, 63
	s_nop 1
	v_fma_f32 v1, s0, v150, v151
	v_mul_f32_e32 v54, 0x4b800000, v1
	v_cmp_gt_f32_e32 vcc, s56, v1
	s_nop 1
	v_cndmask_b32_e32 v1, v1, v54, vcc
	v_rsq_f32_e32 v1, v1
	v_lshlrev_b64 v[54:55], 11, v[126:127]
	v_lshl_add_u64 v[126:127], v[92:93], 0, v[54:55]
	v_lshl_add_u64 v[130:131], v[94:95], 0, v[54:55]
	v_mul_f32_e32 v54, 0x45800000, v1
	v_cndmask_b32_e32 v132, v1, v54, vcc
	v_pk_mul_f32 v[54:55], v[118:119], v[132:133] op_sel_hi:[1,0]
	v_pk_mul_f32 v[56:57], v[62:63], v[132:133] op_sel_hi:[1,0]
	v_pk_mul_f32 v[120:121], v[120:121], v[132:133] op_sel_hi:[1,0]
	v_pk_mul_f32 v[64:65], v[64:65], v[132:133] op_sel_hi:[1,0]
	v_pk_fma_f32 v[118:119], v[112:113], v[54:55], v[116:117]
	v_pk_fma_f32 v[54:55], v[18:19], v[54:55], v[22:23]
	v_pk_fma_f32 v[62:63], v[108:109], v[56:57], v[114:115]
	v_pk_fma_f32 v[56:57], v[20:21], v[56:57], v[24:25]
	v_pk_fma_f32 v[134:135], v[60:61], v[120:121], v[110:111]
	v_pk_fma_f32 v[120:121], v[10:11], v[120:121], v[14:15]
	v_pk_fma_f32 v[136:137], v[58:59], v[64:65], v[106:107]
	v_pk_fma_f32 v[64:65], v[12:13], v[64:65], v[16:17]
	v_cvt_pk_bf16_f32 v54, v54, v55
	v_cvt_pk_bf16_f32 v55, v56, v57
	v_cvt_pk_bf16_f32 v56, v120, v121
	v_cvt_pk_bf16_f32 v57, v64, v65
	global_store_dwordx4 v[126:127], v[54:57], off
	s_nop 1
	v_cvt_pk_bf16_f32 v54, v118, v119
	v_cvt_pk_bf16_f32 v55, v62, v63
	v_cvt_pk_bf16_f32 v56, v134, v135
	v_cvt_pk_bf16_f32 v57, v136, v137
	global_store_dwordx4 v[130:131], v[54:57], off
	ds_write_b128 v141, v[54:57] offset:16
	v_pk_mul_f32 v[118:119], v[124:125], v[132:133] op_sel_hi:[1,0]
	v_pk_mul_f32 v[54:55], v[122:123], v[132:133] op_sel_hi:[1,0]
	v_pk_mul_f32 v[56:57], v[160:161], v[132:133] op_sel_hi:[1,0]
	v_pk_mul_f32 v[122:123], v[128:129], v[132:133] op_sel_hi:[1,0]
	v_pk_fma_f32 v[62:63], v[66:67], v[54:55], v[70:71]
	v_pk_fma_f32 v[54:55], v[26:27], v[54:55], v[30:31]
	v_pk_fma_f32 v[64:65], v[68:69], v[56:57], v[72:73]
	v_pk_fma_f32 v[56:57], v[28:29], v[56:57], v[32:33]
	v_pk_fma_f32 v[120:121], v[76:77], v[118:119], v[74:75]
	v_pk_fma_f32 v[118:119], v[2:3], v[118:119], v[6:7]
	v_pk_fma_f32 v[124:125], v[50:51], v[122:123], v[52:53]
	v_pk_fma_f32 v[122:123], v[4:5], v[122:123], v[8:9]
	v_cvt_pk_bf16_f32 v54, v54, v55
	v_cvt_pk_bf16_f32 v55, v56, v57
	v_cvt_pk_bf16_f32 v56, v118, v119
	v_cvt_pk_bf16_f32 v57, v122, v123
	global_store_dwordx4 v[126:127], v[54:57], off offset:1024
	v_or_b32_e32 v118, s2, v142
	v_ashrrev_i32_e32 v119, 31, v118
	v_cvt_pk_bf16_f32 v54, v62, v63
	v_cvt_pk_bf16_f32 v55, v64, v65
	v_cvt_pk_bf16_f32 v56, v120, v121
	v_cvt_pk_bf16_f32 v57, v124, v125
	global_store_dwordx4 v[130:131], v[54:57], off offset:1024
	ds_write_b128 v141, v[54:57] offset:1040
	s_waitcnt vmcnt(10)
; __device__ __forceinline__ uint4 pack8(const float* v) { uint4 r; r.x = pack2(v[0], v[1]); r.y = pack2(v[2], v[3]); r.z = pack2(v[4], v[5]); r.w = pack2(v[6], v[7]); return r; }
;     ...
;         for (int q = 0; q < 4; ++q) {
;             const int rl = wave * 4 + q, row = r0 + rl;
;             float v[16];
;             up8(raw[q][0], v); up8(raw[q][1], v + 8);
;             float s = 0.f;
; #pragma unroll
;             for (int i = 0; i < 16; ++i) s += v[i];
;             const float mu = wave_sum(s) * (1.f / 1024.f);
;             float s2 = 0.f;
; #pragma unroll
;             for (int i = 0; i < 16; ++i) { const float d = v[i] - mu; s2 += d * d; }
;             const float rstd = rsqrtf(wave_sum(s2) * (1.f / 1024.f) + 1e-5f);
; #pragma unroll
;             for (int i = 0; i < 2; ++i) {
;                 const int c0 = i * 512 + lane * 8;
;                 float x[8], hf[8];
; #pragma unroll
;                 for (int j = 0; j < 8; ++j) { const float n_ = (v[i * 8 + j] - mu) * rstd; x[j] = n_ * ga[i * 8 + j] + be[i * 8 + j]; hf[j] = n_ * a2[i * 8 + j] + b2[i * 8 + j]; }
;                 *(uint4*)(X1 + (size_t)row * 1024 + c0) = pack8(x);
;                 const uint4 pk = pack8(hf);
;                 *(uint4*)(HFF + (size_t)row * 1024 + c0) = pk;
;                 *(uint4*)(hfs + rl * 1032 + c0) = pk;
;             }
;         }
	v_lshlrev_b32_e32 v62, 16, v42
	v_lshlrev_b32_e32 v54, 16, v46
	v_and_b32_e32 v55, 0xffff0000, v46
	v_add_f32_e32 v1, 0, v54
	v_lshlrev_b32_e32 v46, 16, v47
	v_add_f32_e32 v1, v1, v55
	v_and_b32_e32 v47, 0xffff0000, v47
	v_add_f32_e32 v1, v1, v46
	v_lshlrev_b32_e32 v56, 16, v48
	v_add_f32_e32 v1, v1, v47
	v_and_b32_e32 v57, 0xffff0000, v48
	v_add_f32_e32 v1, v1, v56
	v_lshlrev_b32_e32 v48, 16, v49
	v_add_f32_e32 v1, v1, v57
	v_and_b32_e32 v49, 0xffff0000, v49
	v_add_f32_e32 v1, v1, v48
	v_add_f32_e32 v1, v1, v49
	v_and_b32_e32 v63, 0xffff0000, v42
	v_add_f32_e32 v1, v1, v62
	v_lshlrev_b32_e32 v42, 16, v43
	v_add_f32_e32 v1, v1, v63
	v_and_b32_e32 v43, 0xffff0000, v43
	v_add_f32_e32 v1, v1, v42
	v_lshlrev_b32_e32 v64, 16, v44
	v_add_f32_e32 v1, v1, v43
	v_and_b32_e32 v65, 0xffff0000, v44
	v_add_f32_e32 v1, v1, v64
	v_lshlrev_b32_e32 v44, 16, v45
	v_add_f32_e32 v1, v1, v65
	v_and_b32_e32 v45, 0xffff0000, v45
	v_add_f32_e32 v1, v1, v44
	v_add_f32_e32 v1, v1, v45
	s_nop 1
	v_add_f32_dpp v1, v1, v1 row_shr:1 row_mask:0xf bank_mask:0xf bound_ctrl:1
	s_nop 1
	v_add_f32_dpp v1, v1, v1 row_shr:2 row_mask:0xf bank_mask:0xf bound_ctrl:1
	s_nop 1
	v_add_f32_dpp v1, v1, v1 row_shr:4 row_mask:0xf bank_mask:0xf bound_ctrl:1
	s_nop 1
	v_add_f32_dpp v1, v1, v1 row_shr:8 row_mask:0xf bank_mask:0xf bound_ctrl:1
	s_nop 1
	v_mov_b32_dpp v99, v1 row_bcast:15 row_mask:0xa bank_mask:0xf bound_ctrl:1
	v_add_f32_e32 v1, v1, v99
	v_mov_b32_e32 v99, 0
	s_nop 1
	v_mov_b32_dpp v99, v1 row_bcast:31 row_mask:0xc bank_mask:0xf bound_ctrl:1
	v_add_f32_e32 v1, v1, v99
	s_nop 0
	v_readlane_b32 s0, v1, 63
	s_nop 1
	v_mul_f32_e32 v120, s0, v150
	v_pk_add_f32 v[54:55], v[54:55], v[120:121] op_sel_hi:[1,0] neg_lo:[0,1] neg_hi:[0,1]
	v_pk_add_f32 v[46:47], v[46:47], v[120:121] op_sel_hi:[1,0] neg_lo:[0,1] neg_hi:[0,1]
	v_pk_mul_f32 v[122:123], v[54:55], v[54:55]
	v_pk_mul_f32 v[124:125], v[46:47], v[46:47]
	v_add_f32_e32 v1, v122, v123
	v_pk_add_f32 v[56:57], v[56:57], v[120:121] op_sel_hi:[1,0] neg_lo:[0,1] neg_hi:[0,1]
	v_add_f32_e32 v1, v124, v1
	v_pk_mul_f32 v[126:127], v[56:57], v[56:57]
	v_add_f32_e32 v1, v125, v1
	v_pk_add_f32 v[48:49], v[48:49], v[120:121] op_sel_hi:[1,0] neg_lo:[0,1] neg_hi:[0,1]
	v_add_f32_e32 v1, v126, v1
	v_pk_mul_f32 v[128:129], v[48:49], v[48:49]
	v_add_f32_e32 v1, v127, v1
	v_pk_add_f32 v[62:63], v[62:63], v[120:121] op_sel_hi:[1,0] neg_lo:[0,1] neg_hi:[0,1]
	v_add_f32_e32 v1, v128, v1
	v_pk_mul_f32 v[130:131], v[62:63], v[62:63]
	v_add_f32_e32 v1, v129, v1
	v_pk_add_f32 v[132:133], v[42:43], v[120:121] op_sel_hi:[1,0] neg_lo:[0,1] neg_hi:[0,1]
	v_add_f32_e32 v1, v130, v1
	v_pk_mul_f32 v[42:43], v[132:133], v[132:133]
	v_add_f32_e32 v1, v131, v1
	v_pk_add_f32 v[64:65], v[64:65], v[120:121] op_sel_hi:[1,0] neg_lo:[0,1] neg_hi:[0,1]
	v_add_f32_e32 v1, v42, v1
	v_pk_mul_f32 v[134:135], v[64:65], v[64:65]
	v_add_f32_e32 v1, v43, v1
	v_pk_add_f32 v[120:121], v[44:45], v[120:121] op_sel_hi:[1,0] neg_lo:[0,1] neg_hi:[0,1]
	v_add_f32_e32 v1, v134, v1
	v_pk_mul_f32 v[44:45], v[120:121], v[120:121]
	v_add_f32_e32 v1, v135, v1
	v_add_f32_e32 v1, v44, v1
	v_add_f32_e32 v1, v45, v1
	v_mov_b32_e32 v42, 0
	s_nop 0
	v_add_f32_dpp v1, v1, v1 row_shr:1 row_mask:0xf bank_mask:0xf bound_ctrl:1
	s_nop 1
	v_add_f32_dpp v1, v1, v1 row_shr:2 row_mask:0xf bank_mask:0xf bound_ctrl:1
	s_nop 1
	v_add_f32_dpp v1, v1, v1 row_shr:4 row_mask:0xf bank_mask:0xf bound_ctrl:1
	s_nop 1
	v_add_f32_dpp v1, v1, v1 row_shr:8 row_mask:0xf bank_mask:0xf bound_ctrl:1
	s_nop 1
	v_mov_b32_dpp v42, v1 row_bcast:15 row_mask:0xa bank_mask:0xf bound_ctrl:1
	v_add_f32_e32 v1, v1, v42
	v_mov_b32_e32 v42, 0
	s_nop 1
	v_mov_b32_dpp v42, v1 row_bcast:31 row_mask:0xc bank_mask:0xf bound_ctrl:1
	v_add_f32_e32 v1, v1, v42
	s_nop 0
	v_readlane_b32 s0, v1, 63
	s_nop 1
	v_fma_f32 v1, s0, v150, v151
	v_mul_f32_e32 v42, 0x4b800000, v1
	v_cmp_gt_f32_e32 vcc, s56, v1
	s_nop 1
	v_cndmask_b32_e32 v1, v1, v42, vcc
	v_rsq_f32_e32 v1, v1
	v_lshlrev_b64 v[42:43], 11, v[118:119]
	v_lshl_add_u64 v[118:119], v[92:93], 0, v[42:43]
	v_lshl_add_u64 v[122:123], v[94:95], 0, v[42:43]
	v_mul_f32_e32 v42, 0x45800000, v1
	v_cndmask_b32_e32 v124, v1, v42, vcc
	v_pk_mul_f32 v[42:43], v[54:55], v[124:125] op_sel_hi:[1,0]
	v_pk_mul_f32 v[44:45], v[46:47], v[124:125] op_sel_hi:[1,0]
	v_pk_mul_f32 v[56:57], v[56:57], v[124:125] op_sel_hi:[1,0]
	v_pk_mul_f32 v[48:49], v[48:49], v[124:125] op_sel_hi:[1,0]
	v_pk_fma_f32 v[54:55], v[112:113], v[42:43], v[116:117]
	v_pk_fma_f32 v[42:43], v[18:19], v[42:43], v[22:23]
	v_pk_fma_f32 v[46:47], v[108:109], v[44:45], v[114:115]
	v_pk_fma_f32 v[44:45], v[20:21], v[44:45], v[24:25]
	v_pk_fma_f32 v[126:127], v[60:61], v[56:57], v[110:111]
	v_pk_fma_f32 v[56:57], v[10:11], v[56:57], v[14:15]
	v_pk_fma_f32 v[128:129], v[58:59], v[48:49], v[106:107]
	v_pk_fma_f32 v[48:49], v[12:13], v[48:49], v[16:17]
	v_cvt_pk_bf16_f32 v42, v42, v43
	v_cvt_pk_bf16_f32 v43, v44, v45
	v_cvt_pk_bf16_f32 v44, v56, v57
	v_cvt_pk_bf16_f32 v45, v48, v49
	global_store_dwordx4 v[118:119], v[42:45], off
	s_nop 1
	v_cvt_pk_bf16_f32 v42, v54, v55
	v_cvt_pk_bf16_f32 v43, v46, v47
	v_cvt_pk_bf16_f32 v44, v126, v127
	v_cvt_pk_bf16_f32 v45, v128, v129
	global_store_dwordx4 v[122:123], v[42:45], off
	ds_write_b128 v143, v[42:45] offset:16
	v_pk_mul_f32 v[54:55], v[64:65], v[124:125] op_sel_hi:[1,0]
	v_pk_mul_f32 v[42:43], v[62:63], v[124:125] op_sel_hi:[1,0]
	v_pk_mul_f32 v[44:45], v[132:133], v[124:125] op_sel_hi:[1,0]
	v_pk_mul_f32 v[62:63], v[120:121], v[124:125] op_sel_hi:[1,0]
	v_pk_fma_f32 v[46:47], v[66:67], v[42:43], v[70:71]
	v_pk_fma_f32 v[42:43], v[26:27], v[42:43], v[30:31]
	v_pk_fma_f32 v[48:49], v[68:69], v[44:45], v[72:73]
	v_pk_fma_f32 v[44:45], v[28:29], v[44:45], v[32:33]
	v_pk_fma_f32 v[56:57], v[76:77], v[54:55], v[74:75]
	v_pk_fma_f32 v[54:55], v[2:3], v[54:55], v[6:7]
	v_pk_fma_f32 v[64:65], v[50:51], v[62:63], v[52:53]
	v_pk_fma_f32 v[62:63], v[4:5], v[62:63], v[8:9]
	v_cvt_pk_bf16_f32 v42, v42, v43
	v_cvt_pk_bf16_f32 v43, v44, v45
	v_cvt_pk_bf16_f32 v44, v54, v55
	v_cvt_pk_bf16_f32 v45, v62, v63
	global_store_dwordx4 v[118:119], v[42:45], off offset:1024
	v_or_b32_e32 v54, s2, v144
	v_ashrrev_i32_e32 v55, 31, v54
	v_cvt_pk_bf16_f32 v42, v46, v47
	v_cvt_pk_bf16_f32 v43, v48, v49
	v_cvt_pk_bf16_f32 v44, v56, v57
	v_cvt_pk_bf16_f32 v45, v64, v65
	global_store_dwordx4 v[122:123], v[42:45], off offset:1024
	ds_write_b128 v143, v[42:45] offset:1040
	s_waitcnt vmcnt(12)
; __device__ __forceinline__ uint4 pack8(const float* v) { uint4 r; r.x = pack2(v[0], v[1]); r.y = pack2(v[2], v[3]); r.z = pack2(v[4], v[5]); r.w = pack2(v[6], v[7]); return r; }
;     ...
;         for (int q = 0; q < 4; ++q) {
;             const int rl = wave * 4 + q, row = r0 + rl;
;             float v[16];
;             up8(raw[q][0], v); up8(raw[q][1], v + 8);
;             float s = 0.f;
; #pragma unroll
;             for (int i = 0; i < 16; ++i) s += v[i];
;             const float mu = wave_sum(s) * (1.f / 1024.f);
;             float s2 = 0.f;
; #pragma unroll
;             for (int i = 0; i < 16; ++i) { const float d = v[i] - mu; s2 += d * d; }
;             const float rstd = rsqrtf(wave_sum(s2) * (1.f / 1024.f) + 1e-5f);
; #pragma unroll
;             for (int i = 0; i < 2; ++i) {
;                 const int c0 = i * 512 + lane * 8;
;                 float x[8], hf[8];
; #pragma unroll
;                 for (int j = 0; j < 8; ++j) { const float n_ = (v[i * 8 + j] - mu) * rstd; x[j] = n_ * ga[i * 8 + j] + be[i * 8 + j]; hf[j] = n_ * a2[i * 8 + j] + b2[i * 8 + j]; }
;                 *(uint4*)(X1 + (size_t)row * 1024 + c0) = pack8(x);
;                 const uint4 pk = pack8(hf);
;                 *(uint4*)(HFF + (size_t)row * 1024 + c0) = pk;
;                 *(uint4*)(hfs + rl * 1032 + c0) = pk;
;             }
;         }
;         __syncthreads();
;         if (probe < 3) {
;             f32x16 acc;
; #pragma unroll
;             for (int r = 0; r < 16; ++r) acc[r] = 0.f;
	v_lshlrev_b32_e32 v46, 16, v34
	v_lshlrev_b32_e32 v42, 16, v38
	v_and_b32_e32 v43, 0xffff0000, v38
	v_add_f32_e32 v1, 0, v42
	v_lshlrev_b32_e32 v38, 16, v39
	v_add_f32_e32 v1, v1, v43
	v_and_b32_e32 v39, 0xffff0000, v39
	v_add_f32_e32 v1, v1, v38
	v_lshlrev_b32_e32 v44, 16, v40
	v_add_f32_e32 v1, v1, v39
	v_and_b32_e32 v45, 0xffff0000, v40
	v_add_f32_e32 v1, v1, v44
	v_lshlrev_b32_e32 v40, 16, v41
	v_add_f32_e32 v1, v1, v45
	v_and_b32_e32 v41, 0xffff0000, v41
	v_add_f32_e32 v1, v1, v40
	v_add_f32_e32 v1, v1, v41
	v_and_b32_e32 v47, 0xffff0000, v34
	v_add_f32_e32 v1, v1, v46
	v_lshlrev_b32_e32 v34, 16, v35
	v_add_f32_e32 v1, v1, v47
	v_and_b32_e32 v35, 0xffff0000, v35
	v_add_f32_e32 v1, v1, v34
	v_lshlrev_b32_e32 v48, 16, v36
	v_add_f32_e32 v1, v1, v35
	v_and_b32_e32 v49, 0xffff0000, v36
	v_add_f32_e32 v1, v1, v48
	v_lshlrev_b32_e32 v36, 16, v37
	v_add_f32_e32 v1, v1, v49
	v_and_b32_e32 v37, 0xffff0000, v37
	v_add_f32_e32 v1, v1, v36
	v_add_f32_e32 v1, v1, v37
	v_mov_b32_e32 v56, 0
	v_lshlrev_b64 v[54:55], 11, v[54:55]
	v_add_f32_dpp v1, v1, v1 row_shr:1 row_mask:0xf bank_mask:0xf bound_ctrl:1
	s_nop 1
	v_add_f32_dpp v1, v1, v1 row_shr:2 row_mask:0xf bank_mask:0xf bound_ctrl:1
	s_nop 1
	v_add_f32_dpp v1, v1, v1 row_shr:4 row_mask:0xf bank_mask:0xf bound_ctrl:1
	s_nop 1
	v_add_f32_dpp v1, v1, v1 row_shr:8 row_mask:0xf bank_mask:0xf bound_ctrl:1
	s_nop 1
	v_mov_b32_dpp v56, v1 row_bcast:15 row_mask:0xa bank_mask:0xf bound_ctrl:1
	v_add_f32_e32 v1, v1, v56
	v_mov_b32_e32 v56, 0
	s_nop 1
	v_mov_b32_dpp v56, v1 row_bcast:31 row_mask:0xc bank_mask:0xf bound_ctrl:1
	v_add_f32_e32 v1, v1, v56
	s_nop 0
	v_readlane_b32 s0, v1, 63
	s_nop 1
	v_mul_f32_e32 v56, s0, v150
	v_pk_add_f32 v[42:43], v[42:43], v[56:57] op_sel_hi:[1,0] neg_lo:[0,1] neg_hi:[0,1]
	v_pk_add_f32 v[38:39], v[38:39], v[56:57] op_sel_hi:[1,0] neg_lo:[0,1] neg_hi:[0,1]
	v_pk_mul_f32 v[62:63], v[42:43], v[42:43]
	v_pk_mul_f32 v[64:65], v[38:39], v[38:39]
	v_add_f32_e32 v1, v62, v63
	v_pk_add_f32 v[44:45], v[44:45], v[56:57] op_sel_hi:[1,0] neg_lo:[0,1] neg_hi:[0,1]
	v_add_f32_e32 v1, v64, v1
	v_pk_mul_f32 v[118:119], v[44:45], v[44:45]
	v_add_f32_e32 v1, v65, v1
	v_pk_add_f32 v[40:41], v[40:41], v[56:57] op_sel_hi:[1,0] neg_lo:[0,1] neg_hi:[0,1]
	v_add_f32_e32 v1, v118, v1
	v_pk_mul_f32 v[120:121], v[40:41], v[40:41]
	v_add_f32_e32 v1, v119, v1
	v_pk_add_f32 v[46:47], v[46:47], v[56:57] op_sel_hi:[1,0] neg_lo:[0,1] neg_hi:[0,1]
	v_add_f32_e32 v1, v120, v1
	v_pk_mul_f32 v[122:123], v[46:47], v[46:47]
	v_add_f32_e32 v1, v121, v1
	v_pk_add_f32 v[34:35], v[34:35], v[56:57] op_sel_hi:[1,0] neg_lo:[0,1] neg_hi:[0,1]
	v_add_f32_e32 v1, v122, v1
	v_pk_mul_f32 v[124:125], v[34:35], v[34:35]
	v_add_f32_e32 v1, v123, v1
	v_pk_add_f32 v[48:49], v[48:49], v[56:57] op_sel_hi:[1,0] neg_lo:[0,1] neg_hi:[0,1]
	v_add_f32_e32 v1, v124, v1
	v_pk_mul_f32 v[126:127], v[48:49], v[48:49]
	v_add_f32_e32 v1, v125, v1
	v_pk_add_f32 v[36:37], v[36:37], v[56:57] op_sel_hi:[1,0] neg_lo:[0,1] neg_hi:[0,1]
	v_add_f32_e32 v1, v126, v1
	v_pk_mul_f32 v[56:57], v[36:37], v[36:37]
	v_add_f32_e32 v1, v127, v1
	v_add_f32_e32 v1, v56, v1
	v_add_f32_e32 v1, v57, v1
	v_mov_b32_e32 v56, 0
	s_nop 0
	v_add_f32_dpp v1, v1, v1 row_shr:1 row_mask:0xf bank_mask:0xf bound_ctrl:1
	s_nop 1
	v_add_f32_dpp v1, v1, v1 row_shr:2 row_mask:0xf bank_mask:0xf bound_ctrl:1
	s_nop 1
	v_add_f32_dpp v1, v1, v1 row_shr:4 row_mask:0xf bank_mask:0xf bound_ctrl:1
	s_nop 1
	v_add_f32_dpp v1, v1, v1 row_shr:8 row_mask:0xf bank_mask:0xf bound_ctrl:1
	s_nop 1
	v_mov_b32_dpp v56, v1 row_bcast:15 row_mask:0xa bank_mask:0xf bound_ctrl:1
	v_add_f32_e32 v1, v1, v56
	v_mov_b32_e32 v56, 0
	s_nop 1
	v_mov_b32_dpp v56, v1 row_bcast:31 row_mask:0xc bank_mask:0xf bound_ctrl:1
	v_add_f32_e32 v1, v1, v56
	s_nop 0
	v_readlane_b32 s0, v1, 63
	s_nop 1
	v_fma_f32 v1, s0, v150, v151
	v_mul_f32_e32 v56, 0x4b800000, v1
	v_cmp_gt_f32_e32 vcc, s56, v1
	s_mov_b64 s[0:1], 0
	s_nop 0
	v_cndmask_b32_e32 v1, v1, v56, vcc
	v_rsq_f32_e32 v1, v1
	v_lshl_add_u64 v[56:57], v[92:93], 0, v[54:55]
	v_lshl_add_u64 v[54:55], v[94:95], 0, v[54:55]
	v_mul_f32_e32 v62, 0x45800000, v1
	v_cndmask_b32_e32 v62, v1, v62, vcc
	v_pk_mul_f32 v[42:43], v[42:43], v[62:63] op_sel_hi:[1,0]
	v_mov_b32_e32 v1, v148
	v_pk_fma_f32 v[18:19], v[18:19], v[42:43], v[22:23]
	v_pk_mul_f32 v[22:23], v[38:39], v[62:63] op_sel_hi:[1,0]
	v_pk_fma_f32 v[64:65], v[112:113], v[42:43], v[116:117]
	v_pk_fma_f32 v[38:39], v[108:109], v[22:23], v[114:115]
	v_pk_fma_f32 v[20:21], v[20:21], v[22:23], v[24:25]
	v_pk_mul_f32 v[22:23], v[44:45], v[62:63] op_sel_hi:[1,0]
	s_nop 0
	v_pk_fma_f32 v[14:15], v[10:11], v[22:23], v[14:15]
	v_pk_mul_f32 v[10:11], v[40:41], v[62:63] op_sel_hi:[1,0]
	v_pk_fma_f32 v[24:25], v[60:61], v[22:23], v[110:111]
	v_pk_fma_f32 v[16:17], v[12:13], v[10:11], v[16:17]
	v_pk_fma_f32 v[22:23], v[58:59], v[10:11], v[106:107]
	v_cvt_pk_bf16_f32 v10, v18, v19
	v_cvt_pk_bf16_f32 v11, v20, v21
	v_cvt_pk_bf16_f32 v12, v14, v15
	v_cvt_pk_bf16_f32 v13, v16, v17
	global_store_dwordx4 v[56:57], v[10:13], off
	v_pk_mul_f32 v[18:19], v[48:49], v[62:63] op_sel_hi:[1,0]
	v_pk_mul_f32 v[14:15], v[34:35], v[62:63] op_sel_hi:[1,0]
	v_cvt_pk_bf16_f32 v10, v64, v65
	v_cvt_pk_bf16_f32 v11, v38, v39
	v_cvt_pk_bf16_f32 v12, v24, v25
	v_cvt_pk_bf16_f32 v13, v22, v23
	global_store_dwordx4 v[54:55], v[10:13], off
	ds_write_b128 v145, v[10:13] offset:16
	v_pk_fma_f32 v[6:7], v[2:3], v[18:19], v[6:7]
	v_pk_mul_f32 v[10:11], v[46:47], v[62:63] op_sel_hi:[1,0]
	v_pk_mul_f32 v[2:3], v[36:37], v[62:63] op_sel_hi:[1,0]
	v_pk_fma_f32 v[12:13], v[66:67], v[10:11], v[70:71]
	v_pk_fma_f32 v[10:11], v[26:27], v[10:11], v[30:31]
	v_pk_fma_f32 v[16:17], v[68:69], v[14:15], v[72:73]
	v_pk_fma_f32 v[14:15], v[28:29], v[14:15], v[32:33]
	v_pk_fma_f32 v[8:9], v[4:5], v[2:3], v[8:9]
	v_pk_fma_f32 v[20:21], v[76:77], v[18:19], v[74:75]
	v_pk_fma_f32 v[18:19], v[50:51], v[2:3], v[52:53]
	v_cvt_pk_bf16_f32 v2, v10, v11
	v_cvt_pk_bf16_f32 v3, v14, v15
	v_cvt_pk_bf16_f32 v4, v6, v7
	v_cvt_pk_bf16_f32 v5, v8, v9
	global_store_dwordx4 v[56:57], v[2:5], off offset:1024
	v_mov_b32_e32 v6, v79
	v_mov_b32_e32 v7, v79
	v_cvt_pk_bf16_f32 v2, v12, v13
	v_cvt_pk_bf16_f32 v3, v16, v17
	v_cvt_pk_bf16_f32 v4, v20, v21
	v_cvt_pk_bf16_f32 v5, v18, v19
	global_store_dwordx4 v[54:55], v[2:5], off offset:1024
	ds_write_b128 v145, v[2:5] offset:1040
	v_mov_b32_e32 v8, v79
	v_mov_b32_e32 v2, 0
	v_mov_b32_e32 v3, v79
	v_mov_b32_e32 v4, v79
	v_mov_b32_e32 v5, v79
	v_mov_b32_e32 v9, v79
	v_mov_b32_e32 v10, v79
	v_mov_b32_e32 v11, v79
	v_mov_b32_e32 v12, v79
	v_mov_b32_e32 v13, v79
	v_mov_b32_e32 v14, v79
	v_mov_b32_e32 v15, v79
	v_mov_b32_e32 v16, v79
	v_mov_b32_e32 v17, v79
	s_waitcnt lgkmcnt(0)
	s_barrier
;     ...
;             f32x16 acc;
; #pragma unroll
;             for (int r = 0; r < 16; ++r) acc[r] = 0.f;
;             const bfr* bp = RT + ((size_t)wave * 64 + lane) * 8;
;             const bfr* ap = hfs + (lane & 31) * 1032 + (lane >> 5) * 8;
; #pragma unroll 8
;             for (int k = 0; k < 64; ++k) {
;                 const bf16x8 a = *(const bf16x8*)(ap + k * 16);
;                 const bf16x8 b = *(const bf16x8*)(bp + (size_t)k * 8 * 64 * 8);
;                 acc = __builtin_amdgcn_mfma_f32_32x32x16_bf16(a, b, acc, 0, 0, 0);
;             }
	v_readlane_b32 s2, v252, 21
	v_readlane_b32 s3, v252, 22
	v_lshlrev_b32_e32 v158, 4, v0
	s_add_u32 s2, s2, 0xca8000
	s_addc_u32 s3, s3, 0
	global_load_dwordx4 v[34:37], v158, s[2:3]
	s_add_u32 s2, s2, 0x2000
	s_addc_u32 s3, s3, 0
	global_load_dwordx4 v[38:41], v158, s[2:3]
	s_add_u32 s2, s2, 0x2000
	s_addc_u32 s3, s3, 0
	global_load_dwordx4 v[42:45], v158, s[2:3]
	s_add_u32 s2, s2, 0x2000
	s_addc_u32 s3, s3, 0
	global_load_dwordx4 v[46:49], v158, s[2:3]
	s_add_u32 s2, s2, 0x2000
	s_addc_u32 s3, s3, 0
	global_load_dwordx4 v[50:53], v158, s[2:3]
	s_add_u32 s2, s2, 0x2000
	s_addc_u32 s3, s3, 0
	global_load_dwordx4 v[54:57], v158, s[2:3]
	s_add_u32 s2, s2, 0x2000
	s_addc_u32 s3, s3, 0
	global_load_dwordx4 v[58:61], v158, s[2:3]
	s_add_u32 s2, s2, 0x2000
	s_addc_u32 s3, s3, 0
	global_load_dwordx4 v[62:65], v158, s[2:3]
	s_add_u32 s2, s2, 0x2000
	s_addc_u32 s3, s3, 0
	global_load_dwordx4 v[66:69], v158, s[2:3]
	s_add_u32 s2, s2, 0x2000
	s_addc_u32 s3, s3, 0
	global_load_dwordx4 v[70:73], v158, s[2:3]
	s_add_u32 s2, s2, 0x2000
	s_addc_u32 s3, s3, 0
	global_load_dwordx4 v[74:77], v158, s[2:3]
	s_add_u32 s2, s2, 0x2000
	s_addc_u32 s3, s3, 0
	global_load_dwordx4 v[106:109], v158, s[2:3]
	s_add_u32 s2, s2, 0x2000
	s_addc_u32 s3, s3, 0
	global_load_dwordx4 v[110:113], v158, s[2:3]
	s_add_u32 s2, s2, 0x2000
	s_addc_u32 s3, s3, 0
	global_load_dwordx4 v[114:117], v158, s[2:3]
	s_add_u32 s2, s2, 0x2000
	s_addc_u32 s3, s3, 0
	ds_read_b128 v[18:21], v1
	ds_read_b128 v[22:25], v1 offset:32
	ds_read_b128 v[26:29], v1 offset:64
	ds_read_b128 v[30:33], v1 offset:96
	s_waitcnt vmcnt(13) lgkmcnt(3)
	v_mfma_f32_32x32x16_bf16 v[2:17], v[18:21], v[34:37], v[2:17]
	global_load_dwordx4 v[34:37], v158, s[2:3]
	s_add_u32 s2, s2, 0x2000
	s_addc_u32 s3, s3, 0
	ds_read_b128 v[18:21], v1 offset:128
	s_waitcnt vmcnt(13) lgkmcnt(3)
	v_mfma_f32_32x32x16_bf16 v[2:17], v[22:25], v[38:41], v[2:17]
	global_load_dwordx4 v[38:41], v158, s[2:3]
	s_add_u32 s2, s2, 0x2000
	s_addc_u32 s3, s3, 0
	ds_read_b128 v[22:25], v1 offset:160
	s_waitcnt vmcnt(13) lgkmcnt(3)
	v_mfma_f32_32x32x16_bf16 v[2:17], v[26:29], v[42:45], v[2:17]
	global_load_dwordx4 v[42:45], v158, s[2:3]
	s_add_u32 s2, s2, 0x2000
	s_addc_u32 s3, s3, 0
	ds_read_b128 v[26:29], v1 offset:192
	s_waitcnt vmcnt(13) lgkmcnt(3)
	v_mfma_f32_32x32x16_bf16 v[2:17], v[30:33], v[46:49], v[2:17]
	global_load_dwordx4 v[46:49], v158, s[2:3]
	s_add_u32 s2, s2, 0x2000
	s_addc_u32 s3, s3, 0
	ds_read_b128 v[30:33], v1 offset:224
	s_waitcnt vmcnt(13) lgkmcnt(3)
	v_mfma_f32_32x32x16_bf16 v[2:17], v[18:21], v[50:53], v[2:17]
	global_load_dwordx4 v[50:53], v158, s[2:3]
	s_add_u32 s2, s2, 0x2000
	s_addc_u32 s3, s3, 0
	ds_read_b128 v[18:21], v1 offset:256
	s_waitcnt vmcnt(13) lgkmcnt(3)
	v_mfma_f32_32x32x16_bf16 v[2:17], v[22:25], v[54:57], v[2:17]
	global_load_dwordx4 v[54:57], v158, s[2:3]
	s_add_u32 s2, s2, 0x2000
	s_addc_u32 s3, s3, 0
	ds_read_b128 v[22:25], v1 offset:288
	s_waitcnt vmcnt(13) lgkmcnt(3)
	v_mfma_f32_32x32x16_bf16 v[2:17], v[26:29], v[58:61], v[2:17]
	global_load_dwordx4 v[58:61], v158, s[2:3]
	s_add_u32 s2, s2, 0x2000
	s_addc_u32 s3, s3, 0
	ds_read_b128 v[26:29], v1 offset:320
	s_waitcnt vmcnt(13) lgkmcnt(3)
	v_mfma_f32_32x32x16_bf16 v[2:17], v[30:33], v[62:65], v[2:17]
	global_load_dwordx4 v[62:65], v158, s[2:3]
	s_add_u32 s2, s2, 0x2000
	s_addc_u32 s3, s3, 0
	ds_read_b128 v[30:33], v1 offset:352
	s_waitcnt vmcnt(13) lgkmcnt(3)
	v_mfma_f32_32x32x16_bf16 v[2:17], v[18:21], v[66:69], v[2:17]
	global_load_dwordx4 v[66:69], v158, s[2:3]
	s_add_u32 s2, s2, 0x2000
	s_addc_u32 s3, s3, 0
	ds_read_b128 v[18:21], v1 offset:384
	s_waitcnt vmcnt(13) lgkmcnt(3)
	v_mfma_f32_32x32x16_bf16 v[2:17], v[22:25], v[70:73], v[2:17]
	global_load_dwordx4 v[70:73], v158, s[2:3]
	s_add_u32 s2, s2, 0x2000
	s_addc_u32 s3, s3, 0
	ds_read_b128 v[22:25], v1 offset:416
	s_waitcnt vmcnt(13) lgkmcnt(3)
	v_mfma_f32_32x32x16_bf16 v[2:17], v[26:29], v[74:77], v[2:17]
	global_load_dwordx4 v[74:77], v158, s[2:3]
	s_add_u32 s2, s2, 0x2000
	s_addc_u32 s3, s3, 0
	ds_read_b128 v[26:29], v1 offset:448
	s_waitcnt vmcnt(13) lgkmcnt(3)
	v_mfma_f32_32x32x16_bf16 v[2:17], v[30:33], v[106:109], v[2:17]
	global_load_dwordx4 v[106:109], v158, s[2:3]
	s_add_u32 s2, s2, 0x2000
	s_addc_u32 s3, s3, 0
	ds_read_b128 v[30:33], v1 offset:480
	s_waitcnt vmcnt(13) lgkmcnt(3)
	v_mfma_f32_32x32x16_bf16 v[2:17], v[18:21], v[110:113], v[2:17]
	global_load_dwordx4 v[110:113], v158, s[2:3]
	s_add_u32 s2, s2, 0x2000
	s_addc_u32 s3, s3, 0
	ds_read_b128 v[18:21], v1 offset:512
	s_waitcnt vmcnt(13) lgkmcnt(3)
	v_mfma_f32_32x32x16_bf16 v[2:17], v[22:25], v[114:117], v[2:17]
	global_load_dwordx4 v[114:117], v158, s[2:3]
	s_add_u32 s2, s2, 0x2000
	s_addc_u32 s3, s3, 0
	ds_read_b128 v[22:25], v1 offset:544
	s_waitcnt vmcnt(13) lgkmcnt(3)
	v_mfma_f32_32x32x16_bf16 v[2:17], v[26:29], v[34:37], v[2:17]
	global_load_dwordx4 v[34:37], v158, s[2:3]
	s_add_u32 s2, s2, 0x2000
	s_addc_u32 s3, s3, 0
	ds_read_b128 v[26:29], v1 offset:576
	s_waitcnt vmcnt(13) lgkmcnt(3)
	v_mfma_f32_32x32x16_bf16 v[2:17], v[30:33], v[38:41], v[2:17]
	global_load_dwordx4 v[38:41], v158, s[2:3]
	s_add_u32 s2, s2, 0x2000
	s_addc_u32 s3, s3, 0
	ds_read_b128 v[30:33], v1 offset:608
	s_waitcnt vmcnt(13) lgkmcnt(3)
	v_mfma_f32_32x32x16_bf16 v[2:17], v[18:21], v[42:45], v[2:17]
	global_load_dwordx4 v[42:45], v158, s[2:3]
	s_add_u32 s2, s2, 0x2000
	s_addc_u32 s3, s3, 0
	ds_read_b128 v[18:21], v1 offset:640
	s_waitcnt vmcnt(13) lgkmcnt(3)
	v_mfma_f32_32x32x16_bf16 v[2:17], v[22:25], v[46:49], v[2:17]
	global_load_dwordx4 v[46:49], v158, s[2:3]
	s_add_u32 s2, s2, 0x2000
	s_addc_u32 s3, s3, 0
	ds_read_b128 v[22:25], v1 offset:672
	s_waitcnt vmcnt(13) lgkmcnt(3)
;     ...
; #pragma unroll 8
;             for (int k = 0; k < 64; ++k) {
;                 const bf16x8 a = *(const bf16x8*)(ap + k * 16);
;                 const bf16x8 b = *(const bf16x8*)(bp + (size_t)k * 8 * 64 * 8);
;                 acc = __builtin_amdgcn_mfma_f32_32x32x16_bf16(a, b, acc, 0, 0, 0);
;             }
	v_mfma_f32_32x32x16_bf16 v[2:17], v[26:29], v[50:53], v[2:17]
	global_load_dwordx4 v[50:53], v158, s[2:3]
	s_add_u32 s2, s2, 0x2000
	s_addc_u32 s3, s3, 0
	ds_read_b128 v[26:29], v1 offset:704
	s_waitcnt vmcnt(13) lgkmcnt(3)
	v_mfma_f32_32x32x16_bf16 v[2:17], v[30:33], v[54:57], v[2:17]
	global_load_dwordx4 v[54:57], v158, s[2:3]
	s_add_u32 s2, s2, 0x2000
	s_addc_u32 s3, s3, 0
	ds_read_b128 v[30:33], v1 offset:736
	s_waitcnt vmcnt(13) lgkmcnt(3)
	v_mfma_f32_32x32x16_bf16 v[2:17], v[18:21], v[58:61], v[2:17]
	global_load_dwordx4 v[58:61], v158, s[2:3]
	s_add_u32 s2, s2, 0x2000
	s_addc_u32 s3, s3, 0
	ds_read_b128 v[18:21], v1 offset:768
	s_waitcnt vmcnt(13) lgkmcnt(3)
	v_mfma_f32_32x32x16_bf16 v[2:17], v[22:25], v[62:65], v[2:17]
	global_load_dwordx4 v[62:65], v158, s[2:3]
	s_add_u32 s2, s2, 0x2000
	s_addc_u32 s3, s3, 0
	ds_read_b128 v[22:25], v1 offset:800
	s_waitcnt vmcnt(13) lgkmcnt(3)
	v_mfma_f32_32x32x16_bf16 v[2:17], v[26:29], v[66:69], v[2:17]
	global_load_dwordx4 v[66:69], v158, s[2:3]
	s_add_u32 s2, s2, 0x2000
	s_addc_u32 s3, s3, 0
	ds_read_b128 v[26:29], v1 offset:832
	s_waitcnt vmcnt(13) lgkmcnt(3)
	v_mfma_f32_32x32x16_bf16 v[2:17], v[30:33], v[70:73], v[2:17]
	global_load_dwordx4 v[70:73], v158, s[2:3]
	s_add_u32 s2, s2, 0x2000
	s_addc_u32 s3, s3, 0
	ds_read_b128 v[30:33], v1 offset:864
	s_waitcnt vmcnt(13) lgkmcnt(3)
	v_mfma_f32_32x32x16_bf16 v[2:17], v[18:21], v[74:77], v[2:17]
	global_load_dwordx4 v[74:77], v158, s[2:3]
	s_add_u32 s2, s2, 0x2000
	s_addc_u32 s3, s3, 0
	ds_read_b128 v[18:21], v1 offset:896
	s_waitcnt vmcnt(13) lgkmcnt(3)
	v_mfma_f32_32x32x16_bf16 v[2:17], v[22:25], v[106:109], v[2:17]
	global_load_dwordx4 v[106:109], v158, s[2:3]
	s_add_u32 s2, s2, 0x2000
	s_addc_u32 s3, s3, 0
	ds_read_b128 v[22:25], v1 offset:928
	s_waitcnt vmcnt(13) lgkmcnt(3)
	v_mfma_f32_32x32x16_bf16 v[2:17], v[26:29], v[110:113], v[2:17]
	global_load_dwordx4 v[110:113], v158, s[2:3]
	s_add_u32 s2, s2, 0x2000
	s_addc_u32 s3, s3, 0
	ds_read_b128 v[26:29], v1 offset:960
	s_waitcnt vmcnt(13) lgkmcnt(3)
	v_mfma_f32_32x32x16_bf16 v[2:17], v[30:33], v[114:117], v[2:17]
	global_load_dwordx4 v[114:117], v158, s[2:3]
	s_add_u32 s2, s2, 0x2000
	s_addc_u32 s3, s3, 0
	ds_read_b128 v[30:33], v1 offset:992
	s_waitcnt vmcnt(13) lgkmcnt(3)
	v_mfma_f32_32x32x16_bf16 v[2:17], v[18:21], v[34:37], v[2:17]
	global_load_dwordx4 v[34:37], v158, s[2:3]
	s_add_u32 s2, s2, 0x2000
	s_addc_u32 s3, s3, 0
	ds_read_b128 v[18:21], v1 offset:1024
	s_waitcnt vmcnt(13) lgkmcnt(3)
	v_mfma_f32_32x32x16_bf16 v[2:17], v[22:25], v[38:41], v[2:17]
	global_load_dwordx4 v[38:41], v158, s[2:3]
	s_add_u32 s2, s2, 0x2000
	s_addc_u32 s3, s3, 0
	ds_read_b128 v[22:25], v1 offset:1056
	s_waitcnt vmcnt(13) lgkmcnt(3)
	v_mfma_f32_32x32x16_bf16 v[2:17], v[26:29], v[42:45], v[2:17]
	global_load_dwordx4 v[42:45], v158, s[2:3]
	s_add_u32 s2, s2, 0x2000
	s_addc_u32 s3, s3, 0
	ds_read_b128 v[26:29], v1 offset:1088
	s_waitcnt vmcnt(13) lgkmcnt(3)
	v_mfma_f32_32x32x16_bf16 v[2:17], v[30:33], v[46:49], v[2:17]
	global_load_dwordx4 v[46:49], v158, s[2:3]
	s_add_u32 s2, s2, 0x2000
	s_addc_u32 s3, s3, 0
	ds_read_b128 v[30:33], v1 offset:1120
	s_waitcnt vmcnt(13) lgkmcnt(3)
	v_mfma_f32_32x32x16_bf16 v[2:17], v[18:21], v[50:53], v[2:17]
	global_load_dwordx4 v[50:53], v158, s[2:3]
	s_add_u32 s2, s2, 0x2000
	s_addc_u32 s3, s3, 0
	ds_read_b128 v[18:21], v1 offset:1152
	s_waitcnt vmcnt(13) lgkmcnt(3)
	v_mfma_f32_32x32x16_bf16 v[2:17], v[22:25], v[54:57], v[2:17]
	global_load_dwordx4 v[54:57], v158, s[2:3]
	s_add_u32 s2, s2, 0x2000
	s_addc_u32 s3, s3, 0
	ds_read_b128 v[22:25], v1 offset:1184
	s_waitcnt vmcnt(13) lgkmcnt(3)
	v_mfma_f32_32x32x16_bf16 v[2:17], v[26:29], v[58:61], v[2:17]
	global_load_dwordx4 v[58:61], v158, s[2:3]
	s_add_u32 s2, s2, 0x2000
	s_addc_u32 s3, s3, 0
	ds_read_b128 v[26:29], v1 offset:1216
	s_waitcnt vmcnt(13) lgkmcnt(3)
	v_mfma_f32_32x32x16_bf16 v[2:17], v[30:33], v[62:65], v[2:17]
	global_load_dwordx4 v[62:65], v158, s[2:3]
	s_add_u32 s2, s2, 0x2000
	s_addc_u32 s3, s3, 0
	ds_read_b128 v[30:33], v1 offset:1248
	s_waitcnt vmcnt(13) lgkmcnt(3)
	v_mfma_f32_32x32x16_bf16 v[2:17], v[18:21], v[66:69], v[2:17]
	global_load_dwordx4 v[66:69], v158, s[2:3]
	s_add_u32 s2, s2, 0x2000
	s_addc_u32 s3, s3, 0
	ds_read_b128 v[18:21], v1 offset:1280
	s_waitcnt vmcnt(13) lgkmcnt(3)
	v_mfma_f32_32x32x16_bf16 v[2:17], v[22:25], v[70:73], v[2:17]
	global_load_dwordx4 v[70:73], v158, s[2:3]
	s_add_u32 s2, s2, 0x2000
	s_addc_u32 s3, s3, 0
	ds_read_b128 v[22:25], v1 offset:1312
	s_waitcnt vmcnt(13) lgkmcnt(3)
	v_mfma_f32_32x32x16_bf16 v[2:17], v[26:29], v[74:77], v[2:17]
	global_load_dwordx4 v[74:77], v158, s[2:3]
	s_add_u32 s2, s2, 0x2000
	s_addc_u32 s3, s3, 0
	ds_read_b128 v[26:29], v1 offset:1344
	s_waitcnt vmcnt(13) lgkmcnt(3)
	v_mfma_f32_32x32x16_bf16 v[2:17], v[30:33], v[106:109], v[2:17]
	global_load_dwordx4 v[106:109], v158, s[2:3]
	s_add_u32 s2, s2, 0x2000
	s_addc_u32 s3, s3, 0
	ds_read_b128 v[30:33], v1 offset:1376
	s_waitcnt vmcnt(13) lgkmcnt(3)
	v_mfma_f32_32x32x16_bf16 v[2:17], v[18:21], v[110:113], v[2:17]
	global_load_dwordx4 v[110:113], v158, s[2:3]
	s_add_u32 s2, s2, 0x2000
	s_addc_u32 s3, s3, 0
	ds_read_b128 v[18:21], v1 offset:1408
	s_waitcnt vmcnt(13) lgkmcnt(3)
; __device__ __forceinline__ float sigmoidf_(float x) { return __builtin_amdgcn_rcpf(1.f + __expf(-x)); }
;     ...
; #pragma unroll 8
;             for (int k = 0; k < 64; ++k) {
;                 const bf16x8 a = *(const bf16x8*)(ap + k * 16);
;                 const bf16x8 b = *(const bf16x8*)(bp + (size_t)k * 8 * 64 * 8);
;                 acc = __builtin_amdgcn_mfma_f32_32x32x16_bf16(a, b, acc, 0, 0, 0);
;             }
; #pragma unroll
;             for (int r = 0; r < 16; ++r) {
;                 const int row = (r & 3) + 8 * (r >> 2) + 4 * (lane >> 5);
;                 lgt[row * 257 + wave * 32 + (lane & 31)] = acc[r];
;             }
;         }
;         __syncthreads();
;         float rb[4];
; #pragma unroll
;         for (int j = 0; j < 4; ++j) rb[j] = rbias[lane * 4 + j];
;         int selE[4]; float selG[4];
;         if (probe < 2) {
; #pragma unroll
;         for (int q = 0; q < 4; ++q) {
;             const int rl = wave * 4 + q;
;             float b[4];
; #pragma unroll
;             for (int j = 0; j < 4; ++j) b[j] = sigmoidf_(lgt[rl * 257 + lane * 4 + j]) + rb[j];
;             float m1 = -1e30f, m2 = -1e30f;
; #pragma unroll
;             for (int j = 0; j < 4; ++j) { const float v = b[j]; if (v > m1) { m2 = m1; m1 = v; } else if (v > m2) m2 = v; }
	v_mfma_f32_32x32x16_bf16 v[2:17], v[22:25], v[114:117], v[2:17]
	global_load_dwordx4 v[114:117], v158, s[2:3]
	s_add_u32 s2, s2, 0x2000
	s_addc_u32 s3, s3, 0
	ds_read_b128 v[22:25], v1 offset:1440
	s_waitcnt vmcnt(13) lgkmcnt(3)
	v_mfma_f32_32x32x16_bf16 v[2:17], v[26:29], v[34:37], v[2:17]
	global_load_dwordx4 v[34:37], v158, s[2:3]
	s_add_u32 s2, s2, 0x2000
	s_addc_u32 s3, s3, 0
	ds_read_b128 v[26:29], v1 offset:1472
	s_waitcnt vmcnt(13) lgkmcnt(3)
	v_mfma_f32_32x32x16_bf16 v[2:17], v[30:33], v[38:41], v[2:17]
	global_load_dwordx4 v[38:41], v158, s[2:3]
	s_add_u32 s2, s2, 0x2000
	s_addc_u32 s3, s3, 0
	ds_read_b128 v[30:33], v1 offset:1504
	s_waitcnt vmcnt(13) lgkmcnt(3)
	v_mfma_f32_32x32x16_bf16 v[2:17], v[18:21], v[42:45], v[2:17]
	global_load_dwordx4 v[42:45], v158, s[2:3]
	s_add_u32 s2, s2, 0x2000
	s_addc_u32 s3, s3, 0
	ds_read_b128 v[18:21], v1 offset:1536
	s_waitcnt vmcnt(13) lgkmcnt(3)
	v_mfma_f32_32x32x16_bf16 v[2:17], v[22:25], v[46:49], v[2:17]
	global_load_dwordx4 v[46:49], v158, s[2:3]
	s_add_u32 s2, s2, 0x2000
	s_addc_u32 s3, s3, 0
	ds_read_b128 v[22:25], v1 offset:1568
	s_waitcnt vmcnt(13) lgkmcnt(3)
	v_mfma_f32_32x32x16_bf16 v[2:17], v[26:29], v[50:53], v[2:17]
	global_load_dwordx4 v[50:53], v158, s[2:3]
	s_add_u32 s2, s2, 0x2000
	s_addc_u32 s3, s3, 0
	ds_read_b128 v[26:29], v1 offset:1600
	s_waitcnt vmcnt(13) lgkmcnt(3)
	v_mfma_f32_32x32x16_bf16 v[2:17], v[30:33], v[54:57], v[2:17]
	global_load_dwordx4 v[54:57], v158, s[2:3]
	s_add_u32 s2, s2, 0x2000
	s_addc_u32 s3, s3, 0
	ds_read_b128 v[30:33], v1 offset:1632
	s_waitcnt vmcnt(13) lgkmcnt(3)
	v_mfma_f32_32x32x16_bf16 v[2:17], v[18:21], v[58:61], v[2:17]
	global_load_dwordx4 v[58:61], v158, s[2:3]
	s_add_u32 s2, s2, 0x2000
	s_addc_u32 s3, s3, 0
	ds_read_b128 v[18:21], v1 offset:1664
	s_waitcnt vmcnt(13) lgkmcnt(3)
	v_mfma_f32_32x32x16_bf16 v[2:17], v[22:25], v[62:65], v[2:17]
	global_load_dwordx4 v[62:65], v158, s[2:3]
	ds_read_b128 v[22:25], v1 offset:1696
	s_waitcnt vmcnt(13) lgkmcnt(3)
	v_mfma_f32_32x32x16_bf16 v[2:17], v[26:29], v[66:69], v[2:17]
	ds_read_b128 v[26:29], v1 offset:1728
	s_waitcnt vmcnt(12) lgkmcnt(3)
	v_mfma_f32_32x32x16_bf16 v[2:17], v[30:33], v[70:73], v[2:17]
	ds_read_b128 v[30:33], v1 offset:1760
	s_waitcnt vmcnt(11) lgkmcnt(3)
	v_mfma_f32_32x32x16_bf16 v[2:17], v[18:21], v[74:77], v[2:17]
	ds_read_b128 v[18:21], v1 offset:1792
	s_waitcnt vmcnt(10) lgkmcnt(3)
	v_mfma_f32_32x32x16_bf16 v[2:17], v[22:25], v[106:109], v[2:17]
	ds_read_b128 v[22:25], v1 offset:1824
	s_waitcnt vmcnt(9) lgkmcnt(3)
	v_mfma_f32_32x32x16_bf16 v[2:17], v[26:29], v[110:113], v[2:17]
	ds_read_b128 v[26:29], v1 offset:1856
	s_waitcnt vmcnt(8) lgkmcnt(3)
	v_mfma_f32_32x32x16_bf16 v[2:17], v[30:33], v[114:117], v[2:17]
	ds_read_b128 v[30:33], v1 offset:1888
	s_waitcnt vmcnt(7) lgkmcnt(3)
	v_mfma_f32_32x32x16_bf16 v[2:17], v[18:21], v[34:37], v[2:17]
	ds_read_b128 v[18:21], v1 offset:1920
	s_waitcnt vmcnt(6) lgkmcnt(3)
	v_mfma_f32_32x32x16_bf16 v[2:17], v[22:25], v[38:41], v[2:17]
	ds_read_b128 v[22:25], v1 offset:1952
	s_waitcnt vmcnt(5) lgkmcnt(3)
	v_mfma_f32_32x32x16_bf16 v[2:17], v[26:29], v[42:45], v[2:17]
	ds_read_b128 v[26:29], v1 offset:1984
	s_waitcnt vmcnt(4) lgkmcnt(3)
	v_mfma_f32_32x32x16_bf16 v[2:17], v[30:33], v[46:49], v[2:17]
	ds_read_b128 v[30:33], v1 offset:2016
	s_waitcnt vmcnt(3) lgkmcnt(3)
	v_mfma_f32_32x32x16_bf16 v[2:17], v[18:21], v[50:53], v[2:17]
	s_waitcnt vmcnt(2) lgkmcnt(2)
	v_mfma_f32_32x32x16_bf16 v[2:17], v[22:25], v[54:57], v[2:17]
	s_waitcnt vmcnt(1) lgkmcnt(1)
	v_mfma_f32_32x32x16_bf16 v[2:17], v[26:29], v[58:61], v[2:17]
	s_waitcnt vmcnt(0) lgkmcnt(0)
	v_mfma_f32_32x32x16_bf16 v[2:17], v[30:33], v[62:65], v[2:17]
	s_nop 1
	s_nop 10
	ds_write_b32 v152, v2
	ds_write_b32 v152, v3 offset:1028
	ds_write_b32 v152, v4 offset:2056
	ds_write_b32 v152, v5 offset:3084
	ds_write_b32 v152, v6 offset:8224
	ds_write_b32 v152, v7 offset:9252
	ds_write_b32 v152, v8 offset:10280
	ds_write_b32 v152, v9 offset:11308
	ds_write_b32 v152, v10 offset:16448
	ds_write_b32 v152, v11 offset:17476
	ds_write_b32 v152, v12 offset:18504
	ds_write_b32 v152, v13 offset:19532
	ds_write_b32 v152, v14 offset:24672
	ds_write_b32 v152, v15 offset:25700
	ds_write_b32 v152, v16 offset:26728
	ds_write_b32 v152, v17 offset:27756
	s_waitcnt lgkmcnt(0)
	s_barrier
	global_load_dwordx4 v[2:5], v[90:91], off
	ds_read_b128 v[6:9], v153
	s_waitcnt lgkmcnt(0)
	v_mul_f32_e32 v1, 0xbfb8aa3b, v6
	v_mul_f32_e32 v6, 0xbfb8aa3b, v7
	v_exp_f32_e32 v1, v1
	v_exp_f32_e32 v6, v6
	v_add_f32_e32 v1, 1.0, v1
	v_add_f32_e32 v7, 1.0, v6
	v_rcp_f32_e32 v6, v1
	v_rcp_f32_e32 v7, v7
	s_waitcnt vmcnt(0)
	v_pk_add_f32 v[10:11], v[2:3], v[6:7]
	s_nop 0
	v_max_f32_e32 v6, 0xf149f2ca, v10
	v_cmp_ngt_f32_e32 vcc, v11, v6
	v_mov_b32_e32 v1, v6
	v_mov_b32_e32 v12, v11
	s_and_saveexec_b64 s[0:1], vcc
	s_cbranch_execz .LBB0_1051
	v_mov_b32_e32 v1, 0xf149f2ca
	v_cmp_gt_f32_e32 vcc, v11, v1
	s_and_saveexec_b64 s[2:3], vcc
	v_mov_b32_e32 v1, v11
	s_or_b64 exec, exec, s[2:3]
	v_mov_b32_e32 v12, v6

;     ...
;     for (int u = bid; u < ntok / 32; u += nb) {
;         const int r0 = tok0 + u * 32;
;         __syncthreads();
;         const int whu = r0 >= NCTX;
;         float ga[16], be[16], a2[16], b2[16];
; #pragma unroll
;         for (int i = 0; i < 2; ++i) {
;             const int c0 = i * 512 + lane * 8;
;             float sc[8], sh[8];
;             ld8(lg_ + c0, ga + i * 8); ld8(lb_ + c0, be + i * 8); ld8(mod + (size_t)whu * 6144 + 4096 + c0, sc); ld8(mod + (size_t)whu * 6144 + 3072 + c0, sh);
; #pragma unroll
;             for (int j = 0; j < 8; ++j) { a2[i * 8 + j] = ga[i * 8 + j] * (1.f + sc[j]); b2[i * 8 + j] = be[i * 8 + j] * (1.f + sc[j]) + sh[j]; }
;         }
;         uint4 raw[4][2];
; #pragma unroll
;         for (int q = 0; q < 4; ++q) {
;             const bfr* src = PRE + (size_t)(r0 + wave * 4 + q) * 1024 + lane * 8;
;             raw[q][0] = *(const uint4*)src; raw[q][1] = *(const uint4*)(src + 512);
;         }
; #pragma unroll
;         for (int q = 0; q < 4; ++q) {
;             const int rl = wave * 4 + q, row = r0 + rl;
;             float v[16];
;             up8(raw[q][0], v); up8(raw[q][1], v + 8);
;             float s = 0.f;
; #pragma unroll
;             for (int i = 0; i < 16; ++i) s += v[i];
;             const float mu = wave_sum(s) * (1.f / 1024.f);
;             float s2 = 0.f;
; #pragma unroll
;             for (int i = 0; i < 16; ++i) { const float d = v[i] - mu; s2 += d * d; }
;             const float rstd = rsqrtf(wave_sum(s2) * (1.f / 1024.f) + 1e-5f);
.LBB0_2186:
	s_lshl_b32 s55, s54, 5
	s_add_i32 s2, s55, 0x100
	v_or_b32_e32 v34, s2, v106
	v_ashrrev_i32_e32 v35, 31, v34
	v_lshlrev_b64 v[36:37], 11, v[34:35]
	v_lshl_add_u64 v[2:3], v[52:53], 0, v[36:37]
	s_barrier
	global_load_dwordx4 v[74:77], v[2:3], off
	global_load_dwordx4 v[78:81], v[2:3], off offset:1024
	s_cmp_gt_i32 s54, -1
	s_cselect_b32 s0, 0x6000, 0
	s_add_u32 s3, s50, s0
	s_addc_u32 s33, s51, 0
	s_add_u32 s0, s3, 0x4000
	s_addc_u32 s1, s33, 0
	global_load_dwordx4 v[82:85], v50, s[0:1] offset:16
	global_load_dwordx4 v[86:89], v50, s[0:1]
	global_load_dwordx4 v[90:93], v117, s[0:1] offset:16
	global_load_dwordx4 v[18:21], v[58:59], off offset:16
	global_load_dwordx4 v[26:29], v[58:59], off
	global_load_dwordx4 v[2:5], v[62:63], off offset:16
	s_add_u32 s40, s3, 0x3000
	s_addc_u32 s41, s33, 0
	global_load_dwordx4 v[98:101], v50, s[40:41] offset:16
	global_load_dwordx4 v[22:25], v[60:61], off offset:16
	global_load_dwordx4 v[30:33], v[60:61], off
	global_load_dwordx4 v[102:105], v50, s[40:41]
	global_load_dwordx4 v[6:9], v[64:65], off offset:16
	global_load_dwordx4 v[126:129], v117, s[40:41] offset:16
	global_load_dwordx4 v[10:13], v[62:63], off
	global_load_dwordx4 v[130:133], v117, s[0:1]
	global_load_dwordx4 v[14:17], v[64:65], off
	global_load_dwordx4 v[134:137], v117, s[40:41]
	v_or_b32_e32 v38, 1, v34
	v_or_b32_e32 v40, 2, v34
	v_or_b32_e32 v34, 3, v34
	v_ashrrev_i32_e32 v39, 31, v38
	v_ashrrev_i32_e32 v41, 31, v40
	v_ashrrev_i32_e32 v35, 31, v34
	v_lshlrev_b64 v[38:39], 11, v[38:39]
	v_lshlrev_b64 v[40:41], 11, v[40:41]
	v_lshlrev_b64 v[34:35], 11, v[34:35]
	v_lshl_add_u64 v[146:147], v[68:69], 0, v[36:37]
	v_lshl_add_u64 v[148:149], v[70:71], 0, v[36:37]
	v_lshl_add_u64 v[36:37], v[52:53], 0, v[38:39]
	v_lshl_add_u64 v[38:39], v[52:53], 0, v[40:41]
	v_lshl_add_u64 v[34:35], v[52:53], 0, v[34:35]
	global_load_dwordx4 v[138:141], v[36:37], off
	global_load_dwordx4 v[142:145], v[36:37], off offset:1024
	global_load_dwordx4 v[46:49], v[38:39], off
	global_load_dwordx4 v[42:45], v[38:39], off offset:1024
	s_nop 0
	global_load_dwordx4 v[38:41], v[34:35], off
	s_nop 0
	global_load_dwordx4 v[34:37], v[34:35], off offset:1024
	s_waitcnt vmcnt(23)
	v_lshlrev_b32_e32 v150, 16, v74
	v_and_b32_e32 v151, 0xffff0000, v74
	v_add_f32_e32 v1, 0, v150
	v_lshlrev_b32_e32 v152, 16, v75
	v_add_f32_e32 v1, v1, v151
	v_and_b32_e32 v153, 0xffff0000, v75
	v_add_f32_e32 v1, v1, v152
	v_lshlrev_b32_e32 v154, 16, v76
	v_add_f32_e32 v1, v1, v153
	v_and_b32_e32 v155, 0xffff0000, v76
	v_add_f32_e32 v1, v1, v154
	v_lshlrev_b32_e32 v156, 16, v77
	v_add_f32_e32 v1, v1, v155
	v_and_b32_e32 v157, 0xffff0000, v77
	v_add_f32_e32 v1, v1, v156
	s_waitcnt vmcnt(22)
	v_lshlrev_b32_e32 v158, 16, v78
	v_add_f32_e32 v1, v1, v157
	v_and_b32_e32 v159, 0xffff0000, v78
	v_add_f32_e32 v1, v1, v158
	v_lshlrev_b32_e32 v160, 16, v79
	v_add_f32_e32 v1, v1, v159
	v_and_b32_e32 v161, 0xffff0000, v79
	v_add_f32_e32 v1, v1, v160
	v_lshlrev_b32_e32 v162, 16, v80
	v_add_f32_e32 v1, v1, v161
	v_and_b32_e32 v163, 0xffff0000, v80
	v_add_f32_e32 v1, v1, v162
	v_lshlrev_b32_e32 v164, 16, v81
	v_add_f32_e32 v1, v1, v163
	v_and_b32_e32 v165, 0xffff0000, v81
	v_add_f32_e32 v1, v1, v164
	v_add_f32_e32 v1, v1, v165
	s_waitcnt vmcnt(21)
	v_pk_add_f32 v[76:77], v[84:85], 1.0 op_sel_hi:[1,0]
	v_pk_add_f32 v[78:79], v[82:83], 1.0 op_sel_hi:[1,0]
	v_add_f32_dpp v1, v1, v1 row_shr:1 row_mask:0xf bank_mask:0xf bound_ctrl:1
	s_waitcnt vmcnt(20)
	v_pk_add_f32 v[82:83], v[86:87], 1.0 op_sel_hi:[1,0]
	s_waitcnt vmcnt(19)
	v_pk_add_f32 v[166:167], v[90:91], 1.0 op_sel_hi:[1,0]
	v_add_f32_dpp v1, v1, v1 row_shr:2 row_mask:0xf bank_mask:0xf bound_ctrl:1
	s_waitcnt vmcnt(14)
	v_pk_fma_f32 v[90:91], v[24:25], v[76:77], v[100:101]
	s_waitcnt vmcnt(12)
	v_pk_fma_f32 v[100:101], v[30:31], v[82:83], v[102:103]
	v_add_f32_dpp v1, v1, v1 row_shr:4 row_mask:0xf bank_mask:0xf bound_ctrl:1
	v_mov_b32_e32 v102, 0
	v_pk_add_f32 v[80:81], v[88:89], 1.0 op_sel_hi:[1,0]
	v_add_f32_dpp v1, v1, v1 row_shr:8 row_mask:0xf bank_mask:0xf bound_ctrl:1
	v_pk_add_f32 v[84:85], v[92:93], 1.0 op_sel_hi:[1,0]
	v_pk_mul_f32 v[92:93], v[28:29], v[80:81]
	v_mov_b32_dpp v102, v1 row_bcast:15 row_mask:0xa bank_mask:0xf bound_ctrl:1
	v_add_f32_e32 v1, v1, v102
	v_mov_b32_e32 v102, 0
	v_pk_fma_f32 v[94:95], v[22:23], v[78:79], v[98:99]
	v_pk_fma_f32 v[98:99], v[32:33], v[80:81], v[104:105]
	v_mov_b32_dpp v102, v1 row_bcast:31 row_mask:0xc bank_mask:0xf bound_ctrl:1
	v_add_f32_e32 v1, v1, v102
	s_waitcnt vmcnt(10)
	v_pk_fma_f32 v[80:81], v[6:7], v[166:167], v[126:127]
	v_readlane_b32 s0, v1, 63
	v_pk_mul_f32 v[86:87], v[20:21], v[76:77]
	v_pk_fma_f32 v[76:77], v[8:9], v[84:85], v[128:129]
	v_mul_f32_e32 v102, s0, v123
	v_pk_add_f32 v[126:127], v[150:151], v[102:103] op_sel_hi:[1,0] neg_lo:[0,1] neg_hi:[0,1]
	v_pk_add_f32 v[128:129], v[152:153], v[102:103] op_sel_hi:[1,0] neg_lo:[0,1] neg_hi:[0,1]
	v_pk_mul_f32 v[104:105], v[126:127], v[126:127]
	v_pk_mul_f32 v[74:75], v[4:5], v[84:85]
	s_waitcnt vmcnt(8)
	v_pk_add_f32 v[84:85], v[132:133], 1.0 op_sel_hi:[1,0]
	v_pk_mul_f32 v[132:133], v[128:129], v[128:129]
	v_add_f32_e32 v1, v104, v105
	v_pk_mul_f32 v[96:97], v[26:27], v[82:83]
	v_pk_mul_f32 v[82:83], v[12:13], v[84:85]
	s_waitcnt vmcnt(6)
; __device__ __forceinline__ uint4 pack8(const float* v) { uint4 r; r.x = pack2(v[0], v[1]); r.y = pack2(v[2], v[3]); r.z = pack2(v[4], v[5]); r.w = pack2(v[6], v[7]); return r; }
;     ...
;             const float mu = wave_sum(s) * (1.f / 1024.f);
;             float s2 = 0.f;
; #pragma unroll
;             for (int i = 0; i < 16; ++i) { const float d = v[i] - mu; s2 += d * d; }
;             const float rstd = rsqrtf(wave_sum(s2) * (1.f / 1024.f) + 1e-5f);
; #pragma unroll
;             for (int i = 0; i < 2; ++i) {
;                 const int c0 = i * 512 + lane * 8;
;                 float x[8], hf[8];
; #pragma unroll
;                 for (int j = 0; j < 8; ++j) { const float n_ = (v[i * 8 + j] - mu) * rstd; x[j] = n_ * ga[i * 8 + j] + be[i * 8 + j]; hf[j] = n_ * a2[i * 8 + j] + b2[i * 8 + j]; }
;                 *(uint4*)(X1 + (size_t)row * 1024 + c0) = pack8(x);
;                 const uint4 pk = pack8(hf);
;                 *(uint4*)(HFF + (size_t)row * 1024 + c0) = pk;
;                 *(uint4*)(hfs + rl * 1032 + c0) = pk;
;             }
;         }
	v_pk_fma_f32 v[84:85], v[16:17], v[84:85], v[136:137]
	v_pk_add_f32 v[136:137], v[154:155], v[102:103] op_sel_hi:[1,0] neg_lo:[0,1] neg_hi:[0,1]
	v_add_f32_e32 v1, v132, v1
	v_pk_mul_f32 v[150:151], v[136:137], v[136:137]
	v_add_f32_e32 v1, v133, v1
	v_pk_add_f32 v[152:153], v[156:157], v[102:103] op_sel_hi:[1,0] neg_lo:[0,1] neg_hi:[0,1]
	v_add_f32_e32 v1, v150, v1
	v_pk_mul_f32 v[154:155], v[152:153], v[152:153]
	v_add_f32_e32 v1, v151, v1
	v_pk_add_f32 v[156:157], v[158:159], v[102:103] op_sel_hi:[1,0] neg_lo:[0,1] neg_hi:[0,1]
	v_add_f32_e32 v1, v154, v1
	v_pk_mul_f32 v[158:159], v[156:157], v[156:157]
	v_add_f32_e32 v1, v155, v1
	v_pk_add_f32 v[160:161], v[160:161], v[102:103] op_sel_hi:[1,0] neg_lo:[0,1] neg_hi:[0,1]
	v_add_f32_e32 v1, v158, v1
	v_pk_mul_f32 v[88:89], v[18:19], v[78:79]
	v_pk_mul_f32 v[78:79], v[2:3], v[166:167]
	v_pk_mul_f32 v[166:167], v[160:161], v[160:161]
	v_add_f32_e32 v1, v159, v1
	v_pk_add_f32 v[162:163], v[162:163], v[102:103] op_sel_hi:[1,0] neg_lo:[0,1] neg_hi:[0,1]
	v_add_f32_e32 v1, v166, v1
	v_pk_mul_f32 v[168:169], v[162:163], v[162:163]
	v_add_f32_e32 v1, v167, v1
	v_pk_add_f32 v[164:165], v[164:165], v[102:103] op_sel_hi:[1,0] neg_lo:[0,1] neg_hi:[0,1]
	v_add_f32_e32 v1, v168, v1
	v_pk_mul_f32 v[102:103], v[164:165], v[164:165]
	v_add_f32_e32 v1, v169, v1
	v_add_f32_e32 v1, v102, v1
	v_add_f32_e32 v1, v103, v1
	v_mov_b32_e32 v102, 0
	v_pk_add_f32 v[104:105], v[130:131], 1.0 op_sel_hi:[1,0]
	v_add_f32_dpp v1, v1, v1 row_shr:1 row_mask:0xf bank_mask:0xf bound_ctrl:1
	s_nop 1
	v_add_f32_dpp v1, v1, v1 row_shr:2 row_mask:0xf bank_mask:0xf bound_ctrl:1
	s_nop 1
	v_add_f32_dpp v1, v1, v1 row_shr:4 row_mask:0xf bank_mask:0xf bound_ctrl:1
	s_nop 1
	v_add_f32_dpp v1, v1, v1 row_shr:8 row_mask:0xf bank_mask:0xf bound_ctrl:1
	s_nop 1
	v_mov_b32_dpp v102, v1 row_bcast:15 row_mask:0xa bank_mask:0xf bound_ctrl:1
	v_add_f32_e32 v1, v1, v102
	v_mov_b32_e32 v102, 0
	s_nop 1
	v_mov_b32_dpp v102, v1 row_bcast:31 row_mask:0xc bank_mask:0xf bound_ctrl:1
	v_add_f32_e32 v1, v1, v102
	s_nop 0
	v_readlane_b32 s0, v1, 63
	s_nop 1
	v_fma_f32 v1, s0, v123, v118
	v_mul_f32_e32 v102, 0x4b800000, v1
	v_cmp_gt_f32_e32 vcc, s52, v1
	s_nop 1
	v_cndmask_b32_e32 v1, v1, v102, vcc
	v_rsq_f32_e32 v1, v1
	v_pk_mul_f32 v[102:103], v[10:11], v[104:105]
	v_pk_fma_f32 v[104:105], v[14:15], v[104:105], v[134:135]
	v_mul_f32_e32 v125, 0x45800000, v1
	v_cndmask_b32_e32 v130, v1, v125, vcc
	v_pk_mul_f32 v[126:127], v[126:127], v[130:131] op_sel_hi:[1,0]
	v_pk_mul_f32 v[128:129], v[128:129], v[130:131] op_sel_hi:[1,0]
	v_pk_mul_f32 v[136:137], v[136:137], v[130:131] op_sel_hi:[1,0]
	v_pk_mul_f32 v[152:153], v[152:153], v[130:131] op_sel_hi:[1,0]
	v_pk_fma_f32 v[132:133], v[96:97], v[126:127], v[100:101]
	v_pk_fma_f32 v[126:127], v[26:27], v[126:127], v[30:31]
	v_pk_fma_f32 v[134:135], v[92:93], v[128:129], v[98:99]
	v_pk_fma_f32 v[128:129], v[28:29], v[128:129], v[32:33]
	v_pk_fma_f32 v[150:151], v[88:89], v[136:137], v[94:95]
	v_pk_fma_f32 v[136:137], v[18:19], v[136:137], v[22:23]
	v_pk_fma_f32 v[154:155], v[86:87], v[152:153], v[90:91]
	v_pk_fma_f32 v[152:153], v[20:21], v[152:153], v[24:25]
	v_cvt_pk_bf16_f32 v126, v126, v127
	v_cvt_pk_bf16_f32 v127, v128, v129
	v_cvt_pk_bf16_f32 v128, v136, v137
	v_cvt_pk_bf16_f32 v129, v152, v153
	global_store_dwordx4 v[146:147], v[126:129], off
	v_pk_mul_f32 v[136:137], v[162:163], v[130:131] op_sel_hi:[1,0]
	v_mov_b32_e32 v125, 0
	v_cvt_pk_bf16_f32 v126, v132, v133
	v_cvt_pk_bf16_f32 v127, v134, v135
	v_cvt_pk_bf16_f32 v128, v150, v151
	v_cvt_pk_bf16_f32 v129, v154, v155
	global_store_dwordx4 v[148:149], v[126:129], off
	ds_write_b128 v55, v[126:129] offset:16
	v_pk_fma_f32 v[150:151], v[78:79], v[136:137], v[80:81]
	v_pk_mul_f32 v[126:127], v[156:157], v[130:131] op_sel_hi:[1,0]
	v_pk_mul_f32 v[128:129], v[160:161], v[130:131] op_sel_hi:[1,0]
	v_pk_mul_f32 v[130:131], v[164:165], v[130:131] op_sel_hi:[1,0]
	v_pk_fma_f32 v[132:133], v[102:103], v[126:127], v[104:105]
	v_pk_fma_f32 v[126:127], v[10:11], v[126:127], v[14:15]
	v_pk_fma_f32 v[134:135], v[82:83], v[128:129], v[84:85]
	v_pk_fma_f32 v[128:129], v[12:13], v[128:129], v[16:17]
	v_pk_fma_f32 v[136:137], v[2:3], v[136:137], v[6:7]
	v_pk_fma_f32 v[152:153], v[74:75], v[130:131], v[76:77]
	v_pk_fma_f32 v[130:131], v[4:5], v[130:131], v[8:9]
	v_cvt_pk_bf16_f32 v126, v126, v127
	v_cvt_pk_bf16_f32 v127, v128, v129
	v_cvt_pk_bf16_f32 v128, v136, v137
	v_cvt_pk_bf16_f32 v129, v130, v131
	global_store_dwordx4 v[146:147], v[126:129], off offset:1024
	s_waitcnt vmcnt(8)
	v_lshlrev_b32_e32 v130, 16, v140
	v_and_b32_e32 v131, 0xffff0000, v140
	v_cvt_pk_bf16_f32 v126, v132, v133
	v_cvt_pk_bf16_f32 v127, v134, v135
	v_cvt_pk_bf16_f32 v128, v150, v151
	v_cvt_pk_bf16_f32 v129, v152, v153
	global_store_dwordx4 v[148:149], v[126:129], off offset:1024
	ds_write_b128 v55, v[126:129] offset:1040
	v_lshlrev_b32_e32 v132, 16, v141
	v_lshlrev_b32_e32 v126, 16, v138
	v_and_b32_e32 v127, 0xffff0000, v138
	v_add_f32_e32 v1, 0, v126
	v_lshlrev_b32_e32 v128, 16, v139
	v_add_f32_e32 v1, v1, v127
	v_and_b32_e32 v129, 0xffff0000, v139
	v_add_f32_e32 v1, v1, v128
	v_add_f32_e32 v1, v1, v129
	v_add_f32_e32 v1, v1, v130
	v_add_f32_e32 v1, v1, v131
	v_and_b32_e32 v133, 0xffff0000, v141
	v_add_f32_e32 v1, v1, v132
	s_waitcnt vmcnt(8)
; __device__ __forceinline__ uint4 pack8(const float* v) { uint4 r; r.x = pack2(v[0], v[1]); r.y = pack2(v[2], v[3]); r.z = pack2(v[4], v[5]); r.w = pack2(v[6], v[7]); return r; }
;     ...
;         for (int q = 0; q < 4; ++q) {
;             const int rl = wave * 4 + q, row = r0 + rl;
;             float v[16];
;             up8(raw[q][0], v); up8(raw[q][1], v + 8);
;             float s = 0.f;
; #pragma unroll
;             for (int i = 0; i < 16; ++i) s += v[i];
;             const float mu = wave_sum(s) * (1.f / 1024.f);
;             float s2 = 0.f;
; #pragma unroll
;             for (int i = 0; i < 16; ++i) { const float d = v[i] - mu; s2 += d * d; }
;             const float rstd = rsqrtf(wave_sum(s2) * (1.f / 1024.f) + 1e-5f);
; #pragma unroll
;             for (int i = 0; i < 2; ++i) {
;                 const int c0 = i * 512 + lane * 8;
;                 float x[8], hf[8];
; #pragma unroll
;                 for (int j = 0; j < 8; ++j) { const float n_ = (v[i * 8 + j] - mu) * rstd; x[j] = n_ * ga[i * 8 + j] + be[i * 8 + j]; hf[j] = n_ * a2[i * 8 + j] + b2[i * 8 + j]; }
;                 *(uint4*)(X1 + (size_t)row * 1024 + c0) = pack8(x);
;                 const uint4 pk = pack8(hf);
;                 *(uint4*)(HFF + (size_t)row * 1024 + c0) = pk;
;                 *(uint4*)(hfs + rl * 1032 + c0) = pk;
;             }
;         }
	v_lshlrev_b32_e32 v134, 16, v142
	v_add_f32_e32 v1, v1, v133
	v_and_b32_e32 v135, 0xffff0000, v142
	v_add_f32_e32 v1, v1, v134
	v_lshlrev_b32_e32 v136, 16, v143
	v_add_f32_e32 v1, v1, v135
	v_and_b32_e32 v137, 0xffff0000, v143
	v_add_f32_e32 v1, v1, v136
	v_lshlrev_b32_e32 v138, 16, v144
	v_add_f32_e32 v1, v1, v137
	v_and_b32_e32 v139, 0xffff0000, v144
	v_add_f32_e32 v1, v1, v138
	v_lshlrev_b32_e32 v140, 16, v145
	v_add_f32_e32 v1, v1, v139
	v_and_b32_e32 v141, 0xffff0000, v145
	v_add_f32_e32 v1, v1, v140
	v_add_f32_e32 v1, v1, v141
	v_or_b32_e32 v142, s2, v108
	v_ashrrev_i32_e32 v143, 31, v142
	v_add_f32_dpp v1, v1, v1 row_shr:1 row_mask:0xf bank_mask:0xf bound_ctrl:1
	v_lshlrev_b64 v[142:143], 11, v[142:143]
	s_nop 0
	v_add_f32_dpp v1, v1, v1 row_shr:2 row_mask:0xf bank_mask:0xf bound_ctrl:1
	s_nop 1
	v_add_f32_dpp v1, v1, v1 row_shr:4 row_mask:0xf bank_mask:0xf bound_ctrl:1
	s_nop 1
	v_add_f32_dpp v1, v1, v1 row_shr:8 row_mask:0xf bank_mask:0xf bound_ctrl:1
	s_nop 1
	v_mov_b32_dpp v125, v1 row_bcast:15 row_mask:0xa bank_mask:0xf bound_ctrl:1
	v_add_f32_e32 v1, v1, v125
	v_mov_b32_e32 v125, 0
	s_nop 1
	v_mov_b32_dpp v125, v1 row_bcast:31 row_mask:0xc bank_mask:0xf bound_ctrl:1
	v_add_f32_e32 v1, v1, v125
	v_mov_b32_e32 v125, 0
	v_readlane_b32 s0, v1, 63
	s_nop 1
	v_mul_f32_e32 v144, s0, v123
	v_pk_add_f32 v[126:127], v[126:127], v[144:145] op_sel_hi:[1,0] neg_lo:[0,1] neg_hi:[0,1]
	v_pk_add_f32 v[128:129], v[128:129], v[144:145] op_sel_hi:[1,0] neg_lo:[0,1] neg_hi:[0,1]
	v_pk_mul_f32 v[146:147], v[126:127], v[126:127]
	v_pk_mul_f32 v[148:149], v[128:129], v[128:129]
	v_add_f32_e32 v1, v146, v147
	v_pk_add_f32 v[130:131], v[130:131], v[144:145] op_sel_hi:[1,0] neg_lo:[0,1] neg_hi:[0,1]
	v_add_f32_e32 v1, v148, v1
	v_pk_mul_f32 v[150:151], v[130:131], v[130:131]
	v_add_f32_e32 v1, v149, v1
	v_pk_add_f32 v[132:133], v[132:133], v[144:145] op_sel_hi:[1,0] neg_lo:[0,1] neg_hi:[0,1]
	v_add_f32_e32 v1, v150, v1
	v_pk_mul_f32 v[152:153], v[132:133], v[132:133]
	v_add_f32_e32 v1, v151, v1
	v_pk_add_f32 v[134:135], v[134:135], v[144:145] op_sel_hi:[1,0] neg_lo:[0,1] neg_hi:[0,1]
	v_add_f32_e32 v1, v152, v1
	v_pk_mul_f32 v[154:155], v[134:135], v[134:135]
	v_add_f32_e32 v1, v153, v1
	v_pk_add_f32 v[136:137], v[136:137], v[144:145] op_sel_hi:[1,0] neg_lo:[0,1] neg_hi:[0,1]
	v_add_f32_e32 v1, v154, v1
	v_pk_mul_f32 v[156:157], v[136:137], v[136:137]
	v_add_f32_e32 v1, v155, v1
	v_pk_add_f32 v[138:139], v[138:139], v[144:145] op_sel_hi:[1,0] neg_lo:[0,1] neg_hi:[0,1]
	v_add_f32_e32 v1, v156, v1
	v_pk_mul_f32 v[158:159], v[138:139], v[138:139]
	v_add_f32_e32 v1, v157, v1
	v_pk_add_f32 v[140:141], v[140:141], v[144:145] op_sel_hi:[1,0] neg_lo:[0,1] neg_hi:[0,1]
	v_add_f32_e32 v1, v158, v1
	v_pk_mul_f32 v[144:145], v[140:141], v[140:141]
	v_add_f32_e32 v1, v159, v1
	v_add_f32_e32 v1, v144, v1
	v_add_f32_e32 v1, v145, v1
	v_lshl_add_u64 v[144:145], v[68:69], 0, v[142:143]
	v_lshl_add_u64 v[142:143], v[70:71], 0, v[142:143]
	v_add_f32_dpp v1, v1, v1 row_shr:1 row_mask:0xf bank_mask:0xf bound_ctrl:1
	s_nop 1
	v_add_f32_dpp v1, v1, v1 row_shr:2 row_mask:0xf bank_mask:0xf bound_ctrl:1
	s_nop 1
	v_add_f32_dpp v1, v1, v1 row_shr:4 row_mask:0xf bank_mask:0xf bound_ctrl:1
	s_nop 1
	v_add_f32_dpp v1, v1, v1 row_shr:8 row_mask:0xf bank_mask:0xf bound_ctrl:1
	s_nop 1
	v_mov_b32_dpp v125, v1 row_bcast:15 row_mask:0xa bank_mask:0xf bound_ctrl:1
	v_add_f32_e32 v1, v1, v125
	v_mov_b32_e32 v125, 0
	s_nop 1
	v_mov_b32_dpp v125, v1 row_bcast:31 row_mask:0xc bank_mask:0xf bound_ctrl:1
	v_add_f32_e32 v1, v1, v125
	s_nop 0
	v_readlane_b32 s0, v1, 63
	s_nop 1
	v_fma_f32 v1, s0, v123, v118
	v_mul_f32_e32 v125, 0x4b800000, v1
	v_cmp_gt_f32_e32 vcc, s52, v1
	s_nop 1
	v_cndmask_b32_e32 v1, v1, v125, vcc
	v_rsq_f32_e32 v1, v1
	s_nop 0
	v_mul_f32_e32 v125, 0x45800000, v1
	v_cndmask_b32_e32 v146, v1, v125, vcc
	v_pk_mul_f32 v[126:127], v[126:127], v[146:147] op_sel_hi:[1,0]
	v_pk_mul_f32 v[128:129], v[128:129], v[146:147] op_sel_hi:[1,0]
	v_pk_mul_f32 v[130:131], v[130:131], v[146:147] op_sel_hi:[1,0]
	v_pk_mul_f32 v[132:133], v[132:133], v[146:147] op_sel_hi:[1,0]
	v_pk_fma_f32 v[148:149], v[96:97], v[126:127], v[100:101]
	v_pk_fma_f32 v[126:127], v[26:27], v[126:127], v[30:31]
	v_pk_fma_f32 v[150:151], v[92:93], v[128:129], v[98:99]
	v_pk_fma_f32 v[128:129], v[28:29], v[128:129], v[32:33]
	v_pk_fma_f32 v[152:153], v[88:89], v[130:131], v[94:95]
	v_pk_fma_f32 v[130:131], v[18:19], v[130:131], v[22:23]
	v_pk_fma_f32 v[154:155], v[86:87], v[132:133], v[90:91]
	v_pk_fma_f32 v[132:133], v[20:21], v[132:133], v[24:25]
	v_cvt_pk_bf16_f32 v126, v126, v127
	v_cvt_pk_bf16_f32 v127, v128, v129
	v_cvt_pk_bf16_f32 v128, v130, v131
	v_cvt_pk_bf16_f32 v129, v132, v133
	global_store_dwordx4 v[144:145], v[126:129], off
	v_mov_b32_e32 v125, 0
	s_nop 0
	v_cvt_pk_bf16_f32 v126, v148, v149
	v_cvt_pk_bf16_f32 v127, v150, v151
	v_cvt_pk_bf16_f32 v128, v152, v153
	v_cvt_pk_bf16_f32 v129, v154, v155
	global_store_dwordx4 v[142:143], v[126:129], off
	ds_write_b128 v109, v[126:129] offset:16
	s_nop 0
	v_pk_mul_f32 v[126:127], v[134:135], v[146:147] op_sel_hi:[1,0]
	v_pk_mul_f32 v[128:129], v[136:137], v[146:147] op_sel_hi:[1,0]
	v_pk_mul_f32 v[134:135], v[138:139], v[146:147] op_sel_hi:[1,0]
	v_pk_mul_f32 v[138:139], v[140:141], v[146:147] op_sel_hi:[1,0]
	v_pk_fma_f32 v[130:131], v[102:103], v[126:127], v[104:105]
	v_pk_fma_f32 v[126:127], v[10:11], v[126:127], v[14:15]
	v_pk_fma_f32 v[132:133], v[82:83], v[128:129], v[84:85]
	v_pk_fma_f32 v[128:129], v[12:13], v[128:129], v[16:17]
	v_pk_fma_f32 v[136:137], v[78:79], v[134:135], v[80:81]
	v_pk_fma_f32 v[134:135], v[2:3], v[134:135], v[6:7]
	v_pk_fma_f32 v[140:141], v[74:75], v[138:139], v[76:77]
	v_pk_fma_f32 v[138:139], v[4:5], v[138:139], v[8:9]
	v_cvt_pk_bf16_f32 v126, v126, v127
	v_cvt_pk_bf16_f32 v127, v128, v129
	v_cvt_pk_bf16_f32 v128, v134, v135
	v_cvt_pk_bf16_f32 v129, v138, v139
	global_store_dwordx4 v[144:145], v[126:129], off offset:1024
	v_or_b32_e32 v134, s2, v110
	v_ashrrev_i32_e32 v135, 31, v134
	v_cvt_pk_bf16_f32 v126, v130, v131
	v_cvt_pk_bf16_f32 v127, v132, v133
	v_cvt_pk_bf16_f32 v128, v136, v137
	v_cvt_pk_bf16_f32 v129, v140, v141
	global_store_dwordx4 v[142:143], v[126:129], off offset:1024
	ds_write_b128 v109, v[126:129] offset:1040
	s_waitcnt vmcnt(10)
; __device__ __forceinline__ uint4 pack8(const float* v) { uint4 r; r.x = pack2(v[0], v[1]); r.y = pack2(v[2], v[3]); r.z = pack2(v[4], v[5]); r.w = pack2(v[6], v[7]); return r; }
;     ...
;         for (int q = 0; q < 4; ++q) {
;             const int rl = wave * 4 + q, row = r0 + rl;
;             float v[16];
;             up8(raw[q][0], v); up8(raw[q][1], v + 8);
;             float s = 0.f;
; #pragma unroll
;             for (int i = 0; i < 16; ++i) s += v[i];
;             const float mu = wave_sum(s) * (1.f / 1024.f);
;             float s2 = 0.f;
; #pragma unroll
;             for (int i = 0; i < 16; ++i) { const float d = v[i] - mu; s2 += d * d; }
;             const float rstd = rsqrtf(wave_sum(s2) * (1.f / 1024.f) + 1e-5f);
; #pragma unroll
;             for (int i = 0; i < 2; ++i) {
;                 const int c0 = i * 512 + lane * 8;
;                 float x[8], hf[8];
; #pragma unroll
;                 for (int j = 0; j < 8; ++j) { const float n_ = (v[i * 8 + j] - mu) * rstd; x[j] = n_ * ga[i * 8 + j] + be[i * 8 + j]; hf[j] = n_ * a2[i * 8 + j] + b2[i * 8 + j]; }
;                 *(uint4*)(X1 + (size_t)row * 1024 + c0) = pack8(x);
;                 const uint4 pk = pack8(hf);
;                 *(uint4*)(HFF + (size_t)row * 1024 + c0) = pk;
;                 *(uint4*)(hfs + rl * 1032 + c0) = pk;
;             }
;         }
	v_lshlrev_b32_e32 v130, 16, v42
	v_lshlrev_b32_e32 v126, 16, v46
	v_and_b32_e32 v127, 0xffff0000, v46
	v_add_f32_e32 v1, 0, v126
	v_lshlrev_b32_e32 v46, 16, v47
	v_add_f32_e32 v1, v1, v127
	v_and_b32_e32 v47, 0xffff0000, v47
	v_add_f32_e32 v1, v1, v46
	v_lshlrev_b32_e32 v128, 16, v48
	v_add_f32_e32 v1, v1, v47
	v_and_b32_e32 v129, 0xffff0000, v48
	v_add_f32_e32 v1, v1, v128
	v_lshlrev_b32_e32 v48, 16, v49
	v_add_f32_e32 v1, v1, v129
	v_and_b32_e32 v49, 0xffff0000, v49
	v_add_f32_e32 v1, v1, v48
	v_add_f32_e32 v1, v1, v49
	v_and_b32_e32 v131, 0xffff0000, v42
	v_add_f32_e32 v1, v1, v130
	v_lshlrev_b32_e32 v42, 16, v43
	v_add_f32_e32 v1, v1, v131
	v_and_b32_e32 v43, 0xffff0000, v43
	v_add_f32_e32 v1, v1, v42
	v_lshlrev_b32_e32 v132, 16, v44
	v_add_f32_e32 v1, v1, v43
	v_and_b32_e32 v133, 0xffff0000, v44
	v_add_f32_e32 v1, v1, v132
	v_lshlrev_b32_e32 v44, 16, v45
	v_add_f32_e32 v1, v1, v133
	v_and_b32_e32 v45, 0xffff0000, v45
	v_add_f32_e32 v1, v1, v44
	v_add_f32_e32 v1, v1, v45
	s_nop 1
	v_add_f32_dpp v1, v1, v1 row_shr:1 row_mask:0xf bank_mask:0xf bound_ctrl:1
	s_nop 1
	v_add_f32_dpp v1, v1, v1 row_shr:2 row_mask:0xf bank_mask:0xf bound_ctrl:1
	s_nop 1
	v_add_f32_dpp v1, v1, v1 row_shr:4 row_mask:0xf bank_mask:0xf bound_ctrl:1
	s_nop 1
	v_add_f32_dpp v1, v1, v1 row_shr:8 row_mask:0xf bank_mask:0xf bound_ctrl:1
	s_nop 1
	v_mov_b32_dpp v125, v1 row_bcast:15 row_mask:0xa bank_mask:0xf bound_ctrl:1
	v_add_f32_e32 v1, v1, v125
	v_mov_b32_e32 v125, 0
	s_nop 1
	v_mov_b32_dpp v125, v1 row_bcast:31 row_mask:0xc bank_mask:0xf bound_ctrl:1
	v_add_f32_e32 v1, v1, v125
	v_mov_b32_e32 v125, 0
	v_readlane_b32 s0, v1, 63
	s_nop 1
	v_mul_f32_e32 v136, s0, v123
	v_pk_add_f32 v[126:127], v[126:127], v[136:137] op_sel_hi:[1,0] neg_lo:[0,1] neg_hi:[0,1]
	v_pk_add_f32 v[46:47], v[46:47], v[136:137] op_sel_hi:[1,0] neg_lo:[0,1] neg_hi:[0,1]
	v_pk_mul_f32 v[138:139], v[126:127], v[126:127]
	v_pk_mul_f32 v[140:141], v[46:47], v[46:47]
	v_add_f32_e32 v1, v138, v139
	v_pk_add_f32 v[128:129], v[128:129], v[136:137] op_sel_hi:[1,0] neg_lo:[0,1] neg_hi:[0,1]
	v_add_f32_e32 v1, v140, v1
	v_pk_mul_f32 v[142:143], v[128:129], v[128:129]
	v_add_f32_e32 v1, v141, v1
	v_pk_add_f32 v[48:49], v[48:49], v[136:137] op_sel_hi:[1,0] neg_lo:[0,1] neg_hi:[0,1]
	v_add_f32_e32 v1, v142, v1
	v_pk_mul_f32 v[144:145], v[48:49], v[48:49]
	v_add_f32_e32 v1, v143, v1
	v_pk_add_f32 v[130:131], v[130:131], v[136:137] op_sel_hi:[1,0] neg_lo:[0,1] neg_hi:[0,1]
	v_add_f32_e32 v1, v144, v1
	v_pk_mul_f32 v[146:147], v[130:131], v[130:131]
	v_add_f32_e32 v1, v145, v1
	v_pk_add_f32 v[148:149], v[42:43], v[136:137] op_sel_hi:[1,0] neg_lo:[0,1] neg_hi:[0,1]
	v_add_f32_e32 v1, v146, v1
	v_pk_mul_f32 v[42:43], v[148:149], v[148:149]
	v_add_f32_e32 v1, v147, v1
	v_pk_add_f32 v[132:133], v[132:133], v[136:137] op_sel_hi:[1,0] neg_lo:[0,1] neg_hi:[0,1]
	v_add_f32_e32 v1, v42, v1
	v_pk_mul_f32 v[150:151], v[132:133], v[132:133]
	v_add_f32_e32 v1, v43, v1
	v_pk_add_f32 v[136:137], v[44:45], v[136:137] op_sel_hi:[1,0] neg_lo:[0,1] neg_hi:[0,1]
	v_add_f32_e32 v1, v150, v1
	v_pk_mul_f32 v[44:45], v[136:137], v[136:137]
	v_add_f32_e32 v1, v151, v1
	v_add_f32_e32 v1, v44, v1
	v_add_f32_e32 v1, v45, v1
	v_mov_b32_e32 v42, 0
	s_nop 0
	v_add_f32_dpp v1, v1, v1 row_shr:1 row_mask:0xf bank_mask:0xf bound_ctrl:1
	s_nop 1
	v_add_f32_dpp v1, v1, v1 row_shr:2 row_mask:0xf bank_mask:0xf bound_ctrl:1
	s_nop 1
	v_add_f32_dpp v1, v1, v1 row_shr:4 row_mask:0xf bank_mask:0xf bound_ctrl:1
	s_nop 1
	v_add_f32_dpp v1, v1, v1 row_shr:8 row_mask:0xf bank_mask:0xf bound_ctrl:1
	s_nop 1
	v_mov_b32_dpp v42, v1 row_bcast:15 row_mask:0xa bank_mask:0xf bound_ctrl:1
	v_add_f32_e32 v1, v1, v42
	v_mov_b32_e32 v42, 0
	s_nop 1
	v_mov_b32_dpp v42, v1 row_bcast:31 row_mask:0xc bank_mask:0xf bound_ctrl:1
	v_add_f32_e32 v1, v1, v42
	s_nop 0
	v_readlane_b32 s0, v1, 63
	s_nop 1
	v_fma_f32 v1, s0, v123, v118
	v_mul_f32_e32 v42, 0x4b800000, v1
	v_cmp_gt_f32_e32 vcc, s52, v1
	s_nop 1
	v_cndmask_b32_e32 v1, v1, v42, vcc
	v_rsq_f32_e32 v1, v1
	v_lshlrev_b64 v[42:43], 11, v[134:135]
	v_lshl_add_u64 v[134:135], v[68:69], 0, v[42:43]
	v_lshl_add_u64 v[138:139], v[70:71], 0, v[42:43]
	v_mul_f32_e32 v42, 0x45800000, v1
	v_cndmask_b32_e32 v140, v1, v42, vcc
	v_pk_mul_f32 v[42:43], v[126:127], v[140:141] op_sel_hi:[1,0]
	v_pk_mul_f32 v[44:45], v[46:47], v[140:141] op_sel_hi:[1,0]
	v_pk_mul_f32 v[128:129], v[128:129], v[140:141] op_sel_hi:[1,0]
	v_pk_mul_f32 v[48:49], v[48:49], v[140:141] op_sel_hi:[1,0]
	v_pk_fma_f32 v[126:127], v[96:97], v[42:43], v[100:101]
	v_pk_fma_f32 v[42:43], v[26:27], v[42:43], v[30:31]
	v_pk_fma_f32 v[46:47], v[92:93], v[44:45], v[98:99]
	v_pk_fma_f32 v[44:45], v[28:29], v[44:45], v[32:33]
	v_pk_fma_f32 v[142:143], v[88:89], v[128:129], v[94:95]
	v_pk_fma_f32 v[128:129], v[18:19], v[128:129], v[22:23]
	v_pk_fma_f32 v[144:145], v[86:87], v[48:49], v[90:91]
	v_pk_fma_f32 v[48:49], v[20:21], v[48:49], v[24:25]
	v_cvt_pk_bf16_f32 v42, v42, v43
	v_cvt_pk_bf16_f32 v43, v44, v45
	v_cvt_pk_bf16_f32 v44, v128, v129
	v_cvt_pk_bf16_f32 v45, v48, v49
	global_store_dwordx4 v[134:135], v[42:45], off
	s_nop 1
	v_cvt_pk_bf16_f32 v42, v126, v127
	v_cvt_pk_bf16_f32 v43, v46, v47
	v_cvt_pk_bf16_f32 v44, v142, v143
	v_cvt_pk_bf16_f32 v45, v144, v145
	global_store_dwordx4 v[138:139], v[42:45], off
	ds_write_b128 v111, v[42:45] offset:16
	v_pk_mul_f32 v[126:127], v[132:133], v[140:141] op_sel_hi:[1,0]
	v_pk_mul_f32 v[42:43], v[130:131], v[140:141] op_sel_hi:[1,0]
	v_pk_mul_f32 v[44:45], v[148:149], v[140:141] op_sel_hi:[1,0]
	v_pk_mul_f32 v[130:131], v[136:137], v[140:141] op_sel_hi:[1,0]
	v_pk_fma_f32 v[46:47], v[102:103], v[42:43], v[104:105]
	v_pk_fma_f32 v[42:43], v[10:11], v[42:43], v[14:15]
	v_pk_fma_f32 v[48:49], v[82:83], v[44:45], v[84:85]
	v_pk_fma_f32 v[44:45], v[12:13], v[44:45], v[16:17]
	v_pk_fma_f32 v[128:129], v[78:79], v[126:127], v[80:81]
	v_pk_fma_f32 v[126:127], v[2:3], v[126:127], v[6:7]
	v_pk_fma_f32 v[132:133], v[74:75], v[130:131], v[76:77]
	v_pk_fma_f32 v[130:131], v[4:5], v[130:131], v[8:9]
	v_cvt_pk_bf16_f32 v42, v42, v43
	v_cvt_pk_bf16_f32 v43, v44, v45
	v_cvt_pk_bf16_f32 v44, v126, v127
	v_cvt_pk_bf16_f32 v45, v130, v131
	global_store_dwordx4 v[134:135], v[42:45], off offset:1024
	v_or_b32_e32 v126, s2, v112
	v_ashrrev_i32_e32 v127, 31, v126
	v_cvt_pk_bf16_f32 v42, v46, v47
	v_cvt_pk_bf16_f32 v43, v48, v49
	v_cvt_pk_bf16_f32 v44, v128, v129
	v_cvt_pk_bf16_f32 v45, v132, v133
	global_store_dwordx4 v[138:139], v[42:45], off offset:1024
	ds_write_b128 v111, v[42:45] offset:1040
	s_waitcnt vmcnt(12)
; __device__ __forceinline__ uint4 pack8(const float* v) { uint4 r; r.x = pack2(v[0], v[1]); r.y = pack2(v[2], v[3]); r.z = pack2(v[4], v[5]); r.w = pack2(v[6], v[7]); return r; }
;     ...
;         for (int q = 0; q < 4; ++q) {
;             const int rl = wave * 4 + q, row = r0 + rl;
;             float v[16];
;             up8(raw[q][0], v); up8(raw[q][1], v + 8);
;             float s = 0.f;
; #pragma unroll
;             for (int i = 0; i < 16; ++i) s += v[i];
;             const float mu = wave_sum(s) * (1.f / 1024.f);
;             float s2 = 0.f;
; #pragma unroll
;             for (int i = 0; i < 16; ++i) { const float d = v[i] - mu; s2 += d * d; }
;             const float rstd = rsqrtf(wave_sum(s2) * (1.f / 1024.f) + 1e-5f);
; #pragma unroll
;             for (int i = 0; i < 2; ++i) {
;                 const int c0 = i * 512 + lane * 8;
;                 float x[8], hf[8];
; #pragma unroll
;                 for (int j = 0; j < 8; ++j) { const float n_ = (v[i * 8 + j] - mu) * rstd; x[j] = n_ * ga[i * 8 + j] + be[i * 8 + j]; hf[j] = n_ * a2[i * 8 + j] + b2[i * 8 + j]; }
;                 *(uint4*)(X1 + (size_t)row * 1024 + c0) = pack8(x);
;                 const uint4 pk = pack8(hf);
;                 *(uint4*)(HFF + (size_t)row * 1024 + c0) = pk;
;                 *(uint4*)(hfs + rl * 1032 + c0) = pk;
;             }
;         }
;         __syncthreads();
;         if (probe < 3) {
;             f32x16 acc;
; #pragma unroll
;             for (int r = 0; r < 16; ++r) acc[r] = 0.f;
;             const bfr* bp = RT + ((size_t)wave * 64 + lane) * 8;
;             const bfr* ap = hfs + (lane & 31) * 1032 + (lane >> 5) * 8;
	v_lshlrev_b32_e32 v46, 16, v34
	v_lshlrev_b32_e32 v42, 16, v38
	v_and_b32_e32 v43, 0xffff0000, v38
	v_add_f32_e32 v1, 0, v42
	v_lshlrev_b32_e32 v38, 16, v39
	v_add_f32_e32 v1, v1, v43
	v_and_b32_e32 v39, 0xffff0000, v39
	v_add_f32_e32 v1, v1, v38
	v_lshlrev_b32_e32 v44, 16, v40
	v_add_f32_e32 v1, v1, v39
	v_and_b32_e32 v45, 0xffff0000, v40
	v_add_f32_e32 v1, v1, v44
	v_lshlrev_b32_e32 v40, 16, v41
	v_add_f32_e32 v1, v1, v45
	v_and_b32_e32 v41, 0xffff0000, v41
	v_add_f32_e32 v1, v1, v40
	v_add_f32_e32 v1, v1, v41
	v_and_b32_e32 v47, 0xffff0000, v34
	v_add_f32_e32 v1, v1, v46
	v_lshlrev_b32_e32 v34, 16, v35
	v_add_f32_e32 v1, v1, v47
	v_and_b32_e32 v35, 0xffff0000, v35
	v_add_f32_e32 v1, v1, v34
	v_lshlrev_b32_e32 v48, 16, v36
	v_add_f32_e32 v1, v1, v35
	v_and_b32_e32 v49, 0xffff0000, v36
	v_add_f32_e32 v1, v1, v48
	v_lshlrev_b32_e32 v36, 16, v37
	v_add_f32_e32 v1, v1, v49
	v_and_b32_e32 v37, 0xffff0000, v37
	v_add_f32_e32 v1, v1, v36
	v_add_f32_e32 v1, v1, v37
	v_lshlrev_b64 v[126:127], 11, v[126:127]
	s_nop 0
	v_add_f32_dpp v1, v1, v1 row_shr:1 row_mask:0xf bank_mask:0xf bound_ctrl:1
	s_nop 1
	v_add_f32_dpp v1, v1, v1 row_shr:2 row_mask:0xf bank_mask:0xf bound_ctrl:1
	s_nop 1
	v_add_f32_dpp v1, v1, v1 row_shr:4 row_mask:0xf bank_mask:0xf bound_ctrl:1
	s_nop 1
	v_add_f32_dpp v1, v1, v1 row_shr:8 row_mask:0xf bank_mask:0xf bound_ctrl:1
	s_nop 1
	v_mov_b32_dpp v125, v1 row_bcast:15 row_mask:0xa bank_mask:0xf bound_ctrl:1
	v_add_f32_e32 v1, v1, v125
	v_mov_b32_e32 v125, 0
	s_nop 1
	v_mov_b32_dpp v125, v1 row_bcast:31 row_mask:0xc bank_mask:0xf bound_ctrl:1
	v_add_f32_e32 v1, v1, v125
	v_mov_b32_e32 v125, 0
	v_readlane_b32 s0, v1, 63
	s_nop 1
	v_mul_f32_e32 v128, s0, v123
	v_pk_add_f32 v[42:43], v[42:43], v[128:129] op_sel_hi:[1,0] neg_lo:[0,1] neg_hi:[0,1]
	v_pk_add_f32 v[38:39], v[38:39], v[128:129] op_sel_hi:[1,0] neg_lo:[0,1] neg_hi:[0,1]
	v_pk_mul_f32 v[130:131], v[42:43], v[42:43]
	v_pk_mul_f32 v[132:133], v[38:39], v[38:39]
	v_add_f32_e32 v1, v130, v131
	v_pk_add_f32 v[44:45], v[44:45], v[128:129] op_sel_hi:[1,0] neg_lo:[0,1] neg_hi:[0,1]
	v_add_f32_e32 v1, v132, v1
	v_pk_mul_f32 v[134:135], v[44:45], v[44:45]
	v_add_f32_e32 v1, v133, v1
	v_pk_add_f32 v[40:41], v[40:41], v[128:129] op_sel_hi:[1,0] neg_lo:[0,1] neg_hi:[0,1]
	v_add_f32_e32 v1, v134, v1
	v_pk_mul_f32 v[136:137], v[40:41], v[40:41]
	v_add_f32_e32 v1, v135, v1
	v_pk_add_f32 v[46:47], v[46:47], v[128:129] op_sel_hi:[1,0] neg_lo:[0,1] neg_hi:[0,1]
	v_add_f32_e32 v1, v136, v1
	v_pk_mul_f32 v[138:139], v[46:47], v[46:47]
	v_add_f32_e32 v1, v137, v1
	v_pk_add_f32 v[34:35], v[34:35], v[128:129] op_sel_hi:[1,0] neg_lo:[0,1] neg_hi:[0,1]
	v_add_f32_e32 v1, v138, v1
	v_pk_mul_f32 v[140:141], v[34:35], v[34:35]
	v_add_f32_e32 v1, v139, v1
	v_pk_add_f32 v[48:49], v[48:49], v[128:129] op_sel_hi:[1,0] neg_lo:[0,1] neg_hi:[0,1]
	v_add_f32_e32 v1, v140, v1
	v_pk_mul_f32 v[142:143], v[48:49], v[48:49]
	v_add_f32_e32 v1, v141, v1
	v_pk_add_f32 v[36:37], v[36:37], v[128:129] op_sel_hi:[1,0] neg_lo:[0,1] neg_hi:[0,1]
	v_add_f32_e32 v1, v142, v1
	v_pk_mul_f32 v[128:129], v[36:37], v[36:37]
	v_add_f32_e32 v1, v143, v1
	v_add_f32_e32 v1, v128, v1
	v_add_f32_e32 v1, v129, v1
	v_lshl_add_u64 v[128:129], v[68:69], 0, v[126:127]
	v_lshl_add_u64 v[126:127], v[70:71], 0, v[126:127]
	v_add_f32_dpp v1, v1, v1 row_shr:1 row_mask:0xf bank_mask:0xf bound_ctrl:1
	s_nop 1
	v_add_f32_dpp v1, v1, v1 row_shr:2 row_mask:0xf bank_mask:0xf bound_ctrl:1
	s_nop 1
	v_add_f32_dpp v1, v1, v1 row_shr:4 row_mask:0xf bank_mask:0xf bound_ctrl:1
	s_nop 1
	v_add_f32_dpp v1, v1, v1 row_shr:8 row_mask:0xf bank_mask:0xf bound_ctrl:1
	s_nop 1
	v_mov_b32_dpp v125, v1 row_bcast:15 row_mask:0xa bank_mask:0xf bound_ctrl:1
	v_add_f32_e32 v1, v1, v125
	v_mov_b32_e32 v125, 0
	s_nop 1
	v_mov_b32_dpp v125, v1 row_bcast:31 row_mask:0xc bank_mask:0xf bound_ctrl:1
	v_add_f32_e32 v1, v1, v125
	s_nop 0
	v_readlane_b32 s0, v1, 63
	s_nop 1
	v_fma_f32 v1, s0, v123, v118
	v_mul_f32_e32 v125, 0x4b800000, v1
	v_cmp_gt_f32_e32 vcc, s52, v1
	s_mov_b64 s[0:1], 0
	s_nop 0
	v_cndmask_b32_e32 v1, v1, v125, vcc
	v_rsq_f32_e32 v1, v1
	s_nop 0
	v_mul_f32_e32 v125, 0x45800000, v1
	v_cndmask_b32_e32 v130, v1, v125, vcc
	v_pk_mul_f32 v[42:43], v[42:43], v[130:131] op_sel_hi:[1,0]
	v_mov_b32_e32 v1, v116
	v_pk_fma_f32 v[26:27], v[26:27], v[42:43], v[30:31]
	v_pk_mul_f32 v[30:31], v[38:39], v[130:131] op_sel_hi:[1,0]
	v_pk_fma_f32 v[96:97], v[96:97], v[42:43], v[100:101]
	v_pk_fma_f32 v[38:39], v[92:93], v[30:31], v[98:99]
	v_pk_fma_f32 v[28:29], v[28:29], v[30:31], v[32:33]
	v_pk_mul_f32 v[30:31], v[44:45], v[130:131] op_sel_hi:[1,0]
	s_nop 0
	v_pk_fma_f32 v[22:23], v[18:19], v[30:31], v[22:23]
	v_pk_mul_f32 v[18:19], v[40:41], v[130:131] op_sel_hi:[1,0]
	v_pk_fma_f32 v[32:33], v[88:89], v[30:31], v[94:95]
	v_pk_fma_f32 v[24:25], v[20:21], v[18:19], v[24:25]
	v_pk_fma_f32 v[30:31], v[86:87], v[18:19], v[90:91]
	v_cvt_pk_bf16_f32 v18, v26, v27
	v_cvt_pk_bf16_f32 v19, v28, v29
	v_cvt_pk_bf16_f32 v20, v22, v23
	v_cvt_pk_bf16_f32 v21, v24, v25
	global_store_dwordx4 v[128:129], v[18:21], off
	s_nop 1
	v_cvt_pk_bf16_f32 v18, v96, v97
	v_cvt_pk_bf16_f32 v19, v38, v39
	v_cvt_pk_bf16_f32 v20, v32, v33
	v_cvt_pk_bf16_f32 v21, v30, v31
	global_store_dwordx4 v[126:127], v[18:21], off
	ds_write_b128 v113, v[18:21] offset:16
	s_nop 0
	v_pk_mul_f32 v[18:19], v[46:47], v[130:131] op_sel_hi:[1,0]
	s_nop 0
	v_pk_fma_f32 v[10:11], v[10:11], v[18:19], v[14:15]
	v_pk_mul_f32 v[14:15], v[34:35], v[130:131] op_sel_hi:[1,0]
	v_pk_fma_f32 v[20:21], v[102:103], v[18:19], v[104:105]
	v_pk_fma_f32 v[18:19], v[82:83], v[14:15], v[84:85]
	v_pk_fma_f32 v[12:13], v[12:13], v[14:15], v[16:17]
	v_pk_mul_f32 v[14:15], v[48:49], v[130:131] op_sel_hi:[1,0]
	s_nop 0
	v_pk_fma_f32 v[6:7], v[2:3], v[14:15], v[6:7]
	v_pk_mul_f32 v[2:3], v[36:37], v[130:131] op_sel_hi:[1,0]
	v_pk_fma_f32 v[16:17], v[78:79], v[14:15], v[80:81]
	v_pk_fma_f32 v[8:9], v[4:5], v[2:3], v[8:9]
	v_pk_fma_f32 v[14:15], v[74:75], v[2:3], v[76:77]
	v_cvt_pk_bf16_f32 v2, v10, v11
	v_cvt_pk_bf16_f32 v3, v12, v13
	v_cvt_pk_bf16_f32 v4, v6, v7
	v_cvt_pk_bf16_f32 v5, v8, v9
	global_store_dwordx4 v[128:129], v[2:5], off offset:1024
	v_mov_b32_e32 v6, v51
	v_mov_b32_e32 v7, v51
	v_cvt_pk_bf16_f32 v2, v20, v21
	v_cvt_pk_bf16_f32 v3, v18, v19
	v_cvt_pk_bf16_f32 v4, v16, v17
	v_cvt_pk_bf16_f32 v5, v14, v15
	global_store_dwordx4 v[126:127], v[2:5], off offset:1024
	ds_write_b128 v113, v[2:5] offset:1040
	v_mov_b32_e32 v8, v51
	v_mov_b32_e32 v2, 0
	v_mov_b32_e32 v3, v51
	v_mov_b32_e32 v4, v51
	v_mov_b32_e32 v5, v51
	v_mov_b32_e32 v9, v51
	v_mov_b32_e32 v10, v51
	v_mov_b32_e32 v11, v51
	v_mov_b32_e32 v12, v51
	v_mov_b32_e32 v13, v51
	v_mov_b32_e32 v14, v51
	v_mov_b32_e32 v15, v51
	v_mov_b32_e32 v16, v51
	v_mov_b32_e32 v17, v51
	s_waitcnt lgkmcnt(0)
	s_barrier
;     ...
;             const bfr* bp = RT + ((size_t)wave * 64 + lane) * 8;
;             const bfr* ap = hfs + (lane & 31) * 1032 + (lane >> 5) * 8;
; #pragma unroll 8
;             for (int k = 0; k < 64; ++k) {
;                 const bf16x8 a = *(const bf16x8*)(ap + k * 16);
;                 const bf16x8 b = *(const bf16x8*)(bp + (size_t)k * 8 * 64 * 8);
;                 acc = __builtin_amdgcn_mfma_f32_32x32x16_bf16(a, b, acc, 0, 0, 0);
;             }
	v_readlane_b32 s2, v252, 21
	v_readlane_b32 s3, v252, 22
	v_lshlrev_b32_e32 v142, 4, v0
	s_add_u32 s2, s2, 0xd28000
	s_addc_u32 s3, s3, 0
	global_load_dwordx4 v[34:37], v142, s[2:3]
	s_add_u32 s2, s2, 0x2000
	s_addc_u32 s3, s3, 0
	global_load_dwordx4 v[38:41], v142, s[2:3]
	s_add_u32 s2, s2, 0x2000
	s_addc_u32 s3, s3, 0
	global_load_dwordx4 v[42:45], v142, s[2:3]
	s_add_u32 s2, s2, 0x2000
	s_addc_u32 s3, s3, 0
	global_load_dwordx4 v[46:49], v142, s[2:3]
	s_add_u32 s2, s2, 0x2000
	s_addc_u32 s3, s3, 0
	global_load_dwordx4 v[76:79], v142, s[2:3]
	s_add_u32 s2, s2, 0x2000
	s_addc_u32 s3, s3, 0
	global_load_dwordx4 v[80:83], v142, s[2:3]
	s_add_u32 s2, s2, 0x2000
	s_addc_u32 s3, s3, 0
	global_load_dwordx4 v[84:87], v142, s[2:3]
	s_add_u32 s2, s2, 0x2000
	s_addc_u32 s3, s3, 0
	global_load_dwordx4 v[88:91], v142, s[2:3]
	s_add_u32 s2, s2, 0x2000
	s_addc_u32 s3, s3, 0
	global_load_dwordx4 v[98:101], v142, s[2:3]
	s_add_u32 s2, s2, 0x2000
	s_addc_u32 s3, s3, 0
	global_load_dwordx4 v[102:105], v142, s[2:3]
	s_add_u32 s2, s2, 0x2000
	s_addc_u32 s3, s3, 0
	global_load_dwordx4 v[126:129], v142, s[2:3]
	s_add_u32 s2, s2, 0x2000
	s_addc_u32 s3, s3, 0
	global_load_dwordx4 v[130:133], v142, s[2:3]
	s_add_u32 s2, s2, 0x2000
	s_addc_u32 s3, s3, 0
	global_load_dwordx4 v[134:137], v142, s[2:3]
	s_add_u32 s2, s2, 0x2000
	s_addc_u32 s3, s3, 0
	global_load_dwordx4 v[138:141], v142, s[2:3]
	s_add_u32 s2, s2, 0x2000
	s_addc_u32 s3, s3, 0
	ds_read_b128 v[18:21], v1
	ds_read_b128 v[22:25], v1 offset:32
	ds_read_b128 v[26:29], v1 offset:64
	ds_read_b128 v[30:33], v1 offset:96
	s_waitcnt vmcnt(13) lgkmcnt(3)
	v_mfma_f32_32x32x16_bf16 v[2:17], v[18:21], v[34:37], v[2:17]
	global_load_dwordx4 v[34:37], v142, s[2:3]
	s_add_u32 s2, s2, 0x2000
	s_addc_u32 s3, s3, 0
	ds_read_b128 v[18:21], v1 offset:128
	s_waitcnt vmcnt(13) lgkmcnt(3)
	v_mfma_f32_32x32x16_bf16 v[2:17], v[22:25], v[38:41], v[2:17]
	global_load_dwordx4 v[38:41], v142, s[2:3]
	s_add_u32 s2, s2, 0x2000
	s_addc_u32 s3, s3, 0
	ds_read_b128 v[22:25], v1 offset:160
	s_waitcnt vmcnt(13) lgkmcnt(3)
	v_mfma_f32_32x32x16_bf16 v[2:17], v[26:29], v[42:45], v[2:17]
	global_load_dwordx4 v[42:45], v142, s[2:3]
	s_add_u32 s2, s2, 0x2000
	s_addc_u32 s3, s3, 0
	ds_read_b128 v[26:29], v1 offset:192
	s_waitcnt vmcnt(13) lgkmcnt(3)
	v_mfma_f32_32x32x16_bf16 v[2:17], v[30:33], v[46:49], v[2:17]
	global_load_dwordx4 v[46:49], v142, s[2:3]
	s_add_u32 s2, s2, 0x2000
	s_addc_u32 s3, s3, 0
	ds_read_b128 v[30:33], v1 offset:224
	s_waitcnt vmcnt(13) lgkmcnt(3)
	v_mfma_f32_32x32x16_bf16 v[2:17], v[18:21], v[76:79], v[2:17]
	global_load_dwordx4 v[76:79], v142, s[2:3]
	s_add_u32 s2, s2, 0x2000
	s_addc_u32 s3, s3, 0
	ds_read_b128 v[18:21], v1 offset:256
	s_waitcnt vmcnt(13) lgkmcnt(3)
	v_mfma_f32_32x32x16_bf16 v[2:17], v[22:25], v[80:83], v[2:17]
	global_load_dwordx4 v[80:83], v142, s[2:3]
	s_add_u32 s2, s2, 0x2000
	s_addc_u32 s3, s3, 0
	ds_read_b128 v[22:25], v1 offset:288
	s_waitcnt vmcnt(13) lgkmcnt(3)
	v_mfma_f32_32x32x16_bf16 v[2:17], v[26:29], v[84:87], v[2:17]
	global_load_dwordx4 v[84:87], v142, s[2:3]
	s_add_u32 s2, s2, 0x2000
	s_addc_u32 s3, s3, 0
	ds_read_b128 v[26:29], v1 offset:320
	s_waitcnt vmcnt(13) lgkmcnt(3)
	v_mfma_f32_32x32x16_bf16 v[2:17], v[30:33], v[88:91], v[2:17]
	global_load_dwordx4 v[88:91], v142, s[2:3]
	s_add_u32 s2, s2, 0x2000
	s_addc_u32 s3, s3, 0
	ds_read_b128 v[30:33], v1 offset:352
	s_waitcnt vmcnt(13) lgkmcnt(3)
	v_mfma_f32_32x32x16_bf16 v[2:17], v[18:21], v[98:101], v[2:17]
	global_load_dwordx4 v[98:101], v142, s[2:3]
	s_add_u32 s2, s2, 0x2000
	s_addc_u32 s3, s3, 0
	ds_read_b128 v[18:21], v1 offset:384
	s_waitcnt vmcnt(13) lgkmcnt(3)
	v_mfma_f32_32x32x16_bf16 v[2:17], v[22:25], v[102:105], v[2:17]
	global_load_dwordx4 v[102:105], v142, s[2:3]
	s_add_u32 s2, s2, 0x2000
	s_addc_u32 s3, s3, 0
	ds_read_b128 v[22:25], v1 offset:416
	s_waitcnt vmcnt(13) lgkmcnt(3)
	v_mfma_f32_32x32x16_bf16 v[2:17], v[26:29], v[126:129], v[2:17]
	global_load_dwordx4 v[126:129], v142, s[2:3]
	s_add_u32 s2, s2, 0x2000
	s_addc_u32 s3, s3, 0
	ds_read_b128 v[26:29], v1 offset:448
	s_waitcnt vmcnt(13) lgkmcnt(3)
	v_mfma_f32_32x32x16_bf16 v[2:17], v[30:33], v[130:133], v[2:17]
	global_load_dwordx4 v[130:133], v142, s[2:3]
	s_add_u32 s2, s2, 0x2000
	s_addc_u32 s3, s3, 0
	ds_read_b128 v[30:33], v1 offset:480
	s_waitcnt vmcnt(13) lgkmcnt(3)
	v_mfma_f32_32x32x16_bf16 v[2:17], v[18:21], v[134:137], v[2:17]
	global_load_dwordx4 v[134:137], v142, s[2:3]
	s_add_u32 s2, s2, 0x2000
	s_addc_u32 s3, s3, 0
	ds_read_b128 v[18:21], v1 offset:512
	s_waitcnt vmcnt(13) lgkmcnt(3)
	v_mfma_f32_32x32x16_bf16 v[2:17], v[22:25], v[138:141], v[2:17]
	global_load_dwordx4 v[138:141], v142, s[2:3]
	s_add_u32 s2, s2, 0x2000
	s_addc_u32 s3, s3, 0
	ds_read_b128 v[22:25], v1 offset:544
	s_waitcnt vmcnt(13) lgkmcnt(3)
	v_mfma_f32_32x32x16_bf16 v[2:17], v[26:29], v[34:37], v[2:17]
	global_load_dwordx4 v[34:37], v142, s[2:3]
	s_add_u32 s2, s2, 0x2000
	s_addc_u32 s3, s3, 0
	ds_read_b128 v[26:29], v1 offset:576
	s_waitcnt vmcnt(13) lgkmcnt(3)
	v_mfma_f32_32x32x16_bf16 v[2:17], v[30:33], v[38:41], v[2:17]
	global_load_dwordx4 v[38:41], v142, s[2:3]
	s_add_u32 s2, s2, 0x2000
	s_addc_u32 s3, s3, 0
	ds_read_b128 v[30:33], v1 offset:608
	s_waitcnt vmcnt(13) lgkmcnt(3)
	v_mfma_f32_32x32x16_bf16 v[2:17], v[18:21], v[42:45], v[2:17]
	global_load_dwordx4 v[42:45], v142, s[2:3]
	s_add_u32 s2, s2, 0x2000
	s_addc_u32 s3, s3, 0
	ds_read_b128 v[18:21], v1 offset:640
	s_waitcnt vmcnt(13) lgkmcnt(3)
	v_mfma_f32_32x32x16_bf16 v[2:17], v[22:25], v[46:49], v[2:17]
	global_load_dwordx4 v[46:49], v142, s[2:3]
	s_add_u32 s2, s2, 0x2000
	s_addc_u32 s3, s3, 0
	ds_read_b128 v[22:25], v1 offset:672
	s_waitcnt vmcnt(13) lgkmcnt(3)
;     ...
;             const bfr* bp = RT + ((size_t)wave * 64 + lane) * 8;
;             const bfr* ap = hfs + (lane & 31) * 1032 + (lane >> 5) * 8;
; #pragma unroll 8
;             for (int k = 0; k < 64; ++k) {
;                 const bf16x8 a = *(const bf16x8*)(ap + k * 16);
;                 const bf16x8 b = *(const bf16x8*)(bp + (size_t)k * 8 * 64 * 8);
;                 acc = __builtin_amdgcn_mfma_f32_32x32x16_bf16(a, b, acc, 0, 0, 0);
;             }
	v_mfma_f32_32x32x16_bf16 v[2:17], v[26:29], v[76:79], v[2:17]
	global_load_dwordx4 v[76:79], v142, s[2:3]
	s_add_u32 s2, s2, 0x2000
	s_addc_u32 s3, s3, 0
	ds_read_b128 v[26:29], v1 offset:704
	s_waitcnt vmcnt(13) lgkmcnt(3)
	v_mfma_f32_32x32x16_bf16 v[2:17], v[30:33], v[80:83], v[2:17]
	global_load_dwordx4 v[80:83], v142, s[2:3]
	s_add_u32 s2, s2, 0x2000
	s_addc_u32 s3, s3, 0
	ds_read_b128 v[30:33], v1 offset:736
	s_waitcnt vmcnt(13) lgkmcnt(3)
	v_mfma_f32_32x32x16_bf16 v[2:17], v[18:21], v[84:87], v[2:17]
	global_load_dwordx4 v[84:87], v142, s[2:3]
	s_add_u32 s2, s2, 0x2000
	s_addc_u32 s3, s3, 0
	ds_read_b128 v[18:21], v1 offset:768
	s_waitcnt vmcnt(13) lgkmcnt(3)
	v_mfma_f32_32x32x16_bf16 v[2:17], v[22:25], v[88:91], v[2:17]
	global_load_dwordx4 v[88:91], v142, s[2:3]
	s_add_u32 s2, s2, 0x2000
	s_addc_u32 s3, s3, 0
	ds_read_b128 v[22:25], v1 offset:800
	s_waitcnt vmcnt(13) lgkmcnt(3)
	v_mfma_f32_32x32x16_bf16 v[2:17], v[26:29], v[98:101], v[2:17]
	global_load_dwordx4 v[98:101], v142, s[2:3]
	s_add_u32 s2, s2, 0x2000
	s_addc_u32 s3, s3, 0
	ds_read_b128 v[26:29], v1 offset:832
	s_waitcnt vmcnt(13) lgkmcnt(3)
	v_mfma_f32_32x32x16_bf16 v[2:17], v[30:33], v[102:105], v[2:17]
	global_load_dwordx4 v[102:105], v142, s[2:3]
	s_add_u32 s2, s2, 0x2000
	s_addc_u32 s3, s3, 0
	ds_read_b128 v[30:33], v1 offset:864
	s_waitcnt vmcnt(13) lgkmcnt(3)
	v_mfma_f32_32x32x16_bf16 v[2:17], v[18:21], v[126:129], v[2:17]
	global_load_dwordx4 v[126:129], v142, s[2:3]
	s_add_u32 s2, s2, 0x2000
	s_addc_u32 s3, s3, 0
	ds_read_b128 v[18:21], v1 offset:896
	s_waitcnt vmcnt(13) lgkmcnt(3)
	v_mfma_f32_32x32x16_bf16 v[2:17], v[22:25], v[130:133], v[2:17]
	global_load_dwordx4 v[130:133], v142, s[2:3]
	s_add_u32 s2, s2, 0x2000
	s_addc_u32 s3, s3, 0
	ds_read_b128 v[22:25], v1 offset:928
	s_waitcnt vmcnt(13) lgkmcnt(3)
	v_mfma_f32_32x32x16_bf16 v[2:17], v[26:29], v[134:137], v[2:17]
	global_load_dwordx4 v[134:137], v142, s[2:3]
	s_add_u32 s2, s2, 0x2000
	s_addc_u32 s3, s3, 0
	ds_read_b128 v[26:29], v1 offset:960
	s_waitcnt vmcnt(13) lgkmcnt(3)
	v_mfma_f32_32x32x16_bf16 v[2:17], v[30:33], v[138:141], v[2:17]
	global_load_dwordx4 v[138:141], v142, s[2:3]
	s_add_u32 s2, s2, 0x2000
	s_addc_u32 s3, s3, 0
	ds_read_b128 v[30:33], v1 offset:992
	s_waitcnt vmcnt(13) lgkmcnt(3)
	v_mfma_f32_32x32x16_bf16 v[2:17], v[18:21], v[34:37], v[2:17]
	global_load_dwordx4 v[34:37], v142, s[2:3]
	s_add_u32 s2, s2, 0x2000
	s_addc_u32 s3, s3, 0
	ds_read_b128 v[18:21], v1 offset:1024
	s_waitcnt vmcnt(13) lgkmcnt(3)
	v_mfma_f32_32x32x16_bf16 v[2:17], v[22:25], v[38:41], v[2:17]
	global_load_dwordx4 v[38:41], v142, s[2:3]
	s_add_u32 s2, s2, 0x2000
	s_addc_u32 s3, s3, 0
	ds_read_b128 v[22:25], v1 offset:1056
	s_waitcnt vmcnt(13) lgkmcnt(3)
	v_mfma_f32_32x32x16_bf16 v[2:17], v[26:29], v[42:45], v[2:17]
	global_load_dwordx4 v[42:45], v142, s[2:3]
	s_add_u32 s2, s2, 0x2000
	s_addc_u32 s3, s3, 0
	ds_read_b128 v[26:29], v1 offset:1088
	s_waitcnt vmcnt(13) lgkmcnt(3)
	v_mfma_f32_32x32x16_bf16 v[2:17], v[30:33], v[46:49], v[2:17]
	global_load_dwordx4 v[46:49], v142, s[2:3]
	s_add_u32 s2, s2, 0x2000
	s_addc_u32 s3, s3, 0
	ds_read_b128 v[30:33], v1 offset:1120
	s_waitcnt vmcnt(13) lgkmcnt(3)
	v_mfma_f32_32x32x16_bf16 v[2:17], v[18:21], v[76:79], v[2:17]
	global_load_dwordx4 v[76:79], v142, s[2:3]
	s_add_u32 s2, s2, 0x2000
	s_addc_u32 s3, s3, 0
	ds_read_b128 v[18:21], v1 offset:1152
	s_waitcnt vmcnt(13) lgkmcnt(3)
	v_mfma_f32_32x32x16_bf16 v[2:17], v[22:25], v[80:83], v[2:17]
	global_load_dwordx4 v[80:83], v142, s[2:3]
	s_add_u32 s2, s2, 0x2000
	s_addc_u32 s3, s3, 0
	ds_read_b128 v[22:25], v1 offset:1184
	s_waitcnt vmcnt(13) lgkmcnt(3)
	v_mfma_f32_32x32x16_bf16 v[2:17], v[26:29], v[84:87], v[2:17]
	global_load_dwordx4 v[84:87], v142, s[2:3]
	s_add_u32 s2, s2, 0x2000
	s_addc_u32 s3, s3, 0
	ds_read_b128 v[26:29], v1 offset:1216
	s_waitcnt vmcnt(13) lgkmcnt(3)
	v_mfma_f32_32x32x16_bf16 v[2:17], v[30:33], v[88:91], v[2:17]
	global_load_dwordx4 v[88:91], v142, s[2:3]
	s_add_u32 s2, s2, 0x2000
	s_addc_u32 s3, s3, 0
	ds_read_b128 v[30:33], v1 offset:1248
	s_waitcnt vmcnt(13) lgkmcnt(3)
	v_mfma_f32_32x32x16_bf16 v[2:17], v[18:21], v[98:101], v[2:17]
	global_load_dwordx4 v[98:101], v142, s[2:3]
	s_add_u32 s2, s2, 0x2000
	s_addc_u32 s3, s3, 0
	ds_read_b128 v[18:21], v1 offset:1280
	s_waitcnt vmcnt(13) lgkmcnt(3)
	v_mfma_f32_32x32x16_bf16 v[2:17], v[22:25], v[102:105], v[2:17]
	global_load_dwordx4 v[102:105], v142, s[2:3]
	s_add_u32 s2, s2, 0x2000
	s_addc_u32 s3, s3, 0
	ds_read_b128 v[22:25], v1 offset:1312
	s_waitcnt vmcnt(13) lgkmcnt(3)
	v_mfma_f32_32x32x16_bf16 v[2:17], v[26:29], v[126:129], v[2:17]
	global_load_dwordx4 v[126:129], v142, s[2:3]
	s_add_u32 s2, s2, 0x2000
	s_addc_u32 s3, s3, 0
	ds_read_b128 v[26:29], v1 offset:1344
	s_waitcnt vmcnt(13) lgkmcnt(3)
	v_mfma_f32_32x32x16_bf16 v[2:17], v[30:33], v[130:133], v[2:17]
	global_load_dwordx4 v[130:133], v142, s[2:3]
	s_add_u32 s2, s2, 0x2000
	s_addc_u32 s3, s3, 0
	ds_read_b128 v[30:33], v1 offset:1376
	s_waitcnt vmcnt(13) lgkmcnt(3)
	v_mfma_f32_32x32x16_bf16 v[2:17], v[18:21], v[134:137], v[2:17]
	global_load_dwordx4 v[134:137], v142, s[2:3]
	s_add_u32 s2, s2, 0x2000
	s_addc_u32 s3, s3, 0
	ds_read_b128 v[18:21], v1 offset:1408
	s_waitcnt vmcnt(13) lgkmcnt(3)
; __device__ __forceinline__ float sigmoidf_(float x) { return __builtin_amdgcn_rcpf(1.f + __expf(-x)); }
;     ...
;             for (int k = 0; k < 64; ++k) {
;                 const bf16x8 a = *(const bf16x8*)(ap + k * 16);
;                 const bf16x8 b = *(const bf16x8*)(bp + (size_t)k * 8 * 64 * 8);
;                 acc = __builtin_amdgcn_mfma_f32_32x32x16_bf16(a, b, acc, 0, 0, 0);
;             }
; #pragma unroll
;             for (int r = 0; r < 16; ++r) {
;                 const int row = (r & 3) + 8 * (r >> 2) + 4 * (lane >> 5);
;                 lgt[row * 257 + wave * 32 + (lane & 31)] = acc[r];
;             }
;         }
;         __syncthreads();
;         float rb[4];
; #pragma unroll
;         for (int j = 0; j < 4; ++j) rb[j] = rbias[lane * 4 + j];
;         int selE[4]; float selG[4];
;         if (probe < 2) {
; #pragma unroll
;         for (int q = 0; q < 4; ++q) {
;             const int rl = wave * 4 + q;
;             float b[4];
; #pragma unroll
;             for (int j = 0; j < 4; ++j) b[j] = sigmoidf_(lgt[rl * 257 + lane * 4 + j]) + rb[j];
;             float m1 = -1e30f, m2 = -1e30f;
; #pragma unroll
;             for (int j = 0; j < 4; ++j) { const float v = b[j]; if (v > m1) { m2 = m1; m1 = v; } else if (v > m2) m2 = v; }
	v_mfma_f32_32x32x16_bf16 v[2:17], v[22:25], v[138:141], v[2:17]
	global_load_dwordx4 v[138:141], v142, s[2:3]
	s_add_u32 s2, s2, 0x2000
	s_addc_u32 s3, s3, 0
	ds_read_b128 v[22:25], v1 offset:1440
	s_waitcnt vmcnt(13) lgkmcnt(3)
	v_mfma_f32_32x32x16_bf16 v[2:17], v[26:29], v[34:37], v[2:17]
	global_load_dwordx4 v[34:37], v142, s[2:3]
	s_add_u32 s2, s2, 0x2000
	s_addc_u32 s3, s3, 0
	ds_read_b128 v[26:29], v1 offset:1472
	s_waitcnt vmcnt(13) lgkmcnt(3)
	v_mfma_f32_32x32x16_bf16 v[2:17], v[30:33], v[38:41], v[2:17]
	global_load_dwordx4 v[38:41], v142, s[2:3]
	s_add_u32 s2, s2, 0x2000
	s_addc_u32 s3, s3, 0
	ds_read_b128 v[30:33], v1 offset:1504
	s_waitcnt vmcnt(13) lgkmcnt(3)
	v_mfma_f32_32x32x16_bf16 v[2:17], v[18:21], v[42:45], v[2:17]
	global_load_dwordx4 v[42:45], v142, s[2:3]
	s_add_u32 s2, s2, 0x2000
	s_addc_u32 s3, s3, 0
	ds_read_b128 v[18:21], v1 offset:1536
	s_waitcnt vmcnt(13) lgkmcnt(3)
	v_mfma_f32_32x32x16_bf16 v[2:17], v[22:25], v[46:49], v[2:17]
	global_load_dwordx4 v[46:49], v142, s[2:3]
	s_add_u32 s2, s2, 0x2000
	s_addc_u32 s3, s3, 0
	ds_read_b128 v[22:25], v1 offset:1568
	s_waitcnt vmcnt(13) lgkmcnt(3)
	v_mfma_f32_32x32x16_bf16 v[2:17], v[26:29], v[76:79], v[2:17]
	global_load_dwordx4 v[76:79], v142, s[2:3]
	s_add_u32 s2, s2, 0x2000
	s_addc_u32 s3, s3, 0
	ds_read_b128 v[26:29], v1 offset:1600
	s_waitcnt vmcnt(13) lgkmcnt(3)
	v_mfma_f32_32x32x16_bf16 v[2:17], v[30:33], v[80:83], v[2:17]
	global_load_dwordx4 v[80:83], v142, s[2:3]
	s_add_u32 s2, s2, 0x2000
	s_addc_u32 s3, s3, 0
	ds_read_b128 v[30:33], v1 offset:1632
	s_waitcnt vmcnt(13) lgkmcnt(3)
	v_mfma_f32_32x32x16_bf16 v[2:17], v[18:21], v[84:87], v[2:17]
	global_load_dwordx4 v[84:87], v142, s[2:3]
	s_add_u32 s2, s2, 0x2000
	s_addc_u32 s3, s3, 0
	ds_read_b128 v[18:21], v1 offset:1664
	s_waitcnt vmcnt(13) lgkmcnt(3)
	v_mfma_f32_32x32x16_bf16 v[2:17], v[22:25], v[88:91], v[2:17]
	global_load_dwordx4 v[88:91], v142, s[2:3]
	ds_read_b128 v[22:25], v1 offset:1696
	s_waitcnt vmcnt(13) lgkmcnt(3)
	v_mfma_f32_32x32x16_bf16 v[2:17], v[26:29], v[98:101], v[2:17]
	ds_read_b128 v[26:29], v1 offset:1728
	s_waitcnt vmcnt(12) lgkmcnt(3)
	v_mfma_f32_32x32x16_bf16 v[2:17], v[30:33], v[102:105], v[2:17]
	ds_read_b128 v[30:33], v1 offset:1760
	s_waitcnt vmcnt(11) lgkmcnt(3)
	v_mfma_f32_32x32x16_bf16 v[2:17], v[18:21], v[126:129], v[2:17]
	ds_read_b128 v[18:21], v1 offset:1792
	s_waitcnt vmcnt(10) lgkmcnt(3)
	v_mfma_f32_32x32x16_bf16 v[2:17], v[22:25], v[130:133], v[2:17]
	ds_read_b128 v[22:25], v1 offset:1824
	s_waitcnt vmcnt(9) lgkmcnt(3)
	v_mfma_f32_32x32x16_bf16 v[2:17], v[26:29], v[134:137], v[2:17]
	ds_read_b128 v[26:29], v1 offset:1856
	s_waitcnt vmcnt(8) lgkmcnt(3)
	v_mfma_f32_32x32x16_bf16 v[2:17], v[30:33], v[138:141], v[2:17]
	ds_read_b128 v[30:33], v1 offset:1888
	s_waitcnt vmcnt(7) lgkmcnt(3)
	v_mfma_f32_32x32x16_bf16 v[2:17], v[18:21], v[34:37], v[2:17]
	ds_read_b128 v[18:21], v1 offset:1920
	s_waitcnt vmcnt(6) lgkmcnt(3)
	v_mfma_f32_32x32x16_bf16 v[2:17], v[22:25], v[38:41], v[2:17]
	ds_read_b128 v[22:25], v1 offset:1952
	s_waitcnt vmcnt(5) lgkmcnt(3)
	v_mfma_f32_32x32x16_bf16 v[2:17], v[26:29], v[42:45], v[2:17]
	ds_read_b128 v[26:29], v1 offset:1984
	s_waitcnt vmcnt(4) lgkmcnt(3)
	v_mfma_f32_32x32x16_bf16 v[2:17], v[30:33], v[46:49], v[2:17]
	ds_read_b128 v[30:33], v1 offset:2016
	s_waitcnt vmcnt(3) lgkmcnt(3)
	v_mfma_f32_32x32x16_bf16 v[2:17], v[18:21], v[76:79], v[2:17]
	s_waitcnt vmcnt(2) lgkmcnt(2)
	v_mfma_f32_32x32x16_bf16 v[2:17], v[22:25], v[80:83], v[2:17]
	s_waitcnt vmcnt(1) lgkmcnt(1)
	v_mfma_f32_32x32x16_bf16 v[2:17], v[26:29], v[84:87], v[2:17]
	s_waitcnt vmcnt(0) lgkmcnt(0)
	v_mfma_f32_32x32x16_bf16 v[2:17], v[30:33], v[88:91], v[2:17]
	s_nop 1
	s_nop 10
	ds_write_b32 v119, v2
	ds_write_b32 v119, v3 offset:1028
	ds_write_b32 v119, v4 offset:2056
	ds_write_b32 v119, v5 offset:3084
	ds_write_b32 v119, v6 offset:8224
	ds_write_b32 v119, v7 offset:9252
	ds_write_b32 v119, v8 offset:10280
	ds_write_b32 v119, v9 offset:11308
	ds_write_b32 v119, v10 offset:16448
	ds_write_b32 v119, v11 offset:17476
	ds_write_b32 v119, v12 offset:18504
	ds_write_b32 v119, v13 offset:19532
	ds_write_b32 v119, v14 offset:24672
	ds_write_b32 v119, v15 offset:25700
	ds_write_b32 v119, v16 offset:26728
	ds_write_b32 v119, v17 offset:27756
	s_waitcnt lgkmcnt(0)
	s_barrier
	global_load_dwordx4 v[2:5], v[66:67], off offset:1024
	ds_read_b128 v[6:9], v120
	s_waitcnt lgkmcnt(0)
	v_mul_f32_e32 v1, 0xbfb8aa3b, v6
	v_mul_f32_e32 v6, 0xbfb8aa3b, v7
	v_exp_f32_e32 v1, v1
	v_exp_f32_e32 v6, v6
	v_add_f32_e32 v1, 1.0, v1
	v_add_f32_e32 v7, 1.0, v6
	v_rcp_f32_e32 v6, v1
	v_rcp_f32_e32 v7, v7
	s_waitcnt vmcnt(0)
	v_pk_add_f32 v[10:11], v[2:3], v[6:7]
	s_nop 0
	v_max_f32_e32 v6, 0xf149f2ca, v10
	v_cmp_ngt_f32_e32 vcc, v11, v6
	v_mov_b32_e32 v1, v6
	v_mov_b32_e32 v12, v11
	s_and_saveexec_b64 s[0:1], vcc
	s_cbranch_execz .LBB0_2192
	v_mov_b32_e32 v1, 0xf149f2ca
	v_cmp_gt_f32_e32 vcc, v11, v1
	s_and_saveexec_b64 s[2:3], vcc
	v_mov_b32_e32 v1, v11
	s_or_b64 exec, exec, s[2:3]
	v_mov_b32_e32 v12, v6

; __global__ void __launch_bounds__(NTHR, 2) fwd_kernel(Params P) {
;     extern __shared__ __attribute__((aligned(16))) unsigned char lds[];
	.amdhsa_kernel _Z10fwd_kernel6Params
		.amdhsa_group_segment_fixed_size 0
		.amdhsa_private_segment_fixed_size 0
		.amdhsa_kernarg_size 632
		.amdhsa_user_sgpr_count 2
		.amdhsa_user_sgpr_dispatch_ptr 0
		.amdhsa_user_sgpr_queue_ptr 0
		.amdhsa_user_sgpr_kernarg_segment_ptr 1
		.amdhsa_user_sgpr_dispatch_id 0
		.amdhsa_user_sgpr_kernarg_preload_length 0
		.amdhsa_user_sgpr_kernarg_preload_offset 0
		.amdhsa_user_sgpr_private_segment_size 0
		.amdhsa_uses_dynamic_stack 0
		.amdhsa_enable_private_segment 0
		.amdhsa_system_sgpr_workgroup_id_x 1
		.amdhsa_system_sgpr_workgroup_id_y 0
		.amdhsa_system_sgpr_workgroup_id_z 0
		.amdhsa_system_sgpr_workgroup_info 0
		.amdhsa_system_vgpr_workitem_id 0
		.amdhsa_next_free_vgpr 254
		.amdhsa_next_free_sgpr 102
		.amdhsa_accum_offset 256
		.amdhsa_reserve_vcc 1
		.amdhsa_float_round_mode_32 0
		.amdhsa_float_round_mode_16_64 0
		.amdhsa_float_denorm_mode_32 3
		.amdhsa_float_denorm_mode_16_64 3
		.amdhsa_dx10_clamp 1
		.amdhsa_ieee_mode 1
		.amdhsa_fp16_overflow 0
		.amdhsa_tg_split 0
		.amdhsa_exception_fp_ieee_invalid_op 0
		.amdhsa_exception_fp_denorm_src 0
		.amdhsa_exception_fp_ieee_div_zero 0
		.amdhsa_exception_fp_ieee_overflow 0
		.amdhsa_exception_fp_ieee_underflow 0
		.amdhsa_exception_fp_ieee_inexact 0
		.amdhsa_exception_int_div_zero 0
	.end_amdhsa_kernel

; __global__ void __launch_bounds__(NTHR, 2) fwd_kernel(Params P) {
;     extern __shared__ __attribute__((aligned(16))) unsigned char lds[];
amdhsa.kernels:
  - .agpr_count:     0
    .args:
      - .offset:         0
        .size:           376
        .value_kind:     by_value
      - .offset:         376
        .size:           4
        .value_kind:     hidden_block_count_x
      - .offset:         380
        .size:           4
        .value_kind:     hidden_block_count_y
      - .offset:         384
        .size:           4
        .value_kind:     hidden_block_count_z
      - .offset:         388
        .size:           2
        .value_kind:     hidden_group_size_x
      - .offset:         390
        .size:           2
        .value_kind:     hidden_group_size_y
      - .offset:         392
        .size:           2
        .value_kind:     hidden_group_size_z
      - .offset:         394
        .size:           2
        .value_kind:     hidden_remainder_x
      - .offset:         396
        .size:           2
        .value_kind:     hidden_remainder_y
      - .offset:         398
        .size:           2
        .value_kind:     hidden_remainder_z
      - .offset:         416
        .size:           8
        .value_kind:     hidden_global_offset_x
      - .offset:         424
        .size:           8
        .value_kind:     hidden_global_offset_y
      - .offset:         432
        .size:           8
        .value_kind:     hidden_global_offset_z
      - .offset:         440
        .size:           2
        .value_kind:     hidden_grid_dims
      - .offset:         496
        .size:           4
        .value_kind:     hidden_dynamic_lds_size
    .group_segment_fixed_size: 0
    .kernarg_segment_align: 8
    .kernarg_segment_size: 632
    .language:       OpenCL C
    .language_version:
      - 2
      - 0
    .max_flat_workgroup_size: 512
    .name:           _Z10fwd_kernel6Params
    .private_segment_fixed_size: 0
    .sgpr_count:     108
    .sgpr_spill_count: 102
    .symbol:         _Z10fwd_kernel6Params.kd
    .uniform_work_group_size: 1
    .uses_dynamic_stack: false
    .vgpr_count:     254
    .vgpr_spill_count: 0
    .wavefront_size: 64
